# DSA indexer v2: k_idx tiles staged through LDS by LDS-DMA in 8-tile chunks shared by the 8 waves
# speedup vs baseline: 1.0131x; 1.0022x over previous
.LBB0_939:
	s_getreg_b32 s0, hwreg(HW_REG_HW_ID, 0, 6)
	s_and_b32 s0, s0, 63
	s_lshl_b32 s0, s0, 2
	s_or_b32 s0, s0, 0x20400
	v_mov_b32_e32 v0, s0
	ds_read_b32 v2, v0
	v_mbcnt_lo_u32_b32 v0, -1, 0
	v_mbcnt_hi_u32_b32 v0, -1, v0
	s_waitcnt lgkmcnt(0)
	v_readfirstlane_b32 s0, v2
	s_nop 1
	v_lshl_or_b32 v2, s0, 6, v0
	s_nop 0
	v_readfirstlane_b32 s0, v2
	s_ashr_i32 s0, s0, 6
	s_add_i32 s81, s0, s4
	s_movk_i32 s0, 0xb0
	s_cmpk_gt_i32 s81, 0xfff
	s_cbranch_scc1 .LBB0_938
	v_writelane_b32 v255, s3, 45
	v_readlane_b32 s2, v254, 0
	v_readlane_b32 s3, v254, 1
	s_load_dwordx2 s[0:1], s[2:3], s0 offset:0x0
	s_sub_i32 s44, s81, s4
	v_and_b32_e32 v50, 31, v0
	v_lshrrev_b32_e32 v51, 5, v0
	v_bfe_u32 v52, v0, 2, 1
	v_and_b32_e32 v53, 3, v0
	v_lshrrev_b32_e32 v54, 1, v0
	v_and_or_b32 v53, v54, 12, v53
	v_mov_b32_e32 v54, 0x2200
	v_mul_u32_u24_e32 v55, v52, v54
	v_lshl_add_u32 v55, v53, 7, v55
	v_lshl_add_u32 v55, v51, 4, v55
	v_add_u32_e32 v55, 0x1800, v55
	v_mul_u32_u24_e32 v56, v51, v54
	v_add_u32_e32 v56, 0x2080, v56
	v_lshlrev_b32_e32 v57, 4, v0
	v_lshlrev_b32_e32 v58, 2, v0
	v_mov_b32_e32 v61, 0xff800000
	s_lshl_b32 s30, s44, 12
	s_add_i32 s31, s30, 0x8000
	s_waitcnt lgkmcnt(0)
	s_add_u32 s4, s0, 0x3a600000
	s_addc_u32 s5, s1, 0
	s_add_u32 s6, s0, 0x4e100000
	s_addc_u32 s7, s1, 0
	s_add_u32 s6, s6, s30
	s_addc_u32 s7, s7, 0
	s_add_u32 s8, s0, 0x4be00000
	s_addc_u32 s9, s1, 0
	s_mov_b32 s10, 0
.Lidx_id:
	s_and_b32 s11, s81, 0x3ff
	s_lshr_b32 s12, s81, 10
	s_sub_i32 s13, 0x3ff, s11
	s_bitcmp1_b32 s10, 0
	s_cselect_b32 s11, s13, s11
	s_sub_i32 s26, s81, s44
	s_and_b32 s26, s26, 0x3ff
	s_add_i32 s27, s26, 7
	s_sub_i32 s28, 0x3ff, s26
	s_bitcmp1_b32 s10, 0
	s_cselect_b32 s27, s28, s27
	s_lshl_b32 s27, s27, 1
	s_add_i32 s27, s27, 1
	s_lshr_b32 s27, s27, 5
	s_add_i32 s27, s27, 8
	s_lshr_b32 s29, s27, 3
	s_lshl_b32 s13, s11, 1
	s_lshl_b32 s14, s12, 11
	s_or_b32 s14, s14, s13
	s_add_i32 s15, s13, 1
	s_lshr_b32 s15, s15, 5
	s_add_i32 s15, s15, 1
	s_add_i32 s16, s15, 7
	s_lshr_b32 s16, s16, 3
	s_mul_i32 s17, s14, 0x2200
	s_mul_hi_u32 s25, s14, 0x2200
	s_add_u32 s18, s4, s17
	s_addc_u32 s19, s5, s25
	s_lshl_b32 s17, s12, 18
	s_add_u32 s20, s6, s17
	s_addc_u32 s21, s7, 0
	s_lshl_b32 s17, s14, 8
	s_add_u32 s22, s8, s17
	s_addc_u32 s23, s9, 0
	global_load_dwordx4 v[128:131], v55, s[18:19]
	global_load_dwordx4 v[132:135], v55, s[18:19] offset:32
	global_load_dwordx4 v[136:139], v55, s[18:19] offset:64
	global_load_dwordx4 v[140:143], v55, s[18:19] offset:96
	global_load_dwordx4 v[192:195], v56, s[18:19]
	global_load_dwordx4 v[196:199], v56, s[18:19] offset:16
	s_barrier
	s_mov_b32 m0, s30
	s_nop 0
	global_load_lds_dwordx4 v57, s[20:21]
	global_load_lds_dwordx4 v57, s[20:21] offset:1024
	global_load_lds_dwordx4 v57, s[20:21] offset:2048
	global_load_lds_dwordx4 v57, s[20:21] offset:3072
	s_add_u32 s20, s20, 0x8000
	s_addc_u32 s21, s21, 0
	v_sub_u32_e32 v59, v51, v50
	v_add_u32_e32 v59, s13, v59
	v_mov_b32_e32 v60, 0x7fffff
	v_mov_b32_e32 v64, v60
	v_mov_b32_e32 v65, v60
	v_mov_b32_e32 v66, v60
	v_mov_b32_e32 v67, v60
	v_mov_b32_e32 v68, v60
	v_mov_b32_e32 v69, v60
	v_mov_b32_e32 v70, v60
	v_mov_b32_e32 v71, v60
	v_mov_b32_e32 v72, v60
	v_mov_b32_e32 v73, v60
	v_mov_b32_e32 v74, v60
	v_mov_b32_e32 v75, v60
	v_mov_b32_e32 v76, v60
	v_mov_b32_e32 v77, v60
	v_mov_b32_e32 v78, v60
	v_mov_b32_e32 v79, v60
	v_mov_b32_e32 v80, v60
	v_mov_b32_e32 v81, v60
	v_mov_b32_e32 v82, v60
	v_mov_b32_e32 v83, v60
	v_mov_b32_e32 v84, v60
	v_mov_b32_e32 v85, v60
	v_mov_b32_e32 v86, v60
	v_mov_b32_e32 v87, v60
	v_mov_b32_e32 v88, v60
	v_mov_b32_e32 v89, v60
	v_mov_b32_e32 v90, v60
	v_mov_b32_e32 v91, v60
	v_mov_b32_e32 v92, v60
	v_mov_b32_e32 v93, v60
	v_mov_b32_e32 v94, v60
	v_mov_b32_e32 v95, v60
	v_mov_b32_e32 v96, v60
	v_mov_b32_e32 v97, v60
	v_mov_b32_e32 v98, v60
	v_mov_b32_e32 v99, v60
	v_mov_b32_e32 v100, v60
	v_mov_b32_e32 v101, v60
	v_mov_b32_e32 v102, v60
	v_mov_b32_e32 v103, v60
	v_mov_b32_e32 v104, v60
	v_mov_b32_e32 v105, v60
	v_mov_b32_e32 v106, v60
	v_mov_b32_e32 v107, v60
	v_mov_b32_e32 v108, v60
	v_mov_b32_e32 v109, v60
	v_mov_b32_e32 v110, v60
	v_mov_b32_e32 v111, v60
	v_mov_b32_e32 v112, v60
	v_mov_b32_e32 v113, v60
	v_mov_b32_e32 v114, v60
	v_mov_b32_e32 v115, v60
	v_mov_b32_e32 v116, v60
	v_mov_b32_e32 v117, v60
	v_mov_b32_e32 v118, v60
	v_mov_b32_e32 v119, v60
	v_mov_b32_e32 v120, v60
	v_mov_b32_e32 v121, v60
	v_mov_b32_e32 v122, v60
	v_mov_b32_e32 v123, v60
	v_mov_b32_e32 v124, v60
	v_mov_b32_e32 v125, v60
	v_mov_b32_e32 v126, v60
	v_mov_b32_e32 v127, v60
	s_waitcnt vmcnt(4)
	v_lshlrev_b32_e32 v204, 16, v192
	v_and_b32_e32 v208, 0xffff0000, v192
	v_mul_f32_e32 v144, 0x3d000000, v204
	v_mul_f32_e32 v145, 0x3d000000, v208
	v_lshlrev_b32_e32 v204, 16, v193
	v_and_b32_e32 v208, 0xffff0000, v193
	v_mul_f32_e32 v146, 0x3d000000, v204
	v_mul_f32_e32 v147, 0x3d000000, v208
	v_lshlrev_b32_e32 v204, 16, v194
	v_and_b32_e32 v208, 0xffff0000, v194
	v_mul_f32_e32 v148, 0x3d000000, v204
	v_mul_f32_e32 v149, 0x3d000000, v208
	v_lshlrev_b32_e32 v204, 16, v195
	v_and_b32_e32 v208, 0xffff0000, v195
	v_mul_f32_e32 v150, 0x3d000000, v204
	v_mul_f32_e32 v151, 0x3d000000, v208
	v_lshlrev_b32_e32 v204, 16, v196
	v_and_b32_e32 v208, 0xffff0000, v196
	v_mul_f32_e32 v152, 0x3d000000, v204
	v_mul_f32_e32 v153, 0x3d000000, v208
	v_lshlrev_b32_e32 v204, 16, v197
	v_and_b32_e32 v208, 0xffff0000, v197
	v_mul_f32_e32 v154, 0x3d000000, v204
	v_mul_f32_e32 v155, 0x3d000000, v208
	v_lshlrev_b32_e32 v204, 16, v198
	v_and_b32_e32 v208, 0xffff0000, v198
	v_mul_f32_e32 v156, 0x3d000000, v204
	v_mul_f32_e32 v157, 0x3d000000, v208
	v_lshlrev_b32_e32 v204, 16, v199
	v_and_b32_e32 v208, 0xffff0000, v199
	v_mul_f32_e32 v158, 0x3d000000, v204
	v_mul_f32_e32 v159, 0x3d000000, v208
.Lidx_c0:
	s_waitcnt vmcnt(0) lgkmcnt(0)
	s_barrier
	s_cmp_le_u32 s29, 1
	s_cbranch_scc1 .Lidx_nd0
	s_mov_b32 m0, s31
	s_nop 0
	global_load_lds_dwordx4 v57, s[20:21]
	global_load_lds_dwordx4 v57, s[20:21] offset:1024
	global_load_lds_dwordx4 v57, s[20:21] offset:2048
	global_load_lds_dwordx4 v57, s[20:21] offset:3072
	s_add_u32 s20, s20, 0x8000
	s_addc_u32 s21, s21, 0
.Lidx_nd0:
	ds_read_b128 v[2:5], v57 offset:0
	ds_read_b128 v[6:9], v57 offset:1024
	ds_read_b128 v[10:13], v57 offset:2048
	ds_read_b128 v[14:17], v57 offset:3072
	ds_read_b128 v[18:21], v57 offset:4096
	ds_read_b128 v[22:25], v57 offset:5120
	ds_read_b128 v[26:29], v57 offset:6144
	ds_read_b128 v[30:33], v57 offset:7168
	s_waitcnt lgkmcnt(4)
	v_mfma_f32_32x32x16_bf16 v[160:175], v[128:131], v[2:5], 0
	v_mfma_f32_32x32x16_bf16 v[160:175], v[132:135], v[6:9], v[160:175]
	v_mfma_f32_32x32x16_bf16 v[160:175], v[136:139], v[10:13], v[160:175]
	v_mfma_f32_32x32x16_bf16 v[160:175], v[140:143], v[14:17], v[160:175]
	s_cmp_le_u32 s15, 1
	s_cbranch_scc1 .Lidx_x1
	ds_read_b128 v[2:5], v57 offset:8192
	ds_read_b128 v[6:9], v57 offset:9216
	ds_read_b128 v[10:13], v57 offset:10240
	ds_read_b128 v[14:17], v57 offset:11264
	s_waitcnt lgkmcnt(4)
	v_mfma_f32_32x32x16_bf16 v[176:191], v[128:131], v[18:21], 0
	v_mfma_f32_32x32x16_bf16 v[176:191], v[132:135], v[22:25], v[176:191]
	v_mfma_f32_32x32x16_bf16 v[176:191], v[136:139], v[26:29], v[176:191]
	v_mfma_f32_32x32x16_bf16 v[176:191], v[140:143], v[30:33], v[176:191]
	v_cmp_le_i32_e32 vcc, 0, v59
	v_max_f32_e32 v204, 0, v160
	v_max_f32_e32 v208, 0, v161
	v_fma_f32 v201, v144, v204, 0
	v_max_f32_e32 v204, 0, v162
	v_fmac_f32_e32 v201, v145, v208
	v_max_f32_e32 v208, 0, v163
	v_fmac_f32_e32 v201, v146, v204
	v_max_f32_e32 v204, 0, v164
	v_fmac_f32_e32 v201, v147, v208
	v_max_f32_e32 v208, 0, v165
	v_fmac_f32_e32 v201, v148, v204
	v_max_f32_e32 v204, 0, v166
	v_fmac_f32_e32 v201, v149, v208
	v_max_f32_e32 v208, 0, v167
	v_fmac_f32_e32 v201, v150, v204
	v_max_f32_e32 v204, 0, v168
	v_fmac_f32_e32 v201, v151, v208
	v_max_f32_e32 v208, 0, v169
	v_fmac_f32_e32 v201, v152, v204
	v_max_f32_e32 v204, 0, v170
	v_fmac_f32_e32 v201, v153, v208
	v_max_f32_e32 v208, 0, v171
	v_fmac_f32_e32 v201, v154, v204
	v_max_f32_e32 v204, 0, v172
	v_fmac_f32_e32 v201, v155, v208
	v_max_f32_e32 v208, 0, v173
	v_fmac_f32_e32 v201, v156, v204
	v_max_f32_e32 v204, 0, v174
	v_fmac_f32_e32 v201, v157, v208
	v_max_f32_e32 v208, 0, v175
	v_fmac_f32_e32 v201, v158, v204
	v_fmac_f32_e32 v201, v159, v208
	v_cndmask_b32_e32 v201, v61, v201, vcc
	v_ashrrev_i32_e32 v207, 31, v201
	v_or_b32_e32 v207, 0x80000000, v207
	v_xor_b32_e32 v64, v201, v207
	s_cmp_le_u32 s15, 2
	s_cbranch_scc1 .Lidx_x2
	ds_read_b128 v[18:21], v57 offset:12288
	ds_read_b128 v[22:25], v57 offset:13312
	ds_read_b128 v[26:29], v57 offset:14336
	ds_read_b128 v[30:33], v57 offset:15360
	s_waitcnt lgkmcnt(4)
	v_mfma_f32_32x32x16_bf16 v[160:175], v[128:131], v[2:5], 0
	v_mfma_f32_32x32x16_bf16 v[160:175], v[132:135], v[6:9], v[160:175]
	v_mfma_f32_32x32x16_bf16 v[160:175], v[136:139], v[10:13], v[160:175]
	v_mfma_f32_32x32x16_bf16 v[160:175], v[140:143], v[14:17], v[160:175]
	v_cmp_le_i32_e32 vcc, 32, v59
	v_max_f32_e32 v204, 0, v176
	v_max_f32_e32 v208, 0, v177
	v_fma_f32 v201, v144, v204, 0
	v_max_f32_e32 v204, 0, v178
	v_fmac_f32_e32 v201, v145, v208
	v_max_f32_e32 v208, 0, v179
	v_fmac_f32_e32 v201, v146, v204
	v_max_f32_e32 v204, 0, v180
	v_fmac_f32_e32 v201, v147, v208
	v_max_f32_e32 v208, 0, v181
	v_fmac_f32_e32 v201, v148, v204
	v_max_f32_e32 v204, 0, v182
	v_fmac_f32_e32 v201, v149, v208
	v_max_f32_e32 v208, 0, v183
	v_fmac_f32_e32 v201, v150, v204
	v_max_f32_e32 v204, 0, v184
	v_fmac_f32_e32 v201, v151, v208
	v_max_f32_e32 v208, 0, v185
	v_fmac_f32_e32 v201, v152, v204
	v_max_f32_e32 v204, 0, v186
	v_fmac_f32_e32 v201, v153, v208
	v_max_f32_e32 v208, 0, v187
	v_fmac_f32_e32 v201, v154, v204
	v_max_f32_e32 v204, 0, v188
	v_fmac_f32_e32 v201, v155, v208
	v_max_f32_e32 v208, 0, v189
	v_fmac_f32_e32 v201, v156, v204
	v_max_f32_e32 v204, 0, v190
	v_fmac_f32_e32 v201, v157, v208
	v_max_f32_e32 v208, 0, v191
	v_fmac_f32_e32 v201, v158, v204
	v_fmac_f32_e32 v201, v159, v208
	v_cndmask_b32_e32 v201, v61, v201, vcc
	v_ashrrev_i32_e32 v207, 31, v201
	v_or_b32_e32 v207, 0x80000000, v207
	v_xor_b32_e32 v65, v201, v207
	s_cmp_le_u32 s15, 3
	s_cbranch_scc1 .Lidx_x3
	ds_read_b128 v[2:5], v57 offset:16384
	ds_read_b128 v[6:9], v57 offset:17408
	ds_read_b128 v[10:13], v57 offset:18432
	ds_read_b128 v[14:17], v57 offset:19456
	s_waitcnt lgkmcnt(4)
	v_mfma_f32_32x32x16_bf16 v[176:191], v[128:131], v[18:21], 0
	v_mfma_f32_32x32x16_bf16 v[176:191], v[132:135], v[22:25], v[176:191]
	v_mfma_f32_32x32x16_bf16 v[176:191], v[136:139], v[26:29], v[176:191]
	v_mfma_f32_32x32x16_bf16 v[176:191], v[140:143], v[30:33], v[176:191]
	v_cmp_le_i32_e32 vcc, 64, v59
	v_max_f32_e32 v204, 0, v160
	v_max_f32_e32 v208, 0, v161
	v_fma_f32 v201, v144, v204, 0
	v_max_f32_e32 v204, 0, v162
	v_fmac_f32_e32 v201, v145, v208
	v_max_f32_e32 v208, 0, v163
	v_fmac_f32_e32 v201, v146, v204
	v_max_f32_e32 v204, 0, v164
	v_fmac_f32_e32 v201, v147, v208
	v_max_f32_e32 v208, 0, v165
	v_fmac_f32_e32 v201, v148, v204
	v_max_f32_e32 v204, 0, v166
	v_fmac_f32_e32 v201, v149, v208
	v_max_f32_e32 v208, 0, v167
	v_fmac_f32_e32 v201, v150, v204
	v_max_f32_e32 v204, 0, v168
	v_fmac_f32_e32 v201, v151, v208
	v_max_f32_e32 v208, 0, v169
	v_fmac_f32_e32 v201, v152, v204
	v_max_f32_e32 v204, 0, v170
	v_fmac_f32_e32 v201, v153, v208
	v_max_f32_e32 v208, 0, v171
	v_fmac_f32_e32 v201, v154, v204
	v_max_f32_e32 v204, 0, v172
	v_fmac_f32_e32 v201, v155, v208
	v_max_f32_e32 v208, 0, v173
	v_fmac_f32_e32 v201, v156, v204
	v_max_f32_e32 v204, 0, v174
	v_fmac_f32_e32 v201, v157, v208
	v_max_f32_e32 v208, 0, v175
	v_fmac_f32_e32 v201, v158, v204
	v_fmac_f32_e32 v201, v159, v208
	v_cndmask_b32_e32 v201, v61, v201, vcc
	v_ashrrev_i32_e32 v207, 31, v201
	v_or_b32_e32 v207, 0x80000000, v207
	v_xor_b32_e32 v66, v201, v207
	s_cmp_le_u32 s15, 4
	s_cbranch_scc1 .Lidx_x4
	ds_read_b128 v[18:21], v57 offset:20480
	ds_read_b128 v[22:25], v57 offset:21504
	ds_read_b128 v[26:29], v57 offset:22528
	ds_read_b128 v[30:33], v57 offset:23552
	s_waitcnt lgkmcnt(4)
	v_mfma_f32_32x32x16_bf16 v[160:175], v[128:131], v[2:5], 0
	v_mfma_f32_32x32x16_bf16 v[160:175], v[132:135], v[6:9], v[160:175]
	v_mfma_f32_32x32x16_bf16 v[160:175], v[136:139], v[10:13], v[160:175]
	v_mfma_f32_32x32x16_bf16 v[160:175], v[140:143], v[14:17], v[160:175]
	v_cmp_le_i32_e32 vcc, 0x60, v59
	v_max_f32_e32 v204, 0, v176
	v_max_f32_e32 v208, 0, v177
	v_fma_f32 v201, v144, v204, 0
	v_max_f32_e32 v204, 0, v178
	v_fmac_f32_e32 v201, v145, v208
	v_max_f32_e32 v208, 0, v179
	v_fmac_f32_e32 v201, v146, v204
	v_max_f32_e32 v204, 0, v180
	v_fmac_f32_e32 v201, v147, v208
	v_max_f32_e32 v208, 0, v181
	v_fmac_f32_e32 v201, v148, v204
	v_max_f32_e32 v204, 0, v182
	v_fmac_f32_e32 v201, v149, v208
	v_max_f32_e32 v208, 0, v183
	v_fmac_f32_e32 v201, v150, v204
	v_max_f32_e32 v204, 0, v184
	v_fmac_f32_e32 v201, v151, v208
	v_max_f32_e32 v208, 0, v185
	v_fmac_f32_e32 v201, v152, v204
	v_max_f32_e32 v204, 0, v186
	v_fmac_f32_e32 v201, v153, v208
	v_max_f32_e32 v208, 0, v187
	v_fmac_f32_e32 v201, v154, v204
	v_max_f32_e32 v204, 0, v188
	v_fmac_f32_e32 v201, v155, v208
	v_max_f32_e32 v208, 0, v189
	v_fmac_f32_e32 v201, v156, v204
	v_max_f32_e32 v204, 0, v190
	v_fmac_f32_e32 v201, v157, v208
	v_max_f32_e32 v208, 0, v191
	v_fmac_f32_e32 v201, v158, v204
	v_fmac_f32_e32 v201, v159, v208
	v_cndmask_b32_e32 v201, v61, v201, vcc
	v_ashrrev_i32_e32 v207, 31, v201
	v_or_b32_e32 v207, 0x80000000, v207
	v_xor_b32_e32 v67, v201, v207
	s_cmp_le_u32 s15, 5
	s_cbranch_scc1 .Lidx_x5
	ds_read_b128 v[2:5], v57 offset:24576
	ds_read_b128 v[6:9], v57 offset:25600
	ds_read_b128 v[10:13], v57 offset:26624
	ds_read_b128 v[14:17], v57 offset:27648
	s_waitcnt lgkmcnt(4)
	v_mfma_f32_32x32x16_bf16 v[176:191], v[128:131], v[18:21], 0
	v_mfma_f32_32x32x16_bf16 v[176:191], v[132:135], v[22:25], v[176:191]
	v_mfma_f32_32x32x16_bf16 v[176:191], v[136:139], v[26:29], v[176:191]
	v_mfma_f32_32x32x16_bf16 v[176:191], v[140:143], v[30:33], v[176:191]
	v_cmp_le_i32_e32 vcc, 0x80, v59
	v_max_f32_e32 v204, 0, v160
	v_max_f32_e32 v208, 0, v161
	v_fma_f32 v201, v144, v204, 0
	v_max_f32_e32 v204, 0, v162
	v_fmac_f32_e32 v201, v145, v208
	v_max_f32_e32 v208, 0, v163
	v_fmac_f32_e32 v201, v146, v204
	v_max_f32_e32 v204, 0, v164
	v_fmac_f32_e32 v201, v147, v208
	v_max_f32_e32 v208, 0, v165
	v_fmac_f32_e32 v201, v148, v204
	v_max_f32_e32 v204, 0, v166
	v_fmac_f32_e32 v201, v149, v208
	v_max_f32_e32 v208, 0, v167
	v_fmac_f32_e32 v201, v150, v204
	v_max_f32_e32 v204, 0, v168
	v_fmac_f32_e32 v201, v151, v208
	v_max_f32_e32 v208, 0, v169
	v_fmac_f32_e32 v201, v152, v204
	v_max_f32_e32 v204, 0, v170
	v_fmac_f32_e32 v201, v153, v208
	v_max_f32_e32 v208, 0, v171
	v_fmac_f32_e32 v201, v154, v204
	v_max_f32_e32 v204, 0, v172
	v_fmac_f32_e32 v201, v155, v208
	v_max_f32_e32 v208, 0, v173
	v_fmac_f32_e32 v201, v156, v204
	v_max_f32_e32 v204, 0, v174
	v_fmac_f32_e32 v201, v157, v208
	v_max_f32_e32 v208, 0, v175
	v_fmac_f32_e32 v201, v158, v204
	v_fmac_f32_e32 v201, v159, v208
	v_cndmask_b32_e32 v201, v61, v201, vcc
	v_ashrrev_i32_e32 v207, 31, v201
	v_or_b32_e32 v207, 0x80000000, v207
	v_xor_b32_e32 v68, v201, v207
	s_cmp_le_u32 s15, 6
	s_cbranch_scc1 .Lidx_x6
	ds_read_b128 v[18:21], v57 offset:28672
	ds_read_b128 v[22:25], v57 offset:29696
	ds_read_b128 v[26:29], v57 offset:30720
	ds_read_b128 v[30:33], v57 offset:31744
	s_waitcnt lgkmcnt(4)
	v_mfma_f32_32x32x16_bf16 v[160:175], v[128:131], v[2:5], 0
	v_mfma_f32_32x32x16_bf16 v[160:175], v[132:135], v[6:9], v[160:175]
	v_mfma_f32_32x32x16_bf16 v[160:175], v[136:139], v[10:13], v[160:175]
	v_mfma_f32_32x32x16_bf16 v[160:175], v[140:143], v[14:17], v[160:175]
	v_cmp_le_i32_e32 vcc, 0xa0, v59
	v_max_f32_e32 v204, 0, v176
	v_max_f32_e32 v208, 0, v177
	v_fma_f32 v201, v144, v204, 0
	v_max_f32_e32 v204, 0, v178
	v_fmac_f32_e32 v201, v145, v208
	v_max_f32_e32 v208, 0, v179
	v_fmac_f32_e32 v201, v146, v204
	v_max_f32_e32 v204, 0, v180
	v_fmac_f32_e32 v201, v147, v208
	v_max_f32_e32 v208, 0, v181
	v_fmac_f32_e32 v201, v148, v204
	v_max_f32_e32 v204, 0, v182
	v_fmac_f32_e32 v201, v149, v208
	v_max_f32_e32 v208, 0, v183
	v_fmac_f32_e32 v201, v150, v204
	v_max_f32_e32 v204, 0, v184
	v_fmac_f32_e32 v201, v151, v208
	v_max_f32_e32 v208, 0, v185
	v_fmac_f32_e32 v201, v152, v204
	v_max_f32_e32 v204, 0, v186
	v_fmac_f32_e32 v201, v153, v208
	v_max_f32_e32 v208, 0, v187
	v_fmac_f32_e32 v201, v154, v204
	v_max_f32_e32 v204, 0, v188
	v_fmac_f32_e32 v201, v155, v208
	v_max_f32_e32 v208, 0, v189
	v_fmac_f32_e32 v201, v156, v204
	v_max_f32_e32 v204, 0, v190
	v_fmac_f32_e32 v201, v157, v208
	v_max_f32_e32 v208, 0, v191
	v_fmac_f32_e32 v201, v158, v204
	v_fmac_f32_e32 v201, v159, v208
	v_cndmask_b32_e32 v201, v61, v201, vcc
	v_ashrrev_i32_e32 v207, 31, v201
	v_or_b32_e32 v207, 0x80000000, v207
	v_xor_b32_e32 v69, v201, v207
	s_cmp_le_u32 s15, 7
	s_cbranch_scc1 .Lidx_x7
	s_waitcnt lgkmcnt(0)
	v_mfma_f32_32x32x16_bf16 v[176:191], v[128:131], v[18:21], 0
	v_mfma_f32_32x32x16_bf16 v[176:191], v[132:135], v[22:25], v[176:191]
	v_mfma_f32_32x32x16_bf16 v[176:191], v[136:139], v[26:29], v[176:191]
	v_mfma_f32_32x32x16_bf16 v[176:191], v[140:143], v[30:33], v[176:191]
	v_cmp_le_i32_e32 vcc, 0xc0, v59
	v_max_f32_e32 v204, 0, v160
	v_max_f32_e32 v208, 0, v161
	v_fma_f32 v201, v144, v204, 0
	v_max_f32_e32 v204, 0, v162
	v_fmac_f32_e32 v201, v145, v208
	v_max_f32_e32 v208, 0, v163
	v_fmac_f32_e32 v201, v146, v204
	v_max_f32_e32 v204, 0, v164
	v_fmac_f32_e32 v201, v147, v208
	v_max_f32_e32 v208, 0, v165
	v_fmac_f32_e32 v201, v148, v204
	v_max_f32_e32 v204, 0, v166
	v_fmac_f32_e32 v201, v149, v208
	v_max_f32_e32 v208, 0, v167
	v_fmac_f32_e32 v201, v150, v204
	v_max_f32_e32 v204, 0, v168
	v_fmac_f32_e32 v201, v151, v208
	v_max_f32_e32 v208, 0, v169
	v_fmac_f32_e32 v201, v152, v204
	v_max_f32_e32 v204, 0, v170
	v_fmac_f32_e32 v201, v153, v208
	v_max_f32_e32 v208, 0, v171
	v_fmac_f32_e32 v201, v154, v204
	v_max_f32_e32 v204, 0, v172
	v_fmac_f32_e32 v201, v155, v208
	v_max_f32_e32 v208, 0, v173
	v_fmac_f32_e32 v201, v156, v204
	v_max_f32_e32 v204, 0, v174
	v_fmac_f32_e32 v201, v157, v208
	v_max_f32_e32 v208, 0, v175
	v_fmac_f32_e32 v201, v158, v204
	v_fmac_f32_e32 v201, v159, v208
	v_cndmask_b32_e32 v201, v61, v201, vcc
	v_ashrrev_i32_e32 v207, 31, v201
	v_or_b32_e32 v207, 0x80000000, v207
	v_xor_b32_e32 v70, v201, v207
.Lidx_ce0:
.Lidx_c1:
	s_cmp_le_u32 s29, 1
	s_cbranch_scc1 .Lidx_fin1
	s_waitcnt vmcnt(0) lgkmcnt(0)
	s_barrier
	s_cmp_le_u32 s29, 2
	s_cbranch_scc1 .Lidx_nd1
	s_mov_b32 m0, s30
	s_nop 0
	global_load_lds_dwordx4 v57, s[20:21]
	global_load_lds_dwordx4 v57, s[20:21] offset:1024
	global_load_lds_dwordx4 v57, s[20:21] offset:2048
	global_load_lds_dwordx4 v57, s[20:21] offset:3072
	s_add_u32 s20, s20, 0x8000
	s_addc_u32 s21, s21, 0
.Lidx_nd1:
	s_cmp_lt_u32 s15, 8
	s_cbranch_scc1 .Lidx_ce1
	s_cmp_le_u32 s15, 8
	s_cbranch_scc1 .Lidx_x8
	ds_read_b128 v[2:5], v57 offset:32768
	ds_read_b128 v[6:9], v57 offset:33792
	ds_read_b128 v[10:13], v57 offset:34816
	ds_read_b128 v[14:17], v57 offset:35840
	ds_read_b128 v[18:21], v57 offset:36864
	ds_read_b128 v[22:25], v57 offset:37888
	ds_read_b128 v[26:29], v57 offset:38912
	ds_read_b128 v[30:33], v57 offset:39936
	s_waitcnt lgkmcnt(4)
	v_mfma_f32_32x32x16_bf16 v[160:175], v[128:131], v[2:5], 0
	v_mfma_f32_32x32x16_bf16 v[160:175], v[132:135], v[6:9], v[160:175]
	v_mfma_f32_32x32x16_bf16 v[160:175], v[136:139], v[10:13], v[160:175]
	v_mfma_f32_32x32x16_bf16 v[160:175], v[140:143], v[14:17], v[160:175]
	v_cmp_le_i32_e32 vcc, 0xe0, v59
	v_max_f32_e32 v204, 0, v176
	v_max_f32_e32 v208, 0, v177
	v_fma_f32 v201, v144, v204, 0
	v_max_f32_e32 v204, 0, v178
	v_fmac_f32_e32 v201, v145, v208
	v_max_f32_e32 v208, 0, v179
	v_fmac_f32_e32 v201, v146, v204
	v_max_f32_e32 v204, 0, v180
	v_fmac_f32_e32 v201, v147, v208
	v_max_f32_e32 v208, 0, v181
	v_fmac_f32_e32 v201, v148, v204
	v_max_f32_e32 v204, 0, v182
	v_fmac_f32_e32 v201, v149, v208
	v_max_f32_e32 v208, 0, v183
	v_fmac_f32_e32 v201, v150, v204
	v_max_f32_e32 v204, 0, v184
	v_fmac_f32_e32 v201, v151, v208
	v_max_f32_e32 v208, 0, v185
	v_fmac_f32_e32 v201, v152, v204
	v_max_f32_e32 v204, 0, v186
	v_fmac_f32_e32 v201, v153, v208
	v_max_f32_e32 v208, 0, v187
	v_fmac_f32_e32 v201, v154, v204
	v_max_f32_e32 v204, 0, v188
	v_fmac_f32_e32 v201, v155, v208
	v_max_f32_e32 v208, 0, v189
	v_fmac_f32_e32 v201, v156, v204
	v_max_f32_e32 v204, 0, v190
	v_fmac_f32_e32 v201, v157, v208
	v_max_f32_e32 v208, 0, v191
	v_fmac_f32_e32 v201, v158, v204
	v_fmac_f32_e32 v201, v159, v208
	v_cndmask_b32_e32 v201, v61, v201, vcc
	v_ashrrev_i32_e32 v207, 31, v201
	v_or_b32_e32 v207, 0x80000000, v207
	v_xor_b32_e32 v71, v201, v207
	s_cmp_le_u32 s15, 9
	s_cbranch_scc1 .Lidx_x9
	ds_read_b128 v[2:5], v57 offset:40960
	ds_read_b128 v[6:9], v57 offset:41984
	ds_read_b128 v[10:13], v57 offset:43008
	ds_read_b128 v[14:17], v57 offset:44032
	s_waitcnt lgkmcnt(4)
	v_mfma_f32_32x32x16_bf16 v[176:191], v[128:131], v[18:21], 0
	v_mfma_f32_32x32x16_bf16 v[176:191], v[132:135], v[22:25], v[176:191]
	v_mfma_f32_32x32x16_bf16 v[176:191], v[136:139], v[26:29], v[176:191]
	v_mfma_f32_32x32x16_bf16 v[176:191], v[140:143], v[30:33], v[176:191]
	v_cmp_le_i32_e32 vcc, 0x100, v59
	v_max_f32_e32 v204, 0, v160
	v_max_f32_e32 v208, 0, v161
	v_fma_f32 v201, v144, v204, 0
	v_max_f32_e32 v204, 0, v162
	v_fmac_f32_e32 v201, v145, v208
	v_max_f32_e32 v208, 0, v163
	v_fmac_f32_e32 v201, v146, v204
	v_max_f32_e32 v204, 0, v164
	v_fmac_f32_e32 v201, v147, v208
	v_max_f32_e32 v208, 0, v165
	v_fmac_f32_e32 v201, v148, v204
	v_max_f32_e32 v204, 0, v166
	v_fmac_f32_e32 v201, v149, v208
	v_max_f32_e32 v208, 0, v167
	v_fmac_f32_e32 v201, v150, v204
	v_max_f32_e32 v204, 0, v168
	v_fmac_f32_e32 v201, v151, v208
	v_max_f32_e32 v208, 0, v169
	v_fmac_f32_e32 v201, v152, v204
	v_max_f32_e32 v204, 0, v170
	v_fmac_f32_e32 v201, v153, v208
	v_max_f32_e32 v208, 0, v171
	v_fmac_f32_e32 v201, v154, v204
	v_max_f32_e32 v204, 0, v172
	v_fmac_f32_e32 v201, v155, v208
	v_max_f32_e32 v208, 0, v173
	v_fmac_f32_e32 v201, v156, v204
	v_max_f32_e32 v204, 0, v174
	v_fmac_f32_e32 v201, v157, v208
	v_max_f32_e32 v208, 0, v175
	v_fmac_f32_e32 v201, v158, v204
	v_fmac_f32_e32 v201, v159, v208
	v_cndmask_b32_e32 v201, v61, v201, vcc
	v_ashrrev_i32_e32 v207, 31, v201
	v_or_b32_e32 v207, 0x80000000, v207
	v_xor_b32_e32 v72, v201, v207
	s_cmp_le_u32 s15, 10
	s_cbranch_scc1 .Lidx_x10
	ds_read_b128 v[18:21], v57 offset:45056
	ds_read_b128 v[22:25], v57 offset:46080
	ds_read_b128 v[26:29], v57 offset:47104
	ds_read_b128 v[30:33], v57 offset:48128
	s_waitcnt lgkmcnt(4)
	v_mfma_f32_32x32x16_bf16 v[160:175], v[128:131], v[2:5], 0
	v_mfma_f32_32x32x16_bf16 v[160:175], v[132:135], v[6:9], v[160:175]
	v_mfma_f32_32x32x16_bf16 v[160:175], v[136:139], v[10:13], v[160:175]
	v_mfma_f32_32x32x16_bf16 v[160:175], v[140:143], v[14:17], v[160:175]
	v_cmp_le_i32_e32 vcc, 0x120, v59
	v_max_f32_e32 v204, 0, v176
	v_max_f32_e32 v208, 0, v177
	v_fma_f32 v201, v144, v204, 0
	v_max_f32_e32 v204, 0, v178
	v_fmac_f32_e32 v201, v145, v208
	v_max_f32_e32 v208, 0, v179
	v_fmac_f32_e32 v201, v146, v204
	v_max_f32_e32 v204, 0, v180
	v_fmac_f32_e32 v201, v147, v208
	v_max_f32_e32 v208, 0, v181
	v_fmac_f32_e32 v201, v148, v204
	v_max_f32_e32 v204, 0, v182
	v_fmac_f32_e32 v201, v149, v208
	v_max_f32_e32 v208, 0, v183
	v_fmac_f32_e32 v201, v150, v204
	v_max_f32_e32 v204, 0, v184
	v_fmac_f32_e32 v201, v151, v208
	v_max_f32_e32 v208, 0, v185
	v_fmac_f32_e32 v201, v152, v204
	v_max_f32_e32 v204, 0, v186
	v_fmac_f32_e32 v201, v153, v208
	v_max_f32_e32 v208, 0, v187
	v_fmac_f32_e32 v201, v154, v204
	v_max_f32_e32 v204, 0, v188
	v_fmac_f32_e32 v201, v155, v208
	v_max_f32_e32 v208, 0, v189
	v_fmac_f32_e32 v201, v156, v204
	v_max_f32_e32 v204, 0, v190
	v_fmac_f32_e32 v201, v157, v208
	v_max_f32_e32 v208, 0, v191
	v_fmac_f32_e32 v201, v158, v204
	v_fmac_f32_e32 v201, v159, v208
	v_cndmask_b32_e32 v201, v61, v201, vcc
	v_ashrrev_i32_e32 v207, 31, v201
	v_or_b32_e32 v207, 0x80000000, v207
	v_xor_b32_e32 v73, v201, v207
	s_cmp_le_u32 s15, 11
	s_cbranch_scc1 .Lidx_x11
	ds_read_b128 v[2:5], v57 offset:49152
	ds_read_b128 v[6:9], v57 offset:50176
	ds_read_b128 v[10:13], v57 offset:51200
	ds_read_b128 v[14:17], v57 offset:52224
	s_waitcnt lgkmcnt(4)
	v_mfma_f32_32x32x16_bf16 v[176:191], v[128:131], v[18:21], 0
	v_mfma_f32_32x32x16_bf16 v[176:191], v[132:135], v[22:25], v[176:191]
	v_mfma_f32_32x32x16_bf16 v[176:191], v[136:139], v[26:29], v[176:191]
	v_mfma_f32_32x32x16_bf16 v[176:191], v[140:143], v[30:33], v[176:191]
	v_cmp_le_i32_e32 vcc, 0x140, v59
	v_max_f32_e32 v204, 0, v160
	v_max_f32_e32 v208, 0, v161
	v_fma_f32 v201, v144, v204, 0
	v_max_f32_e32 v204, 0, v162
	v_fmac_f32_e32 v201, v145, v208
	v_max_f32_e32 v208, 0, v163
	v_fmac_f32_e32 v201, v146, v204
	v_max_f32_e32 v204, 0, v164
	v_fmac_f32_e32 v201, v147, v208
	v_max_f32_e32 v208, 0, v165
	v_fmac_f32_e32 v201, v148, v204
	v_max_f32_e32 v204, 0, v166
	v_fmac_f32_e32 v201, v149, v208
	v_max_f32_e32 v208, 0, v167
	v_fmac_f32_e32 v201, v150, v204
	v_max_f32_e32 v204, 0, v168
	v_fmac_f32_e32 v201, v151, v208
	v_max_f32_e32 v208, 0, v169
	v_fmac_f32_e32 v201, v152, v204
	v_max_f32_e32 v204, 0, v170
	v_fmac_f32_e32 v201, v153, v208
	v_max_f32_e32 v208, 0, v171
	v_fmac_f32_e32 v201, v154, v204
	v_max_f32_e32 v204, 0, v172
	v_fmac_f32_e32 v201, v155, v208
	v_max_f32_e32 v208, 0, v173
	v_fmac_f32_e32 v201, v156, v204
	v_max_f32_e32 v204, 0, v174
	v_fmac_f32_e32 v201, v157, v208
	v_max_f32_e32 v208, 0, v175
	v_fmac_f32_e32 v201, v158, v204
	v_fmac_f32_e32 v201, v159, v208
	v_cndmask_b32_e32 v201, v61, v201, vcc
	v_ashrrev_i32_e32 v207, 31, v201
	v_or_b32_e32 v207, 0x80000000, v207
	v_xor_b32_e32 v74, v201, v207
	s_cmp_le_u32 s15, 12
	s_cbranch_scc1 .Lidx_x12
	ds_read_b128 v[18:21], v57 offset:53248
	ds_read_b128 v[22:25], v57 offset:54272
	ds_read_b128 v[26:29], v57 offset:55296
	ds_read_b128 v[30:33], v57 offset:56320
	s_waitcnt lgkmcnt(4)
	v_mfma_f32_32x32x16_bf16 v[160:175], v[128:131], v[2:5], 0
	v_mfma_f32_32x32x16_bf16 v[160:175], v[132:135], v[6:9], v[160:175]
	v_mfma_f32_32x32x16_bf16 v[160:175], v[136:139], v[10:13], v[160:175]
	v_mfma_f32_32x32x16_bf16 v[160:175], v[140:143], v[14:17], v[160:175]
	v_cmp_le_i32_e32 vcc, 0x160, v59
	v_max_f32_e32 v204, 0, v176
	v_max_f32_e32 v208, 0, v177
	v_fma_f32 v201, v144, v204, 0
	v_max_f32_e32 v204, 0, v178
	v_fmac_f32_e32 v201, v145, v208
	v_max_f32_e32 v208, 0, v179
	v_fmac_f32_e32 v201, v146, v204
	v_max_f32_e32 v204, 0, v180
	v_fmac_f32_e32 v201, v147, v208
	v_max_f32_e32 v208, 0, v181
	v_fmac_f32_e32 v201, v148, v204
	v_max_f32_e32 v204, 0, v182
	v_fmac_f32_e32 v201, v149, v208
	v_max_f32_e32 v208, 0, v183
	v_fmac_f32_e32 v201, v150, v204
	v_max_f32_e32 v204, 0, v184
	v_fmac_f32_e32 v201, v151, v208
	v_max_f32_e32 v208, 0, v185
	v_fmac_f32_e32 v201, v152, v204
	v_max_f32_e32 v204, 0, v186
	v_fmac_f32_e32 v201, v153, v208
	v_max_f32_e32 v208, 0, v187
	v_fmac_f32_e32 v201, v154, v204
	v_max_f32_e32 v204, 0, v188
	v_fmac_f32_e32 v201, v155, v208
	v_max_f32_e32 v208, 0, v189
	v_fmac_f32_e32 v201, v156, v204
	v_max_f32_e32 v204, 0, v190
	v_fmac_f32_e32 v201, v157, v208
	v_max_f32_e32 v208, 0, v191
	v_fmac_f32_e32 v201, v158, v204
	v_fmac_f32_e32 v201, v159, v208
	v_cndmask_b32_e32 v201, v61, v201, vcc
	v_ashrrev_i32_e32 v207, 31, v201
	v_or_b32_e32 v207, 0x80000000, v207
	v_xor_b32_e32 v75, v201, v207
	s_cmp_le_u32 s15, 13
	s_cbranch_scc1 .Lidx_x13
	ds_read_b128 v[2:5], v57 offset:57344
	ds_read_b128 v[6:9], v57 offset:58368
	ds_read_b128 v[10:13], v57 offset:59392
	ds_read_b128 v[14:17], v57 offset:60416
	s_waitcnt lgkmcnt(4)
	v_mfma_f32_32x32x16_bf16 v[176:191], v[128:131], v[18:21], 0
	v_mfma_f32_32x32x16_bf16 v[176:191], v[132:135], v[22:25], v[176:191]
	v_mfma_f32_32x32x16_bf16 v[176:191], v[136:139], v[26:29], v[176:191]
	v_mfma_f32_32x32x16_bf16 v[176:191], v[140:143], v[30:33], v[176:191]
	v_cmp_le_i32_e32 vcc, 0x180, v59
	v_max_f32_e32 v204, 0, v160
	v_max_f32_e32 v208, 0, v161
	v_fma_f32 v201, v144, v204, 0
	v_max_f32_e32 v204, 0, v162
	v_fmac_f32_e32 v201, v145, v208
	v_max_f32_e32 v208, 0, v163
	v_fmac_f32_e32 v201, v146, v204
	v_max_f32_e32 v204, 0, v164
	v_fmac_f32_e32 v201, v147, v208
	v_max_f32_e32 v208, 0, v165
	v_fmac_f32_e32 v201, v148, v204
	v_max_f32_e32 v204, 0, v166
	v_fmac_f32_e32 v201, v149, v208
	v_max_f32_e32 v208, 0, v167
	v_fmac_f32_e32 v201, v150, v204
	v_max_f32_e32 v204, 0, v168
	v_fmac_f32_e32 v201, v151, v208
	v_max_f32_e32 v208, 0, v169
	v_fmac_f32_e32 v201, v152, v204
	v_max_f32_e32 v204, 0, v170
	v_fmac_f32_e32 v201, v153, v208
	v_max_f32_e32 v208, 0, v171
	v_fmac_f32_e32 v201, v154, v204
	v_max_f32_e32 v204, 0, v172
	v_fmac_f32_e32 v201, v155, v208
	v_max_f32_e32 v208, 0, v173
	v_fmac_f32_e32 v201, v156, v204
	v_max_f32_e32 v204, 0, v174
	v_fmac_f32_e32 v201, v157, v208
	v_max_f32_e32 v208, 0, v175
	v_fmac_f32_e32 v201, v158, v204
	v_fmac_f32_e32 v201, v159, v208
	v_cndmask_b32_e32 v201, v61, v201, vcc
	v_ashrrev_i32_e32 v207, 31, v201
	v_or_b32_e32 v207, 0x80000000, v207
	v_xor_b32_e32 v76, v201, v207
	s_cmp_le_u32 s15, 14
	s_cbranch_scc1 .Lidx_x14
	ds_read_b128 v[18:21], v57 offset:61440
	ds_read_b128 v[22:25], v57 offset:62464
	ds_read_b128 v[26:29], v57 offset:63488
	ds_read_b128 v[30:33], v57 offset:64512
	s_waitcnt lgkmcnt(4)
	v_mfma_f32_32x32x16_bf16 v[160:175], v[128:131], v[2:5], 0
	v_mfma_f32_32x32x16_bf16 v[160:175], v[132:135], v[6:9], v[160:175]
	v_mfma_f32_32x32x16_bf16 v[160:175], v[136:139], v[10:13], v[160:175]
	v_mfma_f32_32x32x16_bf16 v[160:175], v[140:143], v[14:17], v[160:175]
	v_cmp_le_i32_e32 vcc, 0x1a0, v59
	v_max_f32_e32 v204, 0, v176
	v_max_f32_e32 v208, 0, v177
	v_fma_f32 v201, v144, v204, 0
	v_max_f32_e32 v204, 0, v178
	v_fmac_f32_e32 v201, v145, v208
	v_max_f32_e32 v208, 0, v179
	v_fmac_f32_e32 v201, v146, v204
	v_max_f32_e32 v204, 0, v180
	v_fmac_f32_e32 v201, v147, v208
	v_max_f32_e32 v208, 0, v181
	v_fmac_f32_e32 v201, v148, v204
	v_max_f32_e32 v204, 0, v182
	v_fmac_f32_e32 v201, v149, v208
	v_max_f32_e32 v208, 0, v183
	v_fmac_f32_e32 v201, v150, v204
	v_max_f32_e32 v204, 0, v184
	v_fmac_f32_e32 v201, v151, v208
	v_max_f32_e32 v208, 0, v185
	v_fmac_f32_e32 v201, v152, v204
	v_max_f32_e32 v204, 0, v186
	v_fmac_f32_e32 v201, v153, v208
	v_max_f32_e32 v208, 0, v187
	v_fmac_f32_e32 v201, v154, v204
	v_max_f32_e32 v204, 0, v188
	v_fmac_f32_e32 v201, v155, v208
	v_max_f32_e32 v208, 0, v189
	v_fmac_f32_e32 v201, v156, v204
	v_max_f32_e32 v204, 0, v190
	v_fmac_f32_e32 v201, v157, v208
	v_max_f32_e32 v208, 0, v191
	v_fmac_f32_e32 v201, v158, v204
	v_fmac_f32_e32 v201, v159, v208
	v_cndmask_b32_e32 v201, v61, v201, vcc
	v_ashrrev_i32_e32 v207, 31, v201
	v_or_b32_e32 v207, 0x80000000, v207
	v_xor_b32_e32 v77, v201, v207
	s_cmp_le_u32 s15, 15
	s_cbranch_scc1 .Lidx_x15
	s_waitcnt lgkmcnt(0)
	v_mfma_f32_32x32x16_bf16 v[176:191], v[128:131], v[18:21], 0
	v_mfma_f32_32x32x16_bf16 v[176:191], v[132:135], v[22:25], v[176:191]
	v_mfma_f32_32x32x16_bf16 v[176:191], v[136:139], v[26:29], v[176:191]
	v_mfma_f32_32x32x16_bf16 v[176:191], v[140:143], v[30:33], v[176:191]
	v_cmp_le_i32_e32 vcc, 0x1c0, v59
	v_max_f32_e32 v204, 0, v160
	v_max_f32_e32 v208, 0, v161
	v_fma_f32 v201, v144, v204, 0
	v_max_f32_e32 v204, 0, v162
	v_fmac_f32_e32 v201, v145, v208
	v_max_f32_e32 v208, 0, v163
	v_fmac_f32_e32 v201, v146, v204
	v_max_f32_e32 v204, 0, v164
	v_fmac_f32_e32 v201, v147, v208
	v_max_f32_e32 v208, 0, v165
	v_fmac_f32_e32 v201, v148, v204
	v_max_f32_e32 v204, 0, v166
	v_fmac_f32_e32 v201, v149, v208
	v_max_f32_e32 v208, 0, v167
	v_fmac_f32_e32 v201, v150, v204
	v_max_f32_e32 v204, 0, v168
	v_fmac_f32_e32 v201, v151, v208
	v_max_f32_e32 v208, 0, v169
	v_fmac_f32_e32 v201, v152, v204
	v_max_f32_e32 v204, 0, v170
	v_fmac_f32_e32 v201, v153, v208
	v_max_f32_e32 v208, 0, v171
	v_fmac_f32_e32 v201, v154, v204
	v_max_f32_e32 v204, 0, v172
	v_fmac_f32_e32 v201, v155, v208
	v_max_f32_e32 v208, 0, v173
	v_fmac_f32_e32 v201, v156, v204
	v_max_f32_e32 v204, 0, v174
	v_fmac_f32_e32 v201, v157, v208
	v_max_f32_e32 v208, 0, v175
	v_fmac_f32_e32 v201, v158, v204
	v_fmac_f32_e32 v201, v159, v208
	v_cndmask_b32_e32 v201, v61, v201, vcc
	v_ashrrev_i32_e32 v207, 31, v201
	v_or_b32_e32 v207, 0x80000000, v207
	v_xor_b32_e32 v78, v201, v207
.Lidx_ce1:
.Lidx_c2:
	s_cmp_le_u32 s29, 2
	s_cbranch_scc1 .Lidx_fin2
	s_waitcnt vmcnt(0) lgkmcnt(0)
	s_barrier
	s_cmp_le_u32 s29, 3
	s_cbranch_scc1 .Lidx_nd2
	s_mov_b32 m0, s31
	s_nop 0
	global_load_lds_dwordx4 v57, s[20:21]
	global_load_lds_dwordx4 v57, s[20:21] offset:1024
	global_load_lds_dwordx4 v57, s[20:21] offset:2048
	global_load_lds_dwordx4 v57, s[20:21] offset:3072
	s_add_u32 s20, s20, 0x8000
	s_addc_u32 s21, s21, 0
.Lidx_nd2:
	s_cmp_lt_u32 s15, 16
	s_cbranch_scc1 .Lidx_ce2
	s_cmp_le_u32 s15, 16
	s_cbranch_scc1 .Lidx_x16
	ds_read_b128 v[2:5], v57 offset:0
	ds_read_b128 v[6:9], v57 offset:1024
	ds_read_b128 v[10:13], v57 offset:2048
	ds_read_b128 v[14:17], v57 offset:3072
	ds_read_b128 v[18:21], v57 offset:4096
	ds_read_b128 v[22:25], v57 offset:5120
	ds_read_b128 v[26:29], v57 offset:6144
	ds_read_b128 v[30:33], v57 offset:7168
	s_waitcnt lgkmcnt(4)
	v_mfma_f32_32x32x16_bf16 v[160:175], v[128:131], v[2:5], 0
	v_mfma_f32_32x32x16_bf16 v[160:175], v[132:135], v[6:9], v[160:175]
	v_mfma_f32_32x32x16_bf16 v[160:175], v[136:139], v[10:13], v[160:175]
	v_mfma_f32_32x32x16_bf16 v[160:175], v[140:143], v[14:17], v[160:175]
	v_cmp_le_i32_e32 vcc, 0x1e0, v59
	v_max_f32_e32 v204, 0, v176
	v_max_f32_e32 v208, 0, v177
	v_fma_f32 v201, v144, v204, 0
	v_max_f32_e32 v204, 0, v178
	v_fmac_f32_e32 v201, v145, v208
	v_max_f32_e32 v208, 0, v179
	v_fmac_f32_e32 v201, v146, v204
	v_max_f32_e32 v204, 0, v180
	v_fmac_f32_e32 v201, v147, v208
	v_max_f32_e32 v208, 0, v181
	v_fmac_f32_e32 v201, v148, v204
	v_max_f32_e32 v204, 0, v182
	v_fmac_f32_e32 v201, v149, v208
	v_max_f32_e32 v208, 0, v183
	v_fmac_f32_e32 v201, v150, v204
	v_max_f32_e32 v204, 0, v184
	v_fmac_f32_e32 v201, v151, v208
	v_max_f32_e32 v208, 0, v185
	v_fmac_f32_e32 v201, v152, v204
	v_max_f32_e32 v204, 0, v186
	v_fmac_f32_e32 v201, v153, v208
	v_max_f32_e32 v208, 0, v187
	v_fmac_f32_e32 v201, v154, v204
	v_max_f32_e32 v204, 0, v188
	v_fmac_f32_e32 v201, v155, v208
	v_max_f32_e32 v208, 0, v189
	v_fmac_f32_e32 v201, v156, v204
	v_max_f32_e32 v204, 0, v190
	v_fmac_f32_e32 v201, v157, v208
	v_max_f32_e32 v208, 0, v191
	v_fmac_f32_e32 v201, v158, v204
	v_fmac_f32_e32 v201, v159, v208
	v_cndmask_b32_e32 v201, v61, v201, vcc
	v_ashrrev_i32_e32 v207, 31, v201
	v_or_b32_e32 v207, 0x80000000, v207
	v_xor_b32_e32 v79, v201, v207
	s_cmp_le_u32 s15, 17
	s_cbranch_scc1 .Lidx_x17
	ds_read_b128 v[2:5], v57 offset:8192
	ds_read_b128 v[6:9], v57 offset:9216
	ds_read_b128 v[10:13], v57 offset:10240
	ds_read_b128 v[14:17], v57 offset:11264
	s_waitcnt lgkmcnt(4)
	v_mfma_f32_32x32x16_bf16 v[176:191], v[128:131], v[18:21], 0
	v_mfma_f32_32x32x16_bf16 v[176:191], v[132:135], v[22:25], v[176:191]
	v_mfma_f32_32x32x16_bf16 v[176:191], v[136:139], v[26:29], v[176:191]
	v_mfma_f32_32x32x16_bf16 v[176:191], v[140:143], v[30:33], v[176:191]
	v_cmp_le_i32_e32 vcc, 0x200, v59
	v_max_f32_e32 v204, 0, v160
	v_max_f32_e32 v208, 0, v161
	v_fma_f32 v201, v144, v204, 0
	v_max_f32_e32 v204, 0, v162
	v_fmac_f32_e32 v201, v145, v208
	v_max_f32_e32 v208, 0, v163
	v_fmac_f32_e32 v201, v146, v204
	v_max_f32_e32 v204, 0, v164
	v_fmac_f32_e32 v201, v147, v208
	v_max_f32_e32 v208, 0, v165
	v_fmac_f32_e32 v201, v148, v204
	v_max_f32_e32 v204, 0, v166
	v_fmac_f32_e32 v201, v149, v208
	v_max_f32_e32 v208, 0, v167
	v_fmac_f32_e32 v201, v150, v204
	v_max_f32_e32 v204, 0, v168
	v_fmac_f32_e32 v201, v151, v208
	v_max_f32_e32 v208, 0, v169
	v_fmac_f32_e32 v201, v152, v204
	v_max_f32_e32 v204, 0, v170
	v_fmac_f32_e32 v201, v153, v208
	v_max_f32_e32 v208, 0, v171
	v_fmac_f32_e32 v201, v154, v204
	v_max_f32_e32 v204, 0, v172
	v_fmac_f32_e32 v201, v155, v208
	v_max_f32_e32 v208, 0, v173
	v_fmac_f32_e32 v201, v156, v204
	v_max_f32_e32 v204, 0, v174
	v_fmac_f32_e32 v201, v157, v208
	v_max_f32_e32 v208, 0, v175
	v_fmac_f32_e32 v201, v158, v204
	v_fmac_f32_e32 v201, v159, v208
	v_cndmask_b32_e32 v201, v61, v201, vcc
	v_ashrrev_i32_e32 v207, 31, v201
	v_or_b32_e32 v207, 0x80000000, v207
	v_xor_b32_e32 v80, v201, v207
	s_cmp_le_u32 s15, 18
	s_cbranch_scc1 .Lidx_x18
	ds_read_b128 v[18:21], v57 offset:12288
	ds_read_b128 v[22:25], v57 offset:13312
	ds_read_b128 v[26:29], v57 offset:14336
	ds_read_b128 v[30:33], v57 offset:15360
	s_waitcnt lgkmcnt(4)
	v_mfma_f32_32x32x16_bf16 v[160:175], v[128:131], v[2:5], 0
	v_mfma_f32_32x32x16_bf16 v[160:175], v[132:135], v[6:9], v[160:175]
	v_mfma_f32_32x32x16_bf16 v[160:175], v[136:139], v[10:13], v[160:175]
	v_mfma_f32_32x32x16_bf16 v[160:175], v[140:143], v[14:17], v[160:175]
	v_cmp_le_i32_e32 vcc, 0x220, v59
	v_max_f32_e32 v204, 0, v176
	v_max_f32_e32 v208, 0, v177
	v_fma_f32 v201, v144, v204, 0
	v_max_f32_e32 v204, 0, v178
	v_fmac_f32_e32 v201, v145, v208
	v_max_f32_e32 v208, 0, v179
	v_fmac_f32_e32 v201, v146, v204
	v_max_f32_e32 v204, 0, v180
	v_fmac_f32_e32 v201, v147, v208
	v_max_f32_e32 v208, 0, v181
	v_fmac_f32_e32 v201, v148, v204
	v_max_f32_e32 v204, 0, v182
	v_fmac_f32_e32 v201, v149, v208
	v_max_f32_e32 v208, 0, v183
	v_fmac_f32_e32 v201, v150, v204
	v_max_f32_e32 v204, 0, v184
	v_fmac_f32_e32 v201, v151, v208
	v_max_f32_e32 v208, 0, v185
	v_fmac_f32_e32 v201, v152, v204
	v_max_f32_e32 v204, 0, v186
	v_fmac_f32_e32 v201, v153, v208
	v_max_f32_e32 v208, 0, v187
	v_fmac_f32_e32 v201, v154, v204
	v_max_f32_e32 v204, 0, v188
	v_fmac_f32_e32 v201, v155, v208
	v_max_f32_e32 v208, 0, v189
	v_fmac_f32_e32 v201, v156, v204
	v_max_f32_e32 v204, 0, v190
	v_fmac_f32_e32 v201, v157, v208
	v_max_f32_e32 v208, 0, v191
	v_fmac_f32_e32 v201, v158, v204
	v_fmac_f32_e32 v201, v159, v208
	v_cndmask_b32_e32 v201, v61, v201, vcc
	v_ashrrev_i32_e32 v207, 31, v201
	v_or_b32_e32 v207, 0x80000000, v207
	v_xor_b32_e32 v81, v201, v207
	s_cmp_le_u32 s15, 19
	s_cbranch_scc1 .Lidx_x19
	ds_read_b128 v[2:5], v57 offset:16384
	ds_read_b128 v[6:9], v57 offset:17408
	ds_read_b128 v[10:13], v57 offset:18432
	ds_read_b128 v[14:17], v57 offset:19456
	s_waitcnt lgkmcnt(4)
	v_mfma_f32_32x32x16_bf16 v[176:191], v[128:131], v[18:21], 0
	v_mfma_f32_32x32x16_bf16 v[176:191], v[132:135], v[22:25], v[176:191]
	v_mfma_f32_32x32x16_bf16 v[176:191], v[136:139], v[26:29], v[176:191]
	v_mfma_f32_32x32x16_bf16 v[176:191], v[140:143], v[30:33], v[176:191]
	v_cmp_le_i32_e32 vcc, 0x240, v59
	v_max_f32_e32 v204, 0, v160
	v_max_f32_e32 v208, 0, v161
	v_fma_f32 v201, v144, v204, 0
	v_max_f32_e32 v204, 0, v162
	v_fmac_f32_e32 v201, v145, v208
	v_max_f32_e32 v208, 0, v163
	v_fmac_f32_e32 v201, v146, v204
	v_max_f32_e32 v204, 0, v164
	v_fmac_f32_e32 v201, v147, v208
	v_max_f32_e32 v208, 0, v165
	v_fmac_f32_e32 v201, v148, v204
	v_max_f32_e32 v204, 0, v166
	v_fmac_f32_e32 v201, v149, v208
	v_max_f32_e32 v208, 0, v167
	v_fmac_f32_e32 v201, v150, v204
	v_max_f32_e32 v204, 0, v168
	v_fmac_f32_e32 v201, v151, v208
	v_max_f32_e32 v208, 0, v169
	v_fmac_f32_e32 v201, v152, v204
	v_max_f32_e32 v204, 0, v170
	v_fmac_f32_e32 v201, v153, v208
	v_max_f32_e32 v208, 0, v171
	v_fmac_f32_e32 v201, v154, v204
	v_max_f32_e32 v204, 0, v172
	v_fmac_f32_e32 v201, v155, v208
	v_max_f32_e32 v208, 0, v173
	v_fmac_f32_e32 v201, v156, v204
	v_max_f32_e32 v204, 0, v174
	v_fmac_f32_e32 v201, v157, v208
	v_max_f32_e32 v208, 0, v175
	v_fmac_f32_e32 v201, v158, v204
	v_fmac_f32_e32 v201, v159, v208
	v_cndmask_b32_e32 v201, v61, v201, vcc
	v_ashrrev_i32_e32 v207, 31, v201
	v_or_b32_e32 v207, 0x80000000, v207
	v_xor_b32_e32 v82, v201, v207
	s_cmp_le_u32 s15, 20
	s_cbranch_scc1 .Lidx_x20
	ds_read_b128 v[18:21], v57 offset:20480
	ds_read_b128 v[22:25], v57 offset:21504
	ds_read_b128 v[26:29], v57 offset:22528
	ds_read_b128 v[30:33], v57 offset:23552
	s_waitcnt lgkmcnt(4)
	v_mfma_f32_32x32x16_bf16 v[160:175], v[128:131], v[2:5], 0
	v_mfma_f32_32x32x16_bf16 v[160:175], v[132:135], v[6:9], v[160:175]
	v_mfma_f32_32x32x16_bf16 v[160:175], v[136:139], v[10:13], v[160:175]
	v_mfma_f32_32x32x16_bf16 v[160:175], v[140:143], v[14:17], v[160:175]
	v_cmp_le_i32_e32 vcc, 0x260, v59
	v_max_f32_e32 v204, 0, v176
	v_max_f32_e32 v208, 0, v177
	v_fma_f32 v201, v144, v204, 0
	v_max_f32_e32 v204, 0, v178
	v_fmac_f32_e32 v201, v145, v208
	v_max_f32_e32 v208, 0, v179
	v_fmac_f32_e32 v201, v146, v204
	v_max_f32_e32 v204, 0, v180
	v_fmac_f32_e32 v201, v147, v208
	v_max_f32_e32 v208, 0, v181
	v_fmac_f32_e32 v201, v148, v204
	v_max_f32_e32 v204, 0, v182
	v_fmac_f32_e32 v201, v149, v208
	v_max_f32_e32 v208, 0, v183
	v_fmac_f32_e32 v201, v150, v204
	v_max_f32_e32 v204, 0, v184
	v_fmac_f32_e32 v201, v151, v208
	v_max_f32_e32 v208, 0, v185
	v_fmac_f32_e32 v201, v152, v204
	v_max_f32_e32 v204, 0, v186
	v_fmac_f32_e32 v201, v153, v208
	v_max_f32_e32 v208, 0, v187
	v_fmac_f32_e32 v201, v154, v204
	v_max_f32_e32 v204, 0, v188
	v_fmac_f32_e32 v201, v155, v208
	v_max_f32_e32 v208, 0, v189
	v_fmac_f32_e32 v201, v156, v204
	v_max_f32_e32 v204, 0, v190
	v_fmac_f32_e32 v201, v157, v208
	v_max_f32_e32 v208, 0, v191
	v_fmac_f32_e32 v201, v158, v204
	v_fmac_f32_e32 v201, v159, v208
	v_cndmask_b32_e32 v201, v61, v201, vcc
	v_ashrrev_i32_e32 v207, 31, v201
	v_or_b32_e32 v207, 0x80000000, v207
	v_xor_b32_e32 v83, v201, v207
	s_cmp_le_u32 s15, 21
	s_cbranch_scc1 .Lidx_x21
	ds_read_b128 v[2:5], v57 offset:24576
	ds_read_b128 v[6:9], v57 offset:25600
	ds_read_b128 v[10:13], v57 offset:26624
	ds_read_b128 v[14:17], v57 offset:27648
	s_waitcnt lgkmcnt(4)
	v_mfma_f32_32x32x16_bf16 v[176:191], v[128:131], v[18:21], 0
	v_mfma_f32_32x32x16_bf16 v[176:191], v[132:135], v[22:25], v[176:191]
	v_mfma_f32_32x32x16_bf16 v[176:191], v[136:139], v[26:29], v[176:191]
	v_mfma_f32_32x32x16_bf16 v[176:191], v[140:143], v[30:33], v[176:191]
	v_cmp_le_i32_e32 vcc, 0x280, v59
	v_max_f32_e32 v204, 0, v160
	v_max_f32_e32 v208, 0, v161
	v_fma_f32 v201, v144, v204, 0
	v_max_f32_e32 v204, 0, v162
	v_fmac_f32_e32 v201, v145, v208
	v_max_f32_e32 v208, 0, v163
	v_fmac_f32_e32 v201, v146, v204
	v_max_f32_e32 v204, 0, v164
	v_fmac_f32_e32 v201, v147, v208
	v_max_f32_e32 v208, 0, v165
	v_fmac_f32_e32 v201, v148, v204
	v_max_f32_e32 v204, 0, v166
	v_fmac_f32_e32 v201, v149, v208
	v_max_f32_e32 v208, 0, v167
	v_fmac_f32_e32 v201, v150, v204
	v_max_f32_e32 v204, 0, v168
	v_fmac_f32_e32 v201, v151, v208
	v_max_f32_e32 v208, 0, v169
	v_fmac_f32_e32 v201, v152, v204
	v_max_f32_e32 v204, 0, v170
	v_fmac_f32_e32 v201, v153, v208
	v_max_f32_e32 v208, 0, v171
	v_fmac_f32_e32 v201, v154, v204
	v_max_f32_e32 v204, 0, v172
	v_fmac_f32_e32 v201, v155, v208
	v_max_f32_e32 v208, 0, v173
	v_fmac_f32_e32 v201, v156, v204
	v_max_f32_e32 v204, 0, v174
	v_fmac_f32_e32 v201, v157, v208
	v_max_f32_e32 v208, 0, v175
	v_fmac_f32_e32 v201, v158, v204
	v_fmac_f32_e32 v201, v159, v208
	v_cndmask_b32_e32 v201, v61, v201, vcc
	v_ashrrev_i32_e32 v207, 31, v201
	v_or_b32_e32 v207, 0x80000000, v207
	v_xor_b32_e32 v84, v201, v207
	s_cmp_le_u32 s15, 22
	s_cbranch_scc1 .Lidx_x22
	ds_read_b128 v[18:21], v57 offset:28672
	ds_read_b128 v[22:25], v57 offset:29696
	ds_read_b128 v[26:29], v57 offset:30720
	ds_read_b128 v[30:33], v57 offset:31744
	s_waitcnt lgkmcnt(4)
	v_mfma_f32_32x32x16_bf16 v[160:175], v[128:131], v[2:5], 0
	v_mfma_f32_32x32x16_bf16 v[160:175], v[132:135], v[6:9], v[160:175]
	v_mfma_f32_32x32x16_bf16 v[160:175], v[136:139], v[10:13], v[160:175]
	v_mfma_f32_32x32x16_bf16 v[160:175], v[140:143], v[14:17], v[160:175]
	v_cmp_le_i32_e32 vcc, 0x2a0, v59
	v_max_f32_e32 v204, 0, v176
	v_max_f32_e32 v208, 0, v177
	v_fma_f32 v201, v144, v204, 0
	v_max_f32_e32 v204, 0, v178
	v_fmac_f32_e32 v201, v145, v208
	v_max_f32_e32 v208, 0, v179
	v_fmac_f32_e32 v201, v146, v204
	v_max_f32_e32 v204, 0, v180
	v_fmac_f32_e32 v201, v147, v208
	v_max_f32_e32 v208, 0, v181
	v_fmac_f32_e32 v201, v148, v204
	v_max_f32_e32 v204, 0, v182
	v_fmac_f32_e32 v201, v149, v208
	v_max_f32_e32 v208, 0, v183
	v_fmac_f32_e32 v201, v150, v204
	v_max_f32_e32 v204, 0, v184
	v_fmac_f32_e32 v201, v151, v208
	v_max_f32_e32 v208, 0, v185
	v_fmac_f32_e32 v201, v152, v204
	v_max_f32_e32 v204, 0, v186
	v_fmac_f32_e32 v201, v153, v208
	v_max_f32_e32 v208, 0, v187
	v_fmac_f32_e32 v201, v154, v204
	v_max_f32_e32 v204, 0, v188
	v_fmac_f32_e32 v201, v155, v208
	v_max_f32_e32 v208, 0, v189
	v_fmac_f32_e32 v201, v156, v204
	v_max_f32_e32 v204, 0, v190
	v_fmac_f32_e32 v201, v157, v208
	v_max_f32_e32 v208, 0, v191
	v_fmac_f32_e32 v201, v158, v204
	v_fmac_f32_e32 v201, v159, v208
	v_cndmask_b32_e32 v201, v61, v201, vcc
	v_ashrrev_i32_e32 v207, 31, v201
	v_or_b32_e32 v207, 0x80000000, v207
	v_xor_b32_e32 v85, v201, v207
	s_cmp_le_u32 s15, 23
	s_cbranch_scc1 .Lidx_x23
	s_waitcnt lgkmcnt(0)
	v_mfma_f32_32x32x16_bf16 v[176:191], v[128:131], v[18:21], 0
	v_mfma_f32_32x32x16_bf16 v[176:191], v[132:135], v[22:25], v[176:191]
	v_mfma_f32_32x32x16_bf16 v[176:191], v[136:139], v[26:29], v[176:191]
	v_mfma_f32_32x32x16_bf16 v[176:191], v[140:143], v[30:33], v[176:191]
	v_cmp_le_i32_e32 vcc, 0x2c0, v59
	v_max_f32_e32 v204, 0, v160
	v_max_f32_e32 v208, 0, v161
	v_fma_f32 v201, v144, v204, 0
	v_max_f32_e32 v204, 0, v162
	v_fmac_f32_e32 v201, v145, v208
	v_max_f32_e32 v208, 0, v163
	v_fmac_f32_e32 v201, v146, v204
	v_max_f32_e32 v204, 0, v164
	v_fmac_f32_e32 v201, v147, v208
	v_max_f32_e32 v208, 0, v165
	v_fmac_f32_e32 v201, v148, v204
	v_max_f32_e32 v204, 0, v166
	v_fmac_f32_e32 v201, v149, v208
	v_max_f32_e32 v208, 0, v167
	v_fmac_f32_e32 v201, v150, v204
	v_max_f32_e32 v204, 0, v168
	v_fmac_f32_e32 v201, v151, v208
	v_max_f32_e32 v208, 0, v169
	v_fmac_f32_e32 v201, v152, v204
	v_max_f32_e32 v204, 0, v170
	v_fmac_f32_e32 v201, v153, v208
	v_max_f32_e32 v208, 0, v171
	v_fmac_f32_e32 v201, v154, v204
	v_max_f32_e32 v204, 0, v172
	v_fmac_f32_e32 v201, v155, v208
	v_max_f32_e32 v208, 0, v173
	v_fmac_f32_e32 v201, v156, v204
	v_max_f32_e32 v204, 0, v174
	v_fmac_f32_e32 v201, v157, v208
	v_max_f32_e32 v208, 0, v175
	v_fmac_f32_e32 v201, v158, v204
	v_fmac_f32_e32 v201, v159, v208
	v_cndmask_b32_e32 v201, v61, v201, vcc
	v_ashrrev_i32_e32 v207, 31, v201
	v_or_b32_e32 v207, 0x80000000, v207
	v_xor_b32_e32 v86, v201, v207
.Lidx_ce2:
.Lidx_c3:
	s_cmp_le_u32 s29, 3
	s_cbranch_scc1 .Lidx_fin3
	s_waitcnt vmcnt(0) lgkmcnt(0)
	s_barrier
	s_cmp_le_u32 s29, 4
	s_cbranch_scc1 .Lidx_nd3
	s_mov_b32 m0, s30
	s_nop 0
	global_load_lds_dwordx4 v57, s[20:21]
	global_load_lds_dwordx4 v57, s[20:21] offset:1024
	global_load_lds_dwordx4 v57, s[20:21] offset:2048
	global_load_lds_dwordx4 v57, s[20:21] offset:3072
	s_add_u32 s20, s20, 0x8000
	s_addc_u32 s21, s21, 0
.Lidx_nd3:
	s_cmp_lt_u32 s15, 24
	s_cbranch_scc1 .Lidx_ce3
	s_cmp_le_u32 s15, 24
	s_cbranch_scc1 .Lidx_x24
	ds_read_b128 v[2:5], v57 offset:32768
	ds_read_b128 v[6:9], v57 offset:33792
	ds_read_b128 v[10:13], v57 offset:34816
	ds_read_b128 v[14:17], v57 offset:35840
	ds_read_b128 v[18:21], v57 offset:36864
	ds_read_b128 v[22:25], v57 offset:37888
	ds_read_b128 v[26:29], v57 offset:38912
	ds_read_b128 v[30:33], v57 offset:39936
	s_waitcnt lgkmcnt(4)
	v_mfma_f32_32x32x16_bf16 v[160:175], v[128:131], v[2:5], 0
	v_mfma_f32_32x32x16_bf16 v[160:175], v[132:135], v[6:9], v[160:175]
	v_mfma_f32_32x32x16_bf16 v[160:175], v[136:139], v[10:13], v[160:175]
	v_mfma_f32_32x32x16_bf16 v[160:175], v[140:143], v[14:17], v[160:175]
	v_cmp_le_i32_e32 vcc, 0x2e0, v59
	v_max_f32_e32 v204, 0, v176
	v_max_f32_e32 v208, 0, v177
	v_fma_f32 v201, v144, v204, 0
	v_max_f32_e32 v204, 0, v178
	v_fmac_f32_e32 v201, v145, v208
	v_max_f32_e32 v208, 0, v179
	v_fmac_f32_e32 v201, v146, v204
	v_max_f32_e32 v204, 0, v180
	v_fmac_f32_e32 v201, v147, v208
	v_max_f32_e32 v208, 0, v181
	v_fmac_f32_e32 v201, v148, v204
	v_max_f32_e32 v204, 0, v182
	v_fmac_f32_e32 v201, v149, v208
	v_max_f32_e32 v208, 0, v183
	v_fmac_f32_e32 v201, v150, v204
	v_max_f32_e32 v204, 0, v184
	v_fmac_f32_e32 v201, v151, v208
	v_max_f32_e32 v208, 0, v185
	v_fmac_f32_e32 v201, v152, v204
	v_max_f32_e32 v204, 0, v186
	v_fmac_f32_e32 v201, v153, v208
	v_max_f32_e32 v208, 0, v187
	v_fmac_f32_e32 v201, v154, v204
	v_max_f32_e32 v204, 0, v188
	v_fmac_f32_e32 v201, v155, v208
	v_max_f32_e32 v208, 0, v189
	v_fmac_f32_e32 v201, v156, v204
	v_max_f32_e32 v204, 0, v190
	v_fmac_f32_e32 v201, v157, v208
	v_max_f32_e32 v208, 0, v191
	v_fmac_f32_e32 v201, v158, v204
	v_fmac_f32_e32 v201, v159, v208
	v_cndmask_b32_e32 v201, v61, v201, vcc
	v_ashrrev_i32_e32 v207, 31, v201
	v_or_b32_e32 v207, 0x80000000, v207
	v_xor_b32_e32 v87, v201, v207
	s_cmp_le_u32 s15, 25
	s_cbranch_scc1 .Lidx_x25
	ds_read_b128 v[2:5], v57 offset:40960
	ds_read_b128 v[6:9], v57 offset:41984
	ds_read_b128 v[10:13], v57 offset:43008
	ds_read_b128 v[14:17], v57 offset:44032
	s_waitcnt lgkmcnt(4)
	v_mfma_f32_32x32x16_bf16 v[176:191], v[128:131], v[18:21], 0
	v_mfma_f32_32x32x16_bf16 v[176:191], v[132:135], v[22:25], v[176:191]
	v_mfma_f32_32x32x16_bf16 v[176:191], v[136:139], v[26:29], v[176:191]
	v_mfma_f32_32x32x16_bf16 v[176:191], v[140:143], v[30:33], v[176:191]
	v_cmp_le_i32_e32 vcc, 0x300, v59
	v_max_f32_e32 v204, 0, v160
	v_max_f32_e32 v208, 0, v161
	v_fma_f32 v201, v144, v204, 0
	v_max_f32_e32 v204, 0, v162
	v_fmac_f32_e32 v201, v145, v208
	v_max_f32_e32 v208, 0, v163
	v_fmac_f32_e32 v201, v146, v204
	v_max_f32_e32 v204, 0, v164
	v_fmac_f32_e32 v201, v147, v208
	v_max_f32_e32 v208, 0, v165
	v_fmac_f32_e32 v201, v148, v204
	v_max_f32_e32 v204, 0, v166
	v_fmac_f32_e32 v201, v149, v208
	v_max_f32_e32 v208, 0, v167
	v_fmac_f32_e32 v201, v150, v204
	v_max_f32_e32 v204, 0, v168
	v_fmac_f32_e32 v201, v151, v208
	v_max_f32_e32 v208, 0, v169
	v_fmac_f32_e32 v201, v152, v204
	v_max_f32_e32 v204, 0, v170
	v_fmac_f32_e32 v201, v153, v208
	v_max_f32_e32 v208, 0, v171
	v_fmac_f32_e32 v201, v154, v204
	v_max_f32_e32 v204, 0, v172
	v_fmac_f32_e32 v201, v155, v208
	v_max_f32_e32 v208, 0, v173
	v_fmac_f32_e32 v201, v156, v204
	v_max_f32_e32 v204, 0, v174
	v_fmac_f32_e32 v201, v157, v208
	v_max_f32_e32 v208, 0, v175
	v_fmac_f32_e32 v201, v158, v204
	v_fmac_f32_e32 v201, v159, v208
	v_cndmask_b32_e32 v201, v61, v201, vcc
	v_ashrrev_i32_e32 v207, 31, v201
	v_or_b32_e32 v207, 0x80000000, v207
	v_xor_b32_e32 v88, v201, v207
	s_cmp_le_u32 s15, 26
	s_cbranch_scc1 .Lidx_x26
	ds_read_b128 v[18:21], v57 offset:45056
	ds_read_b128 v[22:25], v57 offset:46080
	ds_read_b128 v[26:29], v57 offset:47104
	ds_read_b128 v[30:33], v57 offset:48128
	s_waitcnt lgkmcnt(4)
	v_mfma_f32_32x32x16_bf16 v[160:175], v[128:131], v[2:5], 0
	v_mfma_f32_32x32x16_bf16 v[160:175], v[132:135], v[6:9], v[160:175]
	v_mfma_f32_32x32x16_bf16 v[160:175], v[136:139], v[10:13], v[160:175]
	v_mfma_f32_32x32x16_bf16 v[160:175], v[140:143], v[14:17], v[160:175]
	v_cmp_le_i32_e32 vcc, 0x320, v59
	v_max_f32_e32 v204, 0, v176
	v_max_f32_e32 v208, 0, v177
	v_fma_f32 v201, v144, v204, 0
	v_max_f32_e32 v204, 0, v178
	v_fmac_f32_e32 v201, v145, v208
	v_max_f32_e32 v208, 0, v179
	v_fmac_f32_e32 v201, v146, v204
	v_max_f32_e32 v204, 0, v180
	v_fmac_f32_e32 v201, v147, v208
	v_max_f32_e32 v208, 0, v181
	v_fmac_f32_e32 v201, v148, v204
	v_max_f32_e32 v204, 0, v182
	v_fmac_f32_e32 v201, v149, v208
	v_max_f32_e32 v208, 0, v183
	v_fmac_f32_e32 v201, v150, v204
	v_max_f32_e32 v204, 0, v184
	v_fmac_f32_e32 v201, v151, v208
	v_max_f32_e32 v208, 0, v185
	v_fmac_f32_e32 v201, v152, v204
	v_max_f32_e32 v204, 0, v186
	v_fmac_f32_e32 v201, v153, v208
	v_max_f32_e32 v208, 0, v187
	v_fmac_f32_e32 v201, v154, v204
	v_max_f32_e32 v204, 0, v188
	v_fmac_f32_e32 v201, v155, v208
	v_max_f32_e32 v208, 0, v189
	v_fmac_f32_e32 v201, v156, v204
	v_max_f32_e32 v204, 0, v190
	v_fmac_f32_e32 v201, v157, v208
	v_max_f32_e32 v208, 0, v191
	v_fmac_f32_e32 v201, v158, v204
	v_fmac_f32_e32 v201, v159, v208
	v_cndmask_b32_e32 v201, v61, v201, vcc
	v_ashrrev_i32_e32 v207, 31, v201
	v_or_b32_e32 v207, 0x80000000, v207
	v_xor_b32_e32 v89, v201, v207
	s_cmp_le_u32 s15, 27
	s_cbranch_scc1 .Lidx_x27
	ds_read_b128 v[2:5], v57 offset:49152
	ds_read_b128 v[6:9], v57 offset:50176
	ds_read_b128 v[10:13], v57 offset:51200
	ds_read_b128 v[14:17], v57 offset:52224
	s_waitcnt lgkmcnt(4)
	v_mfma_f32_32x32x16_bf16 v[176:191], v[128:131], v[18:21], 0
	v_mfma_f32_32x32x16_bf16 v[176:191], v[132:135], v[22:25], v[176:191]
	v_mfma_f32_32x32x16_bf16 v[176:191], v[136:139], v[26:29], v[176:191]
	v_mfma_f32_32x32x16_bf16 v[176:191], v[140:143], v[30:33], v[176:191]
	v_cmp_le_i32_e32 vcc, 0x340, v59
	v_max_f32_e32 v204, 0, v160
	v_max_f32_e32 v208, 0, v161
	v_fma_f32 v201, v144, v204, 0
	v_max_f32_e32 v204, 0, v162
	v_fmac_f32_e32 v201, v145, v208
	v_max_f32_e32 v208, 0, v163
	v_fmac_f32_e32 v201, v146, v204
	v_max_f32_e32 v204, 0, v164
	v_fmac_f32_e32 v201, v147, v208
	v_max_f32_e32 v208, 0, v165
	v_fmac_f32_e32 v201, v148, v204
	v_max_f32_e32 v204, 0, v166
	v_fmac_f32_e32 v201, v149, v208
	v_max_f32_e32 v208, 0, v167
	v_fmac_f32_e32 v201, v150, v204
	v_max_f32_e32 v204, 0, v168
	v_fmac_f32_e32 v201, v151, v208
	v_max_f32_e32 v208, 0, v169
	v_fmac_f32_e32 v201, v152, v204
	v_max_f32_e32 v204, 0, v170
	v_fmac_f32_e32 v201, v153, v208
	v_max_f32_e32 v208, 0, v171
	v_fmac_f32_e32 v201, v154, v204
	v_max_f32_e32 v204, 0, v172
	v_fmac_f32_e32 v201, v155, v208
	v_max_f32_e32 v208, 0, v173
	v_fmac_f32_e32 v201, v156, v204
	v_max_f32_e32 v204, 0, v174
	v_fmac_f32_e32 v201, v157, v208
	v_max_f32_e32 v208, 0, v175
	v_fmac_f32_e32 v201, v158, v204
	v_fmac_f32_e32 v201, v159, v208
	v_cndmask_b32_e32 v201, v61, v201, vcc
	v_ashrrev_i32_e32 v207, 31, v201
	v_or_b32_e32 v207, 0x80000000, v207
	v_xor_b32_e32 v90, v201, v207
	s_cmp_le_u32 s15, 28
	s_cbranch_scc1 .Lidx_x28
	ds_read_b128 v[18:21], v57 offset:53248
	ds_read_b128 v[22:25], v57 offset:54272
	ds_read_b128 v[26:29], v57 offset:55296
	ds_read_b128 v[30:33], v57 offset:56320
	s_waitcnt lgkmcnt(4)
	v_mfma_f32_32x32x16_bf16 v[160:175], v[128:131], v[2:5], 0
	v_mfma_f32_32x32x16_bf16 v[160:175], v[132:135], v[6:9], v[160:175]
	v_mfma_f32_32x32x16_bf16 v[160:175], v[136:139], v[10:13], v[160:175]
	v_mfma_f32_32x32x16_bf16 v[160:175], v[140:143], v[14:17], v[160:175]
	v_cmp_le_i32_e32 vcc, 0x360, v59
	v_max_f32_e32 v204, 0, v176
	v_max_f32_e32 v208, 0, v177
	v_fma_f32 v201, v144, v204, 0
	v_max_f32_e32 v204, 0, v178
	v_fmac_f32_e32 v201, v145, v208
	v_max_f32_e32 v208, 0, v179
	v_fmac_f32_e32 v201, v146, v204
	v_max_f32_e32 v204, 0, v180
	v_fmac_f32_e32 v201, v147, v208
	v_max_f32_e32 v208, 0, v181
	v_fmac_f32_e32 v201, v148, v204
	v_max_f32_e32 v204, 0, v182
	v_fmac_f32_e32 v201, v149, v208
	v_max_f32_e32 v208, 0, v183
	v_fmac_f32_e32 v201, v150, v204
	v_max_f32_e32 v204, 0, v184
	v_fmac_f32_e32 v201, v151, v208
	v_max_f32_e32 v208, 0, v185
	v_fmac_f32_e32 v201, v152, v204
	v_max_f32_e32 v204, 0, v186
	v_fmac_f32_e32 v201, v153, v208
	v_max_f32_e32 v208, 0, v187
	v_fmac_f32_e32 v201, v154, v204
	v_max_f32_e32 v204, 0, v188
	v_fmac_f32_e32 v201, v155, v208
	v_max_f32_e32 v208, 0, v189
	v_fmac_f32_e32 v201, v156, v204
	v_max_f32_e32 v204, 0, v190
	v_fmac_f32_e32 v201, v157, v208
	v_max_f32_e32 v208, 0, v191
	v_fmac_f32_e32 v201, v158, v204
	v_fmac_f32_e32 v201, v159, v208
	v_cndmask_b32_e32 v201, v61, v201, vcc
	v_ashrrev_i32_e32 v207, 31, v201
	v_or_b32_e32 v207, 0x80000000, v207
	v_xor_b32_e32 v91, v201, v207
	s_cmp_le_u32 s15, 29
	s_cbranch_scc1 .Lidx_x29
	ds_read_b128 v[2:5], v57 offset:57344
	ds_read_b128 v[6:9], v57 offset:58368
	ds_read_b128 v[10:13], v57 offset:59392
	ds_read_b128 v[14:17], v57 offset:60416
	s_waitcnt lgkmcnt(4)
	v_mfma_f32_32x32x16_bf16 v[176:191], v[128:131], v[18:21], 0
	v_mfma_f32_32x32x16_bf16 v[176:191], v[132:135], v[22:25], v[176:191]
	v_mfma_f32_32x32x16_bf16 v[176:191], v[136:139], v[26:29], v[176:191]
	v_mfma_f32_32x32x16_bf16 v[176:191], v[140:143], v[30:33], v[176:191]
	v_cmp_le_i32_e32 vcc, 0x380, v59
	v_max_f32_e32 v204, 0, v160
	v_max_f32_e32 v208, 0, v161
	v_fma_f32 v201, v144, v204, 0
	v_max_f32_e32 v204, 0, v162
	v_fmac_f32_e32 v201, v145, v208
	v_max_f32_e32 v208, 0, v163
	v_fmac_f32_e32 v201, v146, v204
	v_max_f32_e32 v204, 0, v164
	v_fmac_f32_e32 v201, v147, v208
	v_max_f32_e32 v208, 0, v165
	v_fmac_f32_e32 v201, v148, v204
	v_max_f32_e32 v204, 0, v166
	v_fmac_f32_e32 v201, v149, v208
	v_max_f32_e32 v208, 0, v167
	v_fmac_f32_e32 v201, v150, v204
	v_max_f32_e32 v204, 0, v168
	v_fmac_f32_e32 v201, v151, v208
	v_max_f32_e32 v208, 0, v169
	v_fmac_f32_e32 v201, v152, v204
	v_max_f32_e32 v204, 0, v170
	v_fmac_f32_e32 v201, v153, v208
	v_max_f32_e32 v208, 0, v171
	v_fmac_f32_e32 v201, v154, v204
	v_max_f32_e32 v204, 0, v172
	v_fmac_f32_e32 v201, v155, v208
	v_max_f32_e32 v208, 0, v173
	v_fmac_f32_e32 v201, v156, v204
	v_max_f32_e32 v204, 0, v174
	v_fmac_f32_e32 v201, v157, v208
	v_max_f32_e32 v208, 0, v175
	v_fmac_f32_e32 v201, v158, v204
	v_fmac_f32_e32 v201, v159, v208
	v_cndmask_b32_e32 v201, v61, v201, vcc
	v_ashrrev_i32_e32 v207, 31, v201
	v_or_b32_e32 v207, 0x80000000, v207
	v_xor_b32_e32 v92, v201, v207
	s_cmp_le_u32 s15, 30
	s_cbranch_scc1 .Lidx_x30
	ds_read_b128 v[18:21], v57 offset:61440
	ds_read_b128 v[22:25], v57 offset:62464
	ds_read_b128 v[26:29], v57 offset:63488
	ds_read_b128 v[30:33], v57 offset:64512
	s_waitcnt lgkmcnt(4)
	v_mfma_f32_32x32x16_bf16 v[160:175], v[128:131], v[2:5], 0
	v_mfma_f32_32x32x16_bf16 v[160:175], v[132:135], v[6:9], v[160:175]
	v_mfma_f32_32x32x16_bf16 v[160:175], v[136:139], v[10:13], v[160:175]
	v_mfma_f32_32x32x16_bf16 v[160:175], v[140:143], v[14:17], v[160:175]
	v_cmp_le_i32_e32 vcc, 0x3a0, v59
	v_max_f32_e32 v204, 0, v176
	v_max_f32_e32 v208, 0, v177
	v_fma_f32 v201, v144, v204, 0
	v_max_f32_e32 v204, 0, v178
	v_fmac_f32_e32 v201, v145, v208
	v_max_f32_e32 v208, 0, v179
	v_fmac_f32_e32 v201, v146, v204
	v_max_f32_e32 v204, 0, v180
	v_fmac_f32_e32 v201, v147, v208
	v_max_f32_e32 v208, 0, v181
	v_fmac_f32_e32 v201, v148, v204
	v_max_f32_e32 v204, 0, v182
	v_fmac_f32_e32 v201, v149, v208
	v_max_f32_e32 v208, 0, v183
	v_fmac_f32_e32 v201, v150, v204
	v_max_f32_e32 v204, 0, v184
	v_fmac_f32_e32 v201, v151, v208
	v_max_f32_e32 v208, 0, v185
	v_fmac_f32_e32 v201, v152, v204
	v_max_f32_e32 v204, 0, v186
	v_fmac_f32_e32 v201, v153, v208
	v_max_f32_e32 v208, 0, v187
	v_fmac_f32_e32 v201, v154, v204
	v_max_f32_e32 v204, 0, v188
	v_fmac_f32_e32 v201, v155, v208
	v_max_f32_e32 v208, 0, v189
	v_fmac_f32_e32 v201, v156, v204
	v_max_f32_e32 v204, 0, v190
	v_fmac_f32_e32 v201, v157, v208
	v_max_f32_e32 v208, 0, v191
	v_fmac_f32_e32 v201, v158, v204
	v_fmac_f32_e32 v201, v159, v208
	v_cndmask_b32_e32 v201, v61, v201, vcc
	v_ashrrev_i32_e32 v207, 31, v201
	v_or_b32_e32 v207, 0x80000000, v207
	v_xor_b32_e32 v93, v201, v207
	s_cmp_le_u32 s15, 31
	s_cbranch_scc1 .Lidx_x31
	s_waitcnt lgkmcnt(0)
	v_mfma_f32_32x32x16_bf16 v[176:191], v[128:131], v[18:21], 0
	v_mfma_f32_32x32x16_bf16 v[176:191], v[132:135], v[22:25], v[176:191]
	v_mfma_f32_32x32x16_bf16 v[176:191], v[136:139], v[26:29], v[176:191]
	v_mfma_f32_32x32x16_bf16 v[176:191], v[140:143], v[30:33], v[176:191]
	v_cmp_le_i32_e32 vcc, 0x3c0, v59
	v_max_f32_e32 v204, 0, v160
	v_max_f32_e32 v208, 0, v161
	v_fma_f32 v201, v144, v204, 0
	v_max_f32_e32 v204, 0, v162
	v_fmac_f32_e32 v201, v145, v208
	v_max_f32_e32 v208, 0, v163
	v_fmac_f32_e32 v201, v146, v204
	v_max_f32_e32 v204, 0, v164
	v_fmac_f32_e32 v201, v147, v208
	v_max_f32_e32 v208, 0, v165
	v_fmac_f32_e32 v201, v148, v204
	v_max_f32_e32 v204, 0, v166
	v_fmac_f32_e32 v201, v149, v208
	v_max_f32_e32 v208, 0, v167
	v_fmac_f32_e32 v201, v150, v204
	v_max_f32_e32 v204, 0, v168
	v_fmac_f32_e32 v201, v151, v208
	v_max_f32_e32 v208, 0, v169
	v_fmac_f32_e32 v201, v152, v204
	v_max_f32_e32 v204, 0, v170
	v_fmac_f32_e32 v201, v153, v208
	v_max_f32_e32 v208, 0, v171
	v_fmac_f32_e32 v201, v154, v204
	v_max_f32_e32 v204, 0, v172
	v_fmac_f32_e32 v201, v155, v208
	v_max_f32_e32 v208, 0, v173
	v_fmac_f32_e32 v201, v156, v204
	v_max_f32_e32 v204, 0, v174
	v_fmac_f32_e32 v201, v157, v208
	v_max_f32_e32 v208, 0, v175
	v_fmac_f32_e32 v201, v158, v204
	v_fmac_f32_e32 v201, v159, v208
	v_cndmask_b32_e32 v201, v61, v201, vcc
	v_ashrrev_i32_e32 v207, 31, v201
	v_or_b32_e32 v207, 0x80000000, v207
	v_xor_b32_e32 v94, v201, v207
.Lidx_ce3:
.Lidx_c4:
	s_cmp_le_u32 s29, 4
	s_cbranch_scc1 .Lidx_fin4
	s_waitcnt vmcnt(0) lgkmcnt(0)
	s_barrier
	s_cmp_le_u32 s29, 5
	s_cbranch_scc1 .Lidx_nd4
	s_mov_b32 m0, s31
	s_nop 0
	global_load_lds_dwordx4 v57, s[20:21]
	global_load_lds_dwordx4 v57, s[20:21] offset:1024
	global_load_lds_dwordx4 v57, s[20:21] offset:2048
	global_load_lds_dwordx4 v57, s[20:21] offset:3072
	s_add_u32 s20, s20, 0x8000
	s_addc_u32 s21, s21, 0
.Lidx_nd4:
	s_cmp_lt_u32 s15, 32
	s_cbranch_scc1 .Lidx_ce4
	s_cmp_le_u32 s15, 32
	s_cbranch_scc1 .Lidx_x32
	ds_read_b128 v[2:5], v57 offset:0
	ds_read_b128 v[6:9], v57 offset:1024
	ds_read_b128 v[10:13], v57 offset:2048
	ds_read_b128 v[14:17], v57 offset:3072
	ds_read_b128 v[18:21], v57 offset:4096
	ds_read_b128 v[22:25], v57 offset:5120
	ds_read_b128 v[26:29], v57 offset:6144
	ds_read_b128 v[30:33], v57 offset:7168
	s_waitcnt lgkmcnt(4)
	v_mfma_f32_32x32x16_bf16 v[160:175], v[128:131], v[2:5], 0
	v_mfma_f32_32x32x16_bf16 v[160:175], v[132:135], v[6:9], v[160:175]
	v_mfma_f32_32x32x16_bf16 v[160:175], v[136:139], v[10:13], v[160:175]
	v_mfma_f32_32x32x16_bf16 v[160:175], v[140:143], v[14:17], v[160:175]
	v_cmp_le_i32_e32 vcc, 0x3e0, v59
	v_max_f32_e32 v204, 0, v176
	v_max_f32_e32 v208, 0, v177
	v_fma_f32 v201, v144, v204, 0
	v_max_f32_e32 v204, 0, v178
	v_fmac_f32_e32 v201, v145, v208
	v_max_f32_e32 v208, 0, v179
	v_fmac_f32_e32 v201, v146, v204
	v_max_f32_e32 v204, 0, v180
	v_fmac_f32_e32 v201, v147, v208
	v_max_f32_e32 v208, 0, v181
	v_fmac_f32_e32 v201, v148, v204
	v_max_f32_e32 v204, 0, v182
	v_fmac_f32_e32 v201, v149, v208
	v_max_f32_e32 v208, 0, v183
	v_fmac_f32_e32 v201, v150, v204
	v_max_f32_e32 v204, 0, v184
	v_fmac_f32_e32 v201, v151, v208
	v_max_f32_e32 v208, 0, v185
	v_fmac_f32_e32 v201, v152, v204
	v_max_f32_e32 v204, 0, v186
	v_fmac_f32_e32 v201, v153, v208
	v_max_f32_e32 v208, 0, v187
	v_fmac_f32_e32 v201, v154, v204
	v_max_f32_e32 v204, 0, v188
	v_fmac_f32_e32 v201, v155, v208
	v_max_f32_e32 v208, 0, v189
	v_fmac_f32_e32 v201, v156, v204
	v_max_f32_e32 v204, 0, v190
	v_fmac_f32_e32 v201, v157, v208
	v_max_f32_e32 v208, 0, v191
	v_fmac_f32_e32 v201, v158, v204
	v_fmac_f32_e32 v201, v159, v208
	v_cndmask_b32_e32 v201, v61, v201, vcc
	v_ashrrev_i32_e32 v207, 31, v201
	v_or_b32_e32 v207, 0x80000000, v207
	v_xor_b32_e32 v95, v201, v207
	s_cmp_le_u32 s15, 33
	s_cbranch_scc1 .Lidx_x33
	ds_read_b128 v[2:5], v57 offset:8192
	ds_read_b128 v[6:9], v57 offset:9216
	ds_read_b128 v[10:13], v57 offset:10240
	ds_read_b128 v[14:17], v57 offset:11264
	s_waitcnt lgkmcnt(4)
	v_mfma_f32_32x32x16_bf16 v[176:191], v[128:131], v[18:21], 0
	v_mfma_f32_32x32x16_bf16 v[176:191], v[132:135], v[22:25], v[176:191]
	v_mfma_f32_32x32x16_bf16 v[176:191], v[136:139], v[26:29], v[176:191]
	v_mfma_f32_32x32x16_bf16 v[176:191], v[140:143], v[30:33], v[176:191]
	v_cmp_le_i32_e32 vcc, 0x400, v59
	v_max_f32_e32 v204, 0, v160
	v_max_f32_e32 v208, 0, v161
	v_fma_f32 v201, v144, v204, 0
	v_max_f32_e32 v204, 0, v162
	v_fmac_f32_e32 v201, v145, v208
	v_max_f32_e32 v208, 0, v163
	v_fmac_f32_e32 v201, v146, v204
	v_max_f32_e32 v204, 0, v164
	v_fmac_f32_e32 v201, v147, v208
	v_max_f32_e32 v208, 0, v165
	v_fmac_f32_e32 v201, v148, v204
	v_max_f32_e32 v204, 0, v166
	v_fmac_f32_e32 v201, v149, v208
	v_max_f32_e32 v208, 0, v167
	v_fmac_f32_e32 v201, v150, v204
	v_max_f32_e32 v204, 0, v168
	v_fmac_f32_e32 v201, v151, v208
	v_max_f32_e32 v208, 0, v169
	v_fmac_f32_e32 v201, v152, v204
	v_max_f32_e32 v204, 0, v170
	v_fmac_f32_e32 v201, v153, v208
	v_max_f32_e32 v208, 0, v171
	v_fmac_f32_e32 v201, v154, v204
	v_max_f32_e32 v204, 0, v172
	v_fmac_f32_e32 v201, v155, v208
	v_max_f32_e32 v208, 0, v173
	v_fmac_f32_e32 v201, v156, v204
	v_max_f32_e32 v204, 0, v174
	v_fmac_f32_e32 v201, v157, v208
	v_max_f32_e32 v208, 0, v175
	v_fmac_f32_e32 v201, v158, v204
	v_fmac_f32_e32 v201, v159, v208
	v_cndmask_b32_e32 v201, v61, v201, vcc
	v_ashrrev_i32_e32 v207, 31, v201
	v_or_b32_e32 v207, 0x80000000, v207
	v_xor_b32_e32 v96, v201, v207
	s_cmp_le_u32 s15, 34
	s_cbranch_scc1 .Lidx_x34
	ds_read_b128 v[18:21], v57 offset:12288
	ds_read_b128 v[22:25], v57 offset:13312
	ds_read_b128 v[26:29], v57 offset:14336
	ds_read_b128 v[30:33], v57 offset:15360
	s_waitcnt lgkmcnt(4)
	v_mfma_f32_32x32x16_bf16 v[160:175], v[128:131], v[2:5], 0
	v_mfma_f32_32x32x16_bf16 v[160:175], v[132:135], v[6:9], v[160:175]
	v_mfma_f32_32x32x16_bf16 v[160:175], v[136:139], v[10:13], v[160:175]
	v_mfma_f32_32x32x16_bf16 v[160:175], v[140:143], v[14:17], v[160:175]
	v_cmp_le_i32_e32 vcc, 0x420, v59
	v_max_f32_e32 v204, 0, v176
	v_max_f32_e32 v208, 0, v177
	v_fma_f32 v201, v144, v204, 0
	v_max_f32_e32 v204, 0, v178
	v_fmac_f32_e32 v201, v145, v208
	v_max_f32_e32 v208, 0, v179
	v_fmac_f32_e32 v201, v146, v204
	v_max_f32_e32 v204, 0, v180
	v_fmac_f32_e32 v201, v147, v208
	v_max_f32_e32 v208, 0, v181
	v_fmac_f32_e32 v201, v148, v204
	v_max_f32_e32 v204, 0, v182
	v_fmac_f32_e32 v201, v149, v208
	v_max_f32_e32 v208, 0, v183
	v_fmac_f32_e32 v201, v150, v204
	v_max_f32_e32 v204, 0, v184
	v_fmac_f32_e32 v201, v151, v208
	v_max_f32_e32 v208, 0, v185
	v_fmac_f32_e32 v201, v152, v204
	v_max_f32_e32 v204, 0, v186
	v_fmac_f32_e32 v201, v153, v208
	v_max_f32_e32 v208, 0, v187
	v_fmac_f32_e32 v201, v154, v204
	v_max_f32_e32 v204, 0, v188
	v_fmac_f32_e32 v201, v155, v208
	v_max_f32_e32 v208, 0, v189
	v_fmac_f32_e32 v201, v156, v204
	v_max_f32_e32 v204, 0, v190
	v_fmac_f32_e32 v201, v157, v208
	v_max_f32_e32 v208, 0, v191
	v_fmac_f32_e32 v201, v158, v204
	v_fmac_f32_e32 v201, v159, v208
	v_cndmask_b32_e32 v201, v61, v201, vcc
	v_ashrrev_i32_e32 v207, 31, v201
	v_or_b32_e32 v207, 0x80000000, v207
	v_xor_b32_e32 v97, v201, v207
	s_cmp_le_u32 s15, 35
	s_cbranch_scc1 .Lidx_x35
	ds_read_b128 v[2:5], v57 offset:16384
	ds_read_b128 v[6:9], v57 offset:17408
	ds_read_b128 v[10:13], v57 offset:18432
	ds_read_b128 v[14:17], v57 offset:19456
	s_waitcnt lgkmcnt(4)
	v_mfma_f32_32x32x16_bf16 v[176:191], v[128:131], v[18:21], 0
	v_mfma_f32_32x32x16_bf16 v[176:191], v[132:135], v[22:25], v[176:191]
	v_mfma_f32_32x32x16_bf16 v[176:191], v[136:139], v[26:29], v[176:191]
	v_mfma_f32_32x32x16_bf16 v[176:191], v[140:143], v[30:33], v[176:191]
	v_cmp_le_i32_e32 vcc, 0x440, v59
	v_max_f32_e32 v204, 0, v160
	v_max_f32_e32 v208, 0, v161
	v_fma_f32 v201, v144, v204, 0
	v_max_f32_e32 v204, 0, v162
	v_fmac_f32_e32 v201, v145, v208
	v_max_f32_e32 v208, 0, v163
	v_fmac_f32_e32 v201, v146, v204
	v_max_f32_e32 v204, 0, v164
	v_fmac_f32_e32 v201, v147, v208
	v_max_f32_e32 v208, 0, v165
	v_fmac_f32_e32 v201, v148, v204
	v_max_f32_e32 v204, 0, v166
	v_fmac_f32_e32 v201, v149, v208
	v_max_f32_e32 v208, 0, v167
	v_fmac_f32_e32 v201, v150, v204
	v_max_f32_e32 v204, 0, v168
	v_fmac_f32_e32 v201, v151, v208
	v_max_f32_e32 v208, 0, v169
	v_fmac_f32_e32 v201, v152, v204
	v_max_f32_e32 v204, 0, v170
	v_fmac_f32_e32 v201, v153, v208
	v_max_f32_e32 v208, 0, v171
	v_fmac_f32_e32 v201, v154, v204
	v_max_f32_e32 v204, 0, v172
	v_fmac_f32_e32 v201, v155, v208
	v_max_f32_e32 v208, 0, v173
	v_fmac_f32_e32 v201, v156, v204
	v_max_f32_e32 v204, 0, v174
	v_fmac_f32_e32 v201, v157, v208
	v_max_f32_e32 v208, 0, v175
	v_fmac_f32_e32 v201, v158, v204
	v_fmac_f32_e32 v201, v159, v208
	v_cndmask_b32_e32 v201, v61, v201, vcc
	v_ashrrev_i32_e32 v207, 31, v201
	v_or_b32_e32 v207, 0x80000000, v207
	v_xor_b32_e32 v98, v201, v207
	s_cmp_le_u32 s15, 36
	s_cbranch_scc1 .Lidx_x36
	ds_read_b128 v[18:21], v57 offset:20480
	ds_read_b128 v[22:25], v57 offset:21504
	ds_read_b128 v[26:29], v57 offset:22528
	ds_read_b128 v[30:33], v57 offset:23552
	s_waitcnt lgkmcnt(4)
	v_mfma_f32_32x32x16_bf16 v[160:175], v[128:131], v[2:5], 0
	v_mfma_f32_32x32x16_bf16 v[160:175], v[132:135], v[6:9], v[160:175]
	v_mfma_f32_32x32x16_bf16 v[160:175], v[136:139], v[10:13], v[160:175]
	v_mfma_f32_32x32x16_bf16 v[160:175], v[140:143], v[14:17], v[160:175]
	v_cmp_le_i32_e32 vcc, 0x460, v59
	v_max_f32_e32 v204, 0, v176
	v_max_f32_e32 v208, 0, v177
	v_fma_f32 v201, v144, v204, 0
	v_max_f32_e32 v204, 0, v178
	v_fmac_f32_e32 v201, v145, v208
	v_max_f32_e32 v208, 0, v179
	v_fmac_f32_e32 v201, v146, v204
	v_max_f32_e32 v204, 0, v180
	v_fmac_f32_e32 v201, v147, v208
	v_max_f32_e32 v208, 0, v181
	v_fmac_f32_e32 v201, v148, v204
	v_max_f32_e32 v204, 0, v182
	v_fmac_f32_e32 v201, v149, v208
	v_max_f32_e32 v208, 0, v183
	v_fmac_f32_e32 v201, v150, v204
	v_max_f32_e32 v204, 0, v184
	v_fmac_f32_e32 v201, v151, v208
	v_max_f32_e32 v208, 0, v185
	v_fmac_f32_e32 v201, v152, v204
	v_max_f32_e32 v204, 0, v186
	v_fmac_f32_e32 v201, v153, v208
	v_max_f32_e32 v208, 0, v187
	v_fmac_f32_e32 v201, v154, v204
	v_max_f32_e32 v204, 0, v188
	v_fmac_f32_e32 v201, v155, v208
	v_max_f32_e32 v208, 0, v189
	v_fmac_f32_e32 v201, v156, v204
	v_max_f32_e32 v204, 0, v190
	v_fmac_f32_e32 v201, v157, v208
	v_max_f32_e32 v208, 0, v191
	v_fmac_f32_e32 v201, v158, v204
	v_fmac_f32_e32 v201, v159, v208
	v_cndmask_b32_e32 v201, v61, v201, vcc
	v_ashrrev_i32_e32 v207, 31, v201
	v_or_b32_e32 v207, 0x80000000, v207
	v_xor_b32_e32 v99, v201, v207
	s_cmp_le_u32 s15, 37
	s_cbranch_scc1 .Lidx_x37
	ds_read_b128 v[2:5], v57 offset:24576
	ds_read_b128 v[6:9], v57 offset:25600
	ds_read_b128 v[10:13], v57 offset:26624
	ds_read_b128 v[14:17], v57 offset:27648
	s_waitcnt lgkmcnt(4)
	v_mfma_f32_32x32x16_bf16 v[176:191], v[128:131], v[18:21], 0
	v_mfma_f32_32x32x16_bf16 v[176:191], v[132:135], v[22:25], v[176:191]
	v_mfma_f32_32x32x16_bf16 v[176:191], v[136:139], v[26:29], v[176:191]
	v_mfma_f32_32x32x16_bf16 v[176:191], v[140:143], v[30:33], v[176:191]
	v_cmp_le_i32_e32 vcc, 0x480, v59
	v_max_f32_e32 v204, 0, v160
	v_max_f32_e32 v208, 0, v161
	v_fma_f32 v201, v144, v204, 0
	v_max_f32_e32 v204, 0, v162
	v_fmac_f32_e32 v201, v145, v208
	v_max_f32_e32 v208, 0, v163
	v_fmac_f32_e32 v201, v146, v204
	v_max_f32_e32 v204, 0, v164
	v_fmac_f32_e32 v201, v147, v208
	v_max_f32_e32 v208, 0, v165
	v_fmac_f32_e32 v201, v148, v204
	v_max_f32_e32 v204, 0, v166
	v_fmac_f32_e32 v201, v149, v208
	v_max_f32_e32 v208, 0, v167
	v_fmac_f32_e32 v201, v150, v204
	v_max_f32_e32 v204, 0, v168
	v_fmac_f32_e32 v201, v151, v208
	v_max_f32_e32 v208, 0, v169
	v_fmac_f32_e32 v201, v152, v204
	v_max_f32_e32 v204, 0, v170
	v_fmac_f32_e32 v201, v153, v208
	v_max_f32_e32 v208, 0, v171
	v_fmac_f32_e32 v201, v154, v204
	v_max_f32_e32 v204, 0, v172
	v_fmac_f32_e32 v201, v155, v208
	v_max_f32_e32 v208, 0, v173
	v_fmac_f32_e32 v201, v156, v204
	v_max_f32_e32 v204, 0, v174
	v_fmac_f32_e32 v201, v157, v208
	v_max_f32_e32 v208, 0, v175
	v_fmac_f32_e32 v201, v158, v204
	v_fmac_f32_e32 v201, v159, v208
	v_cndmask_b32_e32 v201, v61, v201, vcc
	v_ashrrev_i32_e32 v207, 31, v201
	v_or_b32_e32 v207, 0x80000000, v207
	v_xor_b32_e32 v100, v201, v207
	s_cmp_le_u32 s15, 38
	s_cbranch_scc1 .Lidx_x38
	ds_read_b128 v[18:21], v57 offset:28672
	ds_read_b128 v[22:25], v57 offset:29696
	ds_read_b128 v[26:29], v57 offset:30720
	ds_read_b128 v[30:33], v57 offset:31744
	s_waitcnt lgkmcnt(4)
	v_mfma_f32_32x32x16_bf16 v[160:175], v[128:131], v[2:5], 0
	v_mfma_f32_32x32x16_bf16 v[160:175], v[132:135], v[6:9], v[160:175]
	v_mfma_f32_32x32x16_bf16 v[160:175], v[136:139], v[10:13], v[160:175]
	v_mfma_f32_32x32x16_bf16 v[160:175], v[140:143], v[14:17], v[160:175]
	v_cmp_le_i32_e32 vcc, 0x4a0, v59
	v_max_f32_e32 v204, 0, v176
	v_max_f32_e32 v208, 0, v177
	v_fma_f32 v201, v144, v204, 0
	v_max_f32_e32 v204, 0, v178
	v_fmac_f32_e32 v201, v145, v208
	v_max_f32_e32 v208, 0, v179
	v_fmac_f32_e32 v201, v146, v204
	v_max_f32_e32 v204, 0, v180
	v_fmac_f32_e32 v201, v147, v208
	v_max_f32_e32 v208, 0, v181
	v_fmac_f32_e32 v201, v148, v204
	v_max_f32_e32 v204, 0, v182
	v_fmac_f32_e32 v201, v149, v208
	v_max_f32_e32 v208, 0, v183
	v_fmac_f32_e32 v201, v150, v204
	v_max_f32_e32 v204, 0, v184
	v_fmac_f32_e32 v201, v151, v208
	v_max_f32_e32 v208, 0, v185
	v_fmac_f32_e32 v201, v152, v204
	v_max_f32_e32 v204, 0, v186
	v_fmac_f32_e32 v201, v153, v208
	v_max_f32_e32 v208, 0, v187
	v_fmac_f32_e32 v201, v154, v204
	v_max_f32_e32 v204, 0, v188
	v_fmac_f32_e32 v201, v155, v208
	v_max_f32_e32 v208, 0, v189
	v_fmac_f32_e32 v201, v156, v204
	v_max_f32_e32 v204, 0, v190
	v_fmac_f32_e32 v201, v157, v208
	v_max_f32_e32 v208, 0, v191
	v_fmac_f32_e32 v201, v158, v204
	v_fmac_f32_e32 v201, v159, v208
	v_cndmask_b32_e32 v201, v61, v201, vcc
	v_ashrrev_i32_e32 v207, 31, v201
	v_or_b32_e32 v207, 0x80000000, v207
	v_xor_b32_e32 v101, v201, v207
	s_cmp_le_u32 s15, 39
	s_cbranch_scc1 .Lidx_x39
	s_waitcnt lgkmcnt(0)
	v_mfma_f32_32x32x16_bf16 v[176:191], v[128:131], v[18:21], 0
	v_mfma_f32_32x32x16_bf16 v[176:191], v[132:135], v[22:25], v[176:191]
	v_mfma_f32_32x32x16_bf16 v[176:191], v[136:139], v[26:29], v[176:191]
	v_mfma_f32_32x32x16_bf16 v[176:191], v[140:143], v[30:33], v[176:191]
	v_cmp_le_i32_e32 vcc, 0x4c0, v59
	v_max_f32_e32 v204, 0, v160
	v_max_f32_e32 v208, 0, v161
	v_fma_f32 v201, v144, v204, 0
	v_max_f32_e32 v204, 0, v162
	v_fmac_f32_e32 v201, v145, v208
	v_max_f32_e32 v208, 0, v163
	v_fmac_f32_e32 v201, v146, v204
	v_max_f32_e32 v204, 0, v164
	v_fmac_f32_e32 v201, v147, v208
	v_max_f32_e32 v208, 0, v165
	v_fmac_f32_e32 v201, v148, v204
	v_max_f32_e32 v204, 0, v166
	v_fmac_f32_e32 v201, v149, v208
	v_max_f32_e32 v208, 0, v167
	v_fmac_f32_e32 v201, v150, v204
	v_max_f32_e32 v204, 0, v168
	v_fmac_f32_e32 v201, v151, v208
	v_max_f32_e32 v208, 0, v169
	v_fmac_f32_e32 v201, v152, v204
	v_max_f32_e32 v204, 0, v170
	v_fmac_f32_e32 v201, v153, v208
	v_max_f32_e32 v208, 0, v171
	v_fmac_f32_e32 v201, v154, v204
	v_max_f32_e32 v204, 0, v172
	v_fmac_f32_e32 v201, v155, v208
	v_max_f32_e32 v208, 0, v173
	v_fmac_f32_e32 v201, v156, v204
	v_max_f32_e32 v204, 0, v174
	v_fmac_f32_e32 v201, v157, v208
	v_max_f32_e32 v208, 0, v175
	v_fmac_f32_e32 v201, v158, v204
	v_fmac_f32_e32 v201, v159, v208
	v_cndmask_b32_e32 v201, v61, v201, vcc
	v_ashrrev_i32_e32 v207, 31, v201
	v_or_b32_e32 v207, 0x80000000, v207
	v_xor_b32_e32 v102, v201, v207
.Lidx_ce4:
.Lidx_c5:
	s_cmp_le_u32 s29, 5
	s_cbranch_scc1 .Lidx_fin5
	s_waitcnt vmcnt(0) lgkmcnt(0)
	s_barrier
	s_cmp_le_u32 s29, 6
	s_cbranch_scc1 .Lidx_nd5
	s_mov_b32 m0, s30
	s_nop 0
	global_load_lds_dwordx4 v57, s[20:21]
	global_load_lds_dwordx4 v57, s[20:21] offset:1024
	global_load_lds_dwordx4 v57, s[20:21] offset:2048
	global_load_lds_dwordx4 v57, s[20:21] offset:3072
	s_add_u32 s20, s20, 0x8000
	s_addc_u32 s21, s21, 0
.Lidx_nd5:
	s_cmp_lt_u32 s15, 40
	s_cbranch_scc1 .Lidx_ce5
	s_cmp_le_u32 s15, 40
	s_cbranch_scc1 .Lidx_x40
	ds_read_b128 v[2:5], v57 offset:32768
	ds_read_b128 v[6:9], v57 offset:33792
	ds_read_b128 v[10:13], v57 offset:34816
	ds_read_b128 v[14:17], v57 offset:35840
	ds_read_b128 v[18:21], v57 offset:36864
	ds_read_b128 v[22:25], v57 offset:37888
	ds_read_b128 v[26:29], v57 offset:38912
	ds_read_b128 v[30:33], v57 offset:39936
	s_waitcnt lgkmcnt(4)
	v_mfma_f32_32x32x16_bf16 v[160:175], v[128:131], v[2:5], 0
	v_mfma_f32_32x32x16_bf16 v[160:175], v[132:135], v[6:9], v[160:175]
	v_mfma_f32_32x32x16_bf16 v[160:175], v[136:139], v[10:13], v[160:175]
	v_mfma_f32_32x32x16_bf16 v[160:175], v[140:143], v[14:17], v[160:175]
	v_cmp_le_i32_e32 vcc, 0x4e0, v59
	v_max_f32_e32 v204, 0, v176
	v_max_f32_e32 v208, 0, v177
	v_fma_f32 v201, v144, v204, 0
	v_max_f32_e32 v204, 0, v178
	v_fmac_f32_e32 v201, v145, v208
	v_max_f32_e32 v208, 0, v179
	v_fmac_f32_e32 v201, v146, v204
	v_max_f32_e32 v204, 0, v180
	v_fmac_f32_e32 v201, v147, v208
	v_max_f32_e32 v208, 0, v181
	v_fmac_f32_e32 v201, v148, v204
	v_max_f32_e32 v204, 0, v182
	v_fmac_f32_e32 v201, v149, v208
	v_max_f32_e32 v208, 0, v183
	v_fmac_f32_e32 v201, v150, v204
	v_max_f32_e32 v204, 0, v184
	v_fmac_f32_e32 v201, v151, v208
	v_max_f32_e32 v208, 0, v185
	v_fmac_f32_e32 v201, v152, v204
	v_max_f32_e32 v204, 0, v186
	v_fmac_f32_e32 v201, v153, v208
	v_max_f32_e32 v208, 0, v187
	v_fmac_f32_e32 v201, v154, v204
	v_max_f32_e32 v204, 0, v188
	v_fmac_f32_e32 v201, v155, v208
	v_max_f32_e32 v208, 0, v189
	v_fmac_f32_e32 v201, v156, v204
	v_max_f32_e32 v204, 0, v190
	v_fmac_f32_e32 v201, v157, v208
	v_max_f32_e32 v208, 0, v191
	v_fmac_f32_e32 v201, v158, v204
	v_fmac_f32_e32 v201, v159, v208
	v_cndmask_b32_e32 v201, v61, v201, vcc
	v_ashrrev_i32_e32 v207, 31, v201
	v_or_b32_e32 v207, 0x80000000, v207
	v_xor_b32_e32 v103, v201, v207
	s_cmp_le_u32 s15, 41
	s_cbranch_scc1 .Lidx_x41
	ds_read_b128 v[2:5], v57 offset:40960
	ds_read_b128 v[6:9], v57 offset:41984
	ds_read_b128 v[10:13], v57 offset:43008
	ds_read_b128 v[14:17], v57 offset:44032
	s_waitcnt lgkmcnt(4)
	v_mfma_f32_32x32x16_bf16 v[176:191], v[128:131], v[18:21], 0
	v_mfma_f32_32x32x16_bf16 v[176:191], v[132:135], v[22:25], v[176:191]
	v_mfma_f32_32x32x16_bf16 v[176:191], v[136:139], v[26:29], v[176:191]
	v_mfma_f32_32x32x16_bf16 v[176:191], v[140:143], v[30:33], v[176:191]
	v_cmp_le_i32_e32 vcc, 0x500, v59
	v_max_f32_e32 v204, 0, v160
	v_max_f32_e32 v208, 0, v161
	v_fma_f32 v201, v144, v204, 0
	v_max_f32_e32 v204, 0, v162
	v_fmac_f32_e32 v201, v145, v208
	v_max_f32_e32 v208, 0, v163
	v_fmac_f32_e32 v201, v146, v204
	v_max_f32_e32 v204, 0, v164
	v_fmac_f32_e32 v201, v147, v208
	v_max_f32_e32 v208, 0, v165
	v_fmac_f32_e32 v201, v148, v204
	v_max_f32_e32 v204, 0, v166
	v_fmac_f32_e32 v201, v149, v208
	v_max_f32_e32 v208, 0, v167
	v_fmac_f32_e32 v201, v150, v204
	v_max_f32_e32 v204, 0, v168
	v_fmac_f32_e32 v201, v151, v208
	v_max_f32_e32 v208, 0, v169
	v_fmac_f32_e32 v201, v152, v204
	v_max_f32_e32 v204, 0, v170
	v_fmac_f32_e32 v201, v153, v208
	v_max_f32_e32 v208, 0, v171
	v_fmac_f32_e32 v201, v154, v204
	v_max_f32_e32 v204, 0, v172
	v_fmac_f32_e32 v201, v155, v208
	v_max_f32_e32 v208, 0, v173
	v_fmac_f32_e32 v201, v156, v204
	v_max_f32_e32 v204, 0, v174
	v_fmac_f32_e32 v201, v157, v208
	v_max_f32_e32 v208, 0, v175
	v_fmac_f32_e32 v201, v158, v204
	v_fmac_f32_e32 v201, v159, v208
	v_cndmask_b32_e32 v201, v61, v201, vcc
	v_ashrrev_i32_e32 v207, 31, v201
	v_or_b32_e32 v207, 0x80000000, v207
	v_xor_b32_e32 v104, v201, v207
	s_cmp_le_u32 s15, 42
	s_cbranch_scc1 .Lidx_x42
	ds_read_b128 v[18:21], v57 offset:45056
	ds_read_b128 v[22:25], v57 offset:46080
	ds_read_b128 v[26:29], v57 offset:47104
	ds_read_b128 v[30:33], v57 offset:48128
	s_waitcnt lgkmcnt(4)
	v_mfma_f32_32x32x16_bf16 v[160:175], v[128:131], v[2:5], 0
	v_mfma_f32_32x32x16_bf16 v[160:175], v[132:135], v[6:9], v[160:175]
	v_mfma_f32_32x32x16_bf16 v[160:175], v[136:139], v[10:13], v[160:175]
	v_mfma_f32_32x32x16_bf16 v[160:175], v[140:143], v[14:17], v[160:175]
	v_cmp_le_i32_e32 vcc, 0x520, v59
	v_max_f32_e32 v204, 0, v176
	v_max_f32_e32 v208, 0, v177
	v_fma_f32 v201, v144, v204, 0
	v_max_f32_e32 v204, 0, v178
	v_fmac_f32_e32 v201, v145, v208
	v_max_f32_e32 v208, 0, v179
	v_fmac_f32_e32 v201, v146, v204
	v_max_f32_e32 v204, 0, v180
	v_fmac_f32_e32 v201, v147, v208
	v_max_f32_e32 v208, 0, v181
	v_fmac_f32_e32 v201, v148, v204
	v_max_f32_e32 v204, 0, v182
	v_fmac_f32_e32 v201, v149, v208
	v_max_f32_e32 v208, 0, v183
	v_fmac_f32_e32 v201, v150, v204
	v_max_f32_e32 v204, 0, v184
	v_fmac_f32_e32 v201, v151, v208
	v_max_f32_e32 v208, 0, v185
	v_fmac_f32_e32 v201, v152, v204
	v_max_f32_e32 v204, 0, v186
	v_fmac_f32_e32 v201, v153, v208
	v_max_f32_e32 v208, 0, v187
	v_fmac_f32_e32 v201, v154, v204
	v_max_f32_e32 v204, 0, v188
	v_fmac_f32_e32 v201, v155, v208
	v_max_f32_e32 v208, 0, v189
	v_fmac_f32_e32 v201, v156, v204
	v_max_f32_e32 v204, 0, v190
	v_fmac_f32_e32 v201, v157, v208
	v_max_f32_e32 v208, 0, v191
	v_fmac_f32_e32 v201, v158, v204
	v_fmac_f32_e32 v201, v159, v208
	v_cndmask_b32_e32 v201, v61, v201, vcc
	v_ashrrev_i32_e32 v207, 31, v201
	v_or_b32_e32 v207, 0x80000000, v207
	v_xor_b32_e32 v105, v201, v207
	s_cmp_le_u32 s15, 43
	s_cbranch_scc1 .Lidx_x43
	ds_read_b128 v[2:5], v57 offset:49152
	ds_read_b128 v[6:9], v57 offset:50176
	ds_read_b128 v[10:13], v57 offset:51200
	ds_read_b128 v[14:17], v57 offset:52224
	s_waitcnt lgkmcnt(4)
	v_mfma_f32_32x32x16_bf16 v[176:191], v[128:131], v[18:21], 0
	v_mfma_f32_32x32x16_bf16 v[176:191], v[132:135], v[22:25], v[176:191]
	v_mfma_f32_32x32x16_bf16 v[176:191], v[136:139], v[26:29], v[176:191]
	v_mfma_f32_32x32x16_bf16 v[176:191], v[140:143], v[30:33], v[176:191]
	v_cmp_le_i32_e32 vcc, 0x540, v59
	v_max_f32_e32 v204, 0, v160
	v_max_f32_e32 v208, 0, v161
	v_fma_f32 v201, v144, v204, 0
	v_max_f32_e32 v204, 0, v162
	v_fmac_f32_e32 v201, v145, v208
	v_max_f32_e32 v208, 0, v163
	v_fmac_f32_e32 v201, v146, v204
	v_max_f32_e32 v204, 0, v164
	v_fmac_f32_e32 v201, v147, v208
	v_max_f32_e32 v208, 0, v165
	v_fmac_f32_e32 v201, v148, v204
	v_max_f32_e32 v204, 0, v166
	v_fmac_f32_e32 v201, v149, v208
	v_max_f32_e32 v208, 0, v167
	v_fmac_f32_e32 v201, v150, v204
	v_max_f32_e32 v204, 0, v168
	v_fmac_f32_e32 v201, v151, v208
	v_max_f32_e32 v208, 0, v169
	v_fmac_f32_e32 v201, v152, v204
	v_max_f32_e32 v204, 0, v170
	v_fmac_f32_e32 v201, v153, v208
	v_max_f32_e32 v208, 0, v171
	v_fmac_f32_e32 v201, v154, v204
	v_max_f32_e32 v204, 0, v172
	v_fmac_f32_e32 v201, v155, v208
	v_max_f32_e32 v208, 0, v173
	v_fmac_f32_e32 v201, v156, v204
	v_max_f32_e32 v204, 0, v174
	v_fmac_f32_e32 v201, v157, v208
	v_max_f32_e32 v208, 0, v175
	v_fmac_f32_e32 v201, v158, v204
	v_fmac_f32_e32 v201, v159, v208
	v_cndmask_b32_e32 v201, v61, v201, vcc
	v_ashrrev_i32_e32 v207, 31, v201
	v_or_b32_e32 v207, 0x80000000, v207
	v_xor_b32_e32 v106, v201, v207
	s_cmp_le_u32 s15, 44
	s_cbranch_scc1 .Lidx_x44
	ds_read_b128 v[18:21], v57 offset:53248
	ds_read_b128 v[22:25], v57 offset:54272
	ds_read_b128 v[26:29], v57 offset:55296
	ds_read_b128 v[30:33], v57 offset:56320
	s_waitcnt lgkmcnt(4)
	v_mfma_f32_32x32x16_bf16 v[160:175], v[128:131], v[2:5], 0
	v_mfma_f32_32x32x16_bf16 v[160:175], v[132:135], v[6:9], v[160:175]
	v_mfma_f32_32x32x16_bf16 v[160:175], v[136:139], v[10:13], v[160:175]
	v_mfma_f32_32x32x16_bf16 v[160:175], v[140:143], v[14:17], v[160:175]
	v_cmp_le_i32_e32 vcc, 0x560, v59
	v_max_f32_e32 v204, 0, v176
	v_max_f32_e32 v208, 0, v177
	v_fma_f32 v201, v144, v204, 0
	v_max_f32_e32 v204, 0, v178
	v_fmac_f32_e32 v201, v145, v208
	v_max_f32_e32 v208, 0, v179
	v_fmac_f32_e32 v201, v146, v204
	v_max_f32_e32 v204, 0, v180
	v_fmac_f32_e32 v201, v147, v208
	v_max_f32_e32 v208, 0, v181
	v_fmac_f32_e32 v201, v148, v204
	v_max_f32_e32 v204, 0, v182
	v_fmac_f32_e32 v201, v149, v208
	v_max_f32_e32 v208, 0, v183
	v_fmac_f32_e32 v201, v150, v204
	v_max_f32_e32 v204, 0, v184
	v_fmac_f32_e32 v201, v151, v208
	v_max_f32_e32 v208, 0, v185
	v_fmac_f32_e32 v201, v152, v204
	v_max_f32_e32 v204, 0, v186
	v_fmac_f32_e32 v201, v153, v208
	v_max_f32_e32 v208, 0, v187
	v_fmac_f32_e32 v201, v154, v204
	v_max_f32_e32 v204, 0, v188
	v_fmac_f32_e32 v201, v155, v208
	v_max_f32_e32 v208, 0, v189
	v_fmac_f32_e32 v201, v156, v204
	v_max_f32_e32 v204, 0, v190
	v_fmac_f32_e32 v201, v157, v208
	v_max_f32_e32 v208, 0, v191
	v_fmac_f32_e32 v201, v158, v204
	v_fmac_f32_e32 v201, v159, v208
	v_cndmask_b32_e32 v201, v61, v201, vcc
	v_ashrrev_i32_e32 v207, 31, v201
	v_or_b32_e32 v207, 0x80000000, v207
	v_xor_b32_e32 v107, v201, v207
	s_cmp_le_u32 s15, 45
	s_cbranch_scc1 .Lidx_x45
	ds_read_b128 v[2:5], v57 offset:57344
	ds_read_b128 v[6:9], v57 offset:58368
	ds_read_b128 v[10:13], v57 offset:59392
	ds_read_b128 v[14:17], v57 offset:60416
	s_waitcnt lgkmcnt(4)
	v_mfma_f32_32x32x16_bf16 v[176:191], v[128:131], v[18:21], 0
	v_mfma_f32_32x32x16_bf16 v[176:191], v[132:135], v[22:25], v[176:191]
	v_mfma_f32_32x32x16_bf16 v[176:191], v[136:139], v[26:29], v[176:191]
	v_mfma_f32_32x32x16_bf16 v[176:191], v[140:143], v[30:33], v[176:191]
	v_cmp_le_i32_e32 vcc, 0x580, v59
	v_max_f32_e32 v204, 0, v160
	v_max_f32_e32 v208, 0, v161
	v_fma_f32 v201, v144, v204, 0
	v_max_f32_e32 v204, 0, v162
	v_fmac_f32_e32 v201, v145, v208
	v_max_f32_e32 v208, 0, v163
	v_fmac_f32_e32 v201, v146, v204
	v_max_f32_e32 v204, 0, v164
	v_fmac_f32_e32 v201, v147, v208
	v_max_f32_e32 v208, 0, v165
	v_fmac_f32_e32 v201, v148, v204
	v_max_f32_e32 v204, 0, v166
	v_fmac_f32_e32 v201, v149, v208
	v_max_f32_e32 v208, 0, v167
	v_fmac_f32_e32 v201, v150, v204
	v_max_f32_e32 v204, 0, v168
	v_fmac_f32_e32 v201, v151, v208
	v_max_f32_e32 v208, 0, v169
	v_fmac_f32_e32 v201, v152, v204
	v_max_f32_e32 v204, 0, v170
	v_fmac_f32_e32 v201, v153, v208
	v_max_f32_e32 v208, 0, v171
	v_fmac_f32_e32 v201, v154, v204
	v_max_f32_e32 v204, 0, v172
	v_fmac_f32_e32 v201, v155, v208
	v_max_f32_e32 v208, 0, v173
	v_fmac_f32_e32 v201, v156, v204
	v_max_f32_e32 v204, 0, v174
	v_fmac_f32_e32 v201, v157, v208
	v_max_f32_e32 v208, 0, v175
	v_fmac_f32_e32 v201, v158, v204
	v_fmac_f32_e32 v201, v159, v208
	v_cndmask_b32_e32 v201, v61, v201, vcc
	v_ashrrev_i32_e32 v207, 31, v201
	v_or_b32_e32 v207, 0x80000000, v207
	v_xor_b32_e32 v108, v201, v207
	s_cmp_le_u32 s15, 46
	s_cbranch_scc1 .Lidx_x46
	ds_read_b128 v[18:21], v57 offset:61440
	ds_read_b128 v[22:25], v57 offset:62464
	ds_read_b128 v[26:29], v57 offset:63488
	ds_read_b128 v[30:33], v57 offset:64512
	s_waitcnt lgkmcnt(4)
	v_mfma_f32_32x32x16_bf16 v[160:175], v[128:131], v[2:5], 0
	v_mfma_f32_32x32x16_bf16 v[160:175], v[132:135], v[6:9], v[160:175]
	v_mfma_f32_32x32x16_bf16 v[160:175], v[136:139], v[10:13], v[160:175]
	v_mfma_f32_32x32x16_bf16 v[160:175], v[140:143], v[14:17], v[160:175]
	v_cmp_le_i32_e32 vcc, 0x5a0, v59
	v_max_f32_e32 v204, 0, v176
	v_max_f32_e32 v208, 0, v177
	v_fma_f32 v201, v144, v204, 0
	v_max_f32_e32 v204, 0, v178
	v_fmac_f32_e32 v201, v145, v208
	v_max_f32_e32 v208, 0, v179
	v_fmac_f32_e32 v201, v146, v204
	v_max_f32_e32 v204, 0, v180
	v_fmac_f32_e32 v201, v147, v208
	v_max_f32_e32 v208, 0, v181
	v_fmac_f32_e32 v201, v148, v204
	v_max_f32_e32 v204, 0, v182
	v_fmac_f32_e32 v201, v149, v208
	v_max_f32_e32 v208, 0, v183
	v_fmac_f32_e32 v201, v150, v204
	v_max_f32_e32 v204, 0, v184
	v_fmac_f32_e32 v201, v151, v208
	v_max_f32_e32 v208, 0, v185
	v_fmac_f32_e32 v201, v152, v204
	v_max_f32_e32 v204, 0, v186
	v_fmac_f32_e32 v201, v153, v208
	v_max_f32_e32 v208, 0, v187
	v_fmac_f32_e32 v201, v154, v204
	v_max_f32_e32 v204, 0, v188
	v_fmac_f32_e32 v201, v155, v208
	v_max_f32_e32 v208, 0, v189
	v_fmac_f32_e32 v201, v156, v204
	v_max_f32_e32 v204, 0, v190
	v_fmac_f32_e32 v201, v157, v208
	v_max_f32_e32 v208, 0, v191
	v_fmac_f32_e32 v201, v158, v204
	v_fmac_f32_e32 v201, v159, v208
	v_cndmask_b32_e32 v201, v61, v201, vcc
	v_ashrrev_i32_e32 v207, 31, v201
	v_or_b32_e32 v207, 0x80000000, v207
	v_xor_b32_e32 v109, v201, v207
	s_cmp_le_u32 s15, 47
	s_cbranch_scc1 .Lidx_x47
	s_waitcnt lgkmcnt(0)
	v_mfma_f32_32x32x16_bf16 v[176:191], v[128:131], v[18:21], 0
	v_mfma_f32_32x32x16_bf16 v[176:191], v[132:135], v[22:25], v[176:191]
	v_mfma_f32_32x32x16_bf16 v[176:191], v[136:139], v[26:29], v[176:191]
	v_mfma_f32_32x32x16_bf16 v[176:191], v[140:143], v[30:33], v[176:191]
	v_cmp_le_i32_e32 vcc, 0x5c0, v59
	v_max_f32_e32 v204, 0, v160
	v_max_f32_e32 v208, 0, v161
	v_fma_f32 v201, v144, v204, 0
	v_max_f32_e32 v204, 0, v162
	v_fmac_f32_e32 v201, v145, v208
	v_max_f32_e32 v208, 0, v163
	v_fmac_f32_e32 v201, v146, v204
	v_max_f32_e32 v204, 0, v164
	v_fmac_f32_e32 v201, v147, v208
	v_max_f32_e32 v208, 0, v165
	v_fmac_f32_e32 v201, v148, v204
	v_max_f32_e32 v204, 0, v166
	v_fmac_f32_e32 v201, v149, v208
	v_max_f32_e32 v208, 0, v167
	v_fmac_f32_e32 v201, v150, v204
	v_max_f32_e32 v204, 0, v168
	v_fmac_f32_e32 v201, v151, v208
	v_max_f32_e32 v208, 0, v169
	v_fmac_f32_e32 v201, v152, v204
	v_max_f32_e32 v204, 0, v170
	v_fmac_f32_e32 v201, v153, v208
	v_max_f32_e32 v208, 0, v171
	v_fmac_f32_e32 v201, v154, v204
	v_max_f32_e32 v204, 0, v172
	v_fmac_f32_e32 v201, v155, v208
	v_max_f32_e32 v208, 0, v173
	v_fmac_f32_e32 v201, v156, v204
	v_max_f32_e32 v204, 0, v174
	v_fmac_f32_e32 v201, v157, v208
	v_max_f32_e32 v208, 0, v175
	v_fmac_f32_e32 v201, v158, v204
	v_fmac_f32_e32 v201, v159, v208
	v_cndmask_b32_e32 v201, v61, v201, vcc
	v_ashrrev_i32_e32 v207, 31, v201
	v_or_b32_e32 v207, 0x80000000, v207
	v_xor_b32_e32 v110, v201, v207
.Lidx_ce5:
.Lidx_c6:
	s_cmp_le_u32 s29, 6
	s_cbranch_scc1 .Lidx_fin6
	s_waitcnt vmcnt(0) lgkmcnt(0)
	s_barrier
	s_cmp_le_u32 s29, 7
	s_cbranch_scc1 .Lidx_nd6
	s_mov_b32 m0, s31
	s_nop 0
	global_load_lds_dwordx4 v57, s[20:21]
	global_load_lds_dwordx4 v57, s[20:21] offset:1024
	global_load_lds_dwordx4 v57, s[20:21] offset:2048
	global_load_lds_dwordx4 v57, s[20:21] offset:3072
	s_add_u32 s20, s20, 0x8000
	s_addc_u32 s21, s21, 0
.Lidx_nd6:
	s_cmp_lt_u32 s15, 48
	s_cbranch_scc1 .Lidx_ce6
	s_cmp_le_u32 s15, 48
	s_cbranch_scc1 .Lidx_x48
	ds_read_b128 v[2:5], v57 offset:0
	ds_read_b128 v[6:9], v57 offset:1024
	ds_read_b128 v[10:13], v57 offset:2048
	ds_read_b128 v[14:17], v57 offset:3072
	ds_read_b128 v[18:21], v57 offset:4096
	ds_read_b128 v[22:25], v57 offset:5120
	ds_read_b128 v[26:29], v57 offset:6144
	ds_read_b128 v[30:33], v57 offset:7168
	s_waitcnt lgkmcnt(4)
	v_mfma_f32_32x32x16_bf16 v[160:175], v[128:131], v[2:5], 0
	v_mfma_f32_32x32x16_bf16 v[160:175], v[132:135], v[6:9], v[160:175]
	v_mfma_f32_32x32x16_bf16 v[160:175], v[136:139], v[10:13], v[160:175]
	v_mfma_f32_32x32x16_bf16 v[160:175], v[140:143], v[14:17], v[160:175]
	v_cmp_le_i32_e32 vcc, 0x5e0, v59
	v_max_f32_e32 v204, 0, v176
	v_max_f32_e32 v208, 0, v177
	v_fma_f32 v201, v144, v204, 0
	v_max_f32_e32 v204, 0, v178
	v_fmac_f32_e32 v201, v145, v208
	v_max_f32_e32 v208, 0, v179
	v_fmac_f32_e32 v201, v146, v204
	v_max_f32_e32 v204, 0, v180
	v_fmac_f32_e32 v201, v147, v208
	v_max_f32_e32 v208, 0, v181
	v_fmac_f32_e32 v201, v148, v204
	v_max_f32_e32 v204, 0, v182
	v_fmac_f32_e32 v201, v149, v208
	v_max_f32_e32 v208, 0, v183
	v_fmac_f32_e32 v201, v150, v204
	v_max_f32_e32 v204, 0, v184
	v_fmac_f32_e32 v201, v151, v208
	v_max_f32_e32 v208, 0, v185
	v_fmac_f32_e32 v201, v152, v204
	v_max_f32_e32 v204, 0, v186
	v_fmac_f32_e32 v201, v153, v208
	v_max_f32_e32 v208, 0, v187
	v_fmac_f32_e32 v201, v154, v204
	v_max_f32_e32 v204, 0, v188
	v_fmac_f32_e32 v201, v155, v208
	v_max_f32_e32 v208, 0, v189
	v_fmac_f32_e32 v201, v156, v204
	v_max_f32_e32 v204, 0, v190
	v_fmac_f32_e32 v201, v157, v208
	v_max_f32_e32 v208, 0, v191
	v_fmac_f32_e32 v201, v158, v204
	v_fmac_f32_e32 v201, v159, v208
	v_cndmask_b32_e32 v201, v61, v201, vcc
	v_ashrrev_i32_e32 v207, 31, v201
	v_or_b32_e32 v207, 0x80000000, v207
	v_xor_b32_e32 v111, v201, v207
	s_cmp_le_u32 s15, 49
	s_cbranch_scc1 .Lidx_x49
	ds_read_b128 v[2:5], v57 offset:8192
	ds_read_b128 v[6:9], v57 offset:9216
	ds_read_b128 v[10:13], v57 offset:10240
	ds_read_b128 v[14:17], v57 offset:11264
	s_waitcnt lgkmcnt(4)
	v_mfma_f32_32x32x16_bf16 v[176:191], v[128:131], v[18:21], 0
	v_mfma_f32_32x32x16_bf16 v[176:191], v[132:135], v[22:25], v[176:191]
	v_mfma_f32_32x32x16_bf16 v[176:191], v[136:139], v[26:29], v[176:191]
	v_mfma_f32_32x32x16_bf16 v[176:191], v[140:143], v[30:33], v[176:191]
	v_cmp_le_i32_e32 vcc, 0x600, v59
	v_max_f32_e32 v204, 0, v160
	v_max_f32_e32 v208, 0, v161
	v_fma_f32 v201, v144, v204, 0
	v_max_f32_e32 v204, 0, v162
	v_fmac_f32_e32 v201, v145, v208
	v_max_f32_e32 v208, 0, v163
	v_fmac_f32_e32 v201, v146, v204
	v_max_f32_e32 v204, 0, v164
	v_fmac_f32_e32 v201, v147, v208
	v_max_f32_e32 v208, 0, v165
	v_fmac_f32_e32 v201, v148, v204
	v_max_f32_e32 v204, 0, v166
	v_fmac_f32_e32 v201, v149, v208
	v_max_f32_e32 v208, 0, v167
	v_fmac_f32_e32 v201, v150, v204
	v_max_f32_e32 v204, 0, v168
	v_fmac_f32_e32 v201, v151, v208
	v_max_f32_e32 v208, 0, v169
	v_fmac_f32_e32 v201, v152, v204
	v_max_f32_e32 v204, 0, v170
	v_fmac_f32_e32 v201, v153, v208
	v_max_f32_e32 v208, 0, v171
	v_fmac_f32_e32 v201, v154, v204
	v_max_f32_e32 v204, 0, v172
	v_fmac_f32_e32 v201, v155, v208
	v_max_f32_e32 v208, 0, v173
	v_fmac_f32_e32 v201, v156, v204
	v_max_f32_e32 v204, 0, v174
	v_fmac_f32_e32 v201, v157, v208
	v_max_f32_e32 v208, 0, v175
	v_fmac_f32_e32 v201, v158, v204
	v_fmac_f32_e32 v201, v159, v208
	v_cndmask_b32_e32 v201, v61, v201, vcc
	v_ashrrev_i32_e32 v207, 31, v201
	v_or_b32_e32 v207, 0x80000000, v207
	v_xor_b32_e32 v112, v201, v207
	s_cmp_le_u32 s15, 50
	s_cbranch_scc1 .Lidx_x50
	ds_read_b128 v[18:21], v57 offset:12288
	ds_read_b128 v[22:25], v57 offset:13312
	ds_read_b128 v[26:29], v57 offset:14336
	ds_read_b128 v[30:33], v57 offset:15360
	s_waitcnt lgkmcnt(4)
	v_mfma_f32_32x32x16_bf16 v[160:175], v[128:131], v[2:5], 0
	v_mfma_f32_32x32x16_bf16 v[160:175], v[132:135], v[6:9], v[160:175]
	v_mfma_f32_32x32x16_bf16 v[160:175], v[136:139], v[10:13], v[160:175]
	v_mfma_f32_32x32x16_bf16 v[160:175], v[140:143], v[14:17], v[160:175]
	v_cmp_le_i32_e32 vcc, 0x620, v59
	v_max_f32_e32 v204, 0, v176
	v_max_f32_e32 v208, 0, v177
	v_fma_f32 v201, v144, v204, 0
	v_max_f32_e32 v204, 0, v178
	v_fmac_f32_e32 v201, v145, v208
	v_max_f32_e32 v208, 0, v179
	v_fmac_f32_e32 v201, v146, v204
	v_max_f32_e32 v204, 0, v180
	v_fmac_f32_e32 v201, v147, v208
	v_max_f32_e32 v208, 0, v181
	v_fmac_f32_e32 v201, v148, v204
	v_max_f32_e32 v204, 0, v182
	v_fmac_f32_e32 v201, v149, v208
	v_max_f32_e32 v208, 0, v183
	v_fmac_f32_e32 v201, v150, v204
	v_max_f32_e32 v204, 0, v184
	v_fmac_f32_e32 v201, v151, v208
	v_max_f32_e32 v208, 0, v185
	v_fmac_f32_e32 v201, v152, v204
	v_max_f32_e32 v204, 0, v186
	v_fmac_f32_e32 v201, v153, v208
	v_max_f32_e32 v208, 0, v187
	v_fmac_f32_e32 v201, v154, v204
	v_max_f32_e32 v204, 0, v188
	v_fmac_f32_e32 v201, v155, v208
	v_max_f32_e32 v208, 0, v189
	v_fmac_f32_e32 v201, v156, v204
	v_max_f32_e32 v204, 0, v190
	v_fmac_f32_e32 v201, v157, v208
	v_max_f32_e32 v208, 0, v191
	v_fmac_f32_e32 v201, v158, v204
	v_fmac_f32_e32 v201, v159, v208
	v_cndmask_b32_e32 v201, v61, v201, vcc
	v_ashrrev_i32_e32 v207, 31, v201
	v_or_b32_e32 v207, 0x80000000, v207
	v_xor_b32_e32 v113, v201, v207
	s_cmp_le_u32 s15, 51
	s_cbranch_scc1 .Lidx_x51
	ds_read_b128 v[2:5], v57 offset:16384
	ds_read_b128 v[6:9], v57 offset:17408
	ds_read_b128 v[10:13], v57 offset:18432
	ds_read_b128 v[14:17], v57 offset:19456
	s_waitcnt lgkmcnt(4)
	v_mfma_f32_32x32x16_bf16 v[176:191], v[128:131], v[18:21], 0
	v_mfma_f32_32x32x16_bf16 v[176:191], v[132:135], v[22:25], v[176:191]
	v_mfma_f32_32x32x16_bf16 v[176:191], v[136:139], v[26:29], v[176:191]
	v_mfma_f32_32x32x16_bf16 v[176:191], v[140:143], v[30:33], v[176:191]
	v_cmp_le_i32_e32 vcc, 0x640, v59
	v_max_f32_e32 v204, 0, v160
	v_max_f32_e32 v208, 0, v161
	v_fma_f32 v201, v144, v204, 0
	v_max_f32_e32 v204, 0, v162
	v_fmac_f32_e32 v201, v145, v208
	v_max_f32_e32 v208, 0, v163
	v_fmac_f32_e32 v201, v146, v204
	v_max_f32_e32 v204, 0, v164
	v_fmac_f32_e32 v201, v147, v208
	v_max_f32_e32 v208, 0, v165
	v_fmac_f32_e32 v201, v148, v204
	v_max_f32_e32 v204, 0, v166
	v_fmac_f32_e32 v201, v149, v208
	v_max_f32_e32 v208, 0, v167
	v_fmac_f32_e32 v201, v150, v204
	v_max_f32_e32 v204, 0, v168
	v_fmac_f32_e32 v201, v151, v208
	v_max_f32_e32 v208, 0, v169
	v_fmac_f32_e32 v201, v152, v204
	v_max_f32_e32 v204, 0, v170
	v_fmac_f32_e32 v201, v153, v208
	v_max_f32_e32 v208, 0, v171
	v_fmac_f32_e32 v201, v154, v204
	v_max_f32_e32 v204, 0, v172
	v_fmac_f32_e32 v201, v155, v208
	v_max_f32_e32 v208, 0, v173
	v_fmac_f32_e32 v201, v156, v204
	v_max_f32_e32 v204, 0, v174
	v_fmac_f32_e32 v201, v157, v208
	v_max_f32_e32 v208, 0, v175
	v_fmac_f32_e32 v201, v158, v204
	v_fmac_f32_e32 v201, v159, v208
	v_cndmask_b32_e32 v201, v61, v201, vcc
	v_ashrrev_i32_e32 v207, 31, v201
	v_or_b32_e32 v207, 0x80000000, v207
	v_xor_b32_e32 v114, v201, v207
	s_cmp_le_u32 s15, 52
	s_cbranch_scc1 .Lidx_x52
	ds_read_b128 v[18:21], v57 offset:20480
	ds_read_b128 v[22:25], v57 offset:21504
	ds_read_b128 v[26:29], v57 offset:22528
	ds_read_b128 v[30:33], v57 offset:23552
	s_waitcnt lgkmcnt(4)
	v_mfma_f32_32x32x16_bf16 v[160:175], v[128:131], v[2:5], 0
	v_mfma_f32_32x32x16_bf16 v[160:175], v[132:135], v[6:9], v[160:175]
	v_mfma_f32_32x32x16_bf16 v[160:175], v[136:139], v[10:13], v[160:175]
	v_mfma_f32_32x32x16_bf16 v[160:175], v[140:143], v[14:17], v[160:175]
	v_cmp_le_i32_e32 vcc, 0x660, v59
	v_max_f32_e32 v204, 0, v176
	v_max_f32_e32 v208, 0, v177
	v_fma_f32 v201, v144, v204, 0
	v_max_f32_e32 v204, 0, v178
	v_fmac_f32_e32 v201, v145, v208
	v_max_f32_e32 v208, 0, v179
	v_fmac_f32_e32 v201, v146, v204
	v_max_f32_e32 v204, 0, v180
	v_fmac_f32_e32 v201, v147, v208
	v_max_f32_e32 v208, 0, v181
	v_fmac_f32_e32 v201, v148, v204
	v_max_f32_e32 v204, 0, v182
	v_fmac_f32_e32 v201, v149, v208
	v_max_f32_e32 v208, 0, v183
	v_fmac_f32_e32 v201, v150, v204
	v_max_f32_e32 v204, 0, v184
	v_fmac_f32_e32 v201, v151, v208
	v_max_f32_e32 v208, 0, v185
	v_fmac_f32_e32 v201, v152, v204
	v_max_f32_e32 v204, 0, v186
	v_fmac_f32_e32 v201, v153, v208
	v_max_f32_e32 v208, 0, v187
	v_fmac_f32_e32 v201, v154, v204
	v_max_f32_e32 v204, 0, v188
	v_fmac_f32_e32 v201, v155, v208
	v_max_f32_e32 v208, 0, v189
	v_fmac_f32_e32 v201, v156, v204
	v_max_f32_e32 v204, 0, v190
	v_fmac_f32_e32 v201, v157, v208
	v_max_f32_e32 v208, 0, v191
	v_fmac_f32_e32 v201, v158, v204
	v_fmac_f32_e32 v201, v159, v208
	v_cndmask_b32_e32 v201, v61, v201, vcc
	v_ashrrev_i32_e32 v207, 31, v201
	v_or_b32_e32 v207, 0x80000000, v207
	v_xor_b32_e32 v115, v201, v207
	s_cmp_le_u32 s15, 53
	s_cbranch_scc1 .Lidx_x53
	ds_read_b128 v[2:5], v57 offset:24576
	ds_read_b128 v[6:9], v57 offset:25600
	ds_read_b128 v[10:13], v57 offset:26624
	ds_read_b128 v[14:17], v57 offset:27648
	s_waitcnt lgkmcnt(4)
	v_mfma_f32_32x32x16_bf16 v[176:191], v[128:131], v[18:21], 0
	v_mfma_f32_32x32x16_bf16 v[176:191], v[132:135], v[22:25], v[176:191]
	v_mfma_f32_32x32x16_bf16 v[176:191], v[136:139], v[26:29], v[176:191]
	v_mfma_f32_32x32x16_bf16 v[176:191], v[140:143], v[30:33], v[176:191]
	v_cmp_le_i32_e32 vcc, 0x680, v59
	v_max_f32_e32 v204, 0, v160
	v_max_f32_e32 v208, 0, v161
	v_fma_f32 v201, v144, v204, 0
	v_max_f32_e32 v204, 0, v162
	v_fmac_f32_e32 v201, v145, v208
	v_max_f32_e32 v208, 0, v163
	v_fmac_f32_e32 v201, v146, v204
	v_max_f32_e32 v204, 0, v164
	v_fmac_f32_e32 v201, v147, v208
	v_max_f32_e32 v208, 0, v165
	v_fmac_f32_e32 v201, v148, v204
	v_max_f32_e32 v204, 0, v166
	v_fmac_f32_e32 v201, v149, v208
	v_max_f32_e32 v208, 0, v167
	v_fmac_f32_e32 v201, v150, v204
	v_max_f32_e32 v204, 0, v168
	v_fmac_f32_e32 v201, v151, v208
	v_max_f32_e32 v208, 0, v169
	v_fmac_f32_e32 v201, v152, v204
	v_max_f32_e32 v204, 0, v170
	v_fmac_f32_e32 v201, v153, v208
	v_max_f32_e32 v208, 0, v171
	v_fmac_f32_e32 v201, v154, v204
	v_max_f32_e32 v204, 0, v172
	v_fmac_f32_e32 v201, v155, v208
	v_max_f32_e32 v208, 0, v173
	v_fmac_f32_e32 v201, v156, v204
	v_max_f32_e32 v204, 0, v174
	v_fmac_f32_e32 v201, v157, v208
	v_max_f32_e32 v208, 0, v175
	v_fmac_f32_e32 v201, v158, v204
	v_fmac_f32_e32 v201, v159, v208
	v_cndmask_b32_e32 v201, v61, v201, vcc
	v_ashrrev_i32_e32 v207, 31, v201
	v_or_b32_e32 v207, 0x80000000, v207
	v_xor_b32_e32 v116, v201, v207
	s_cmp_le_u32 s15, 54
	s_cbranch_scc1 .Lidx_x54
	ds_read_b128 v[18:21], v57 offset:28672
	ds_read_b128 v[22:25], v57 offset:29696
	ds_read_b128 v[26:29], v57 offset:30720
	ds_read_b128 v[30:33], v57 offset:31744
	s_waitcnt lgkmcnt(4)
	v_mfma_f32_32x32x16_bf16 v[160:175], v[128:131], v[2:5], 0
	v_mfma_f32_32x32x16_bf16 v[160:175], v[132:135], v[6:9], v[160:175]
	v_mfma_f32_32x32x16_bf16 v[160:175], v[136:139], v[10:13], v[160:175]
	v_mfma_f32_32x32x16_bf16 v[160:175], v[140:143], v[14:17], v[160:175]
	v_cmp_le_i32_e32 vcc, 0x6a0, v59
	v_max_f32_e32 v204, 0, v176
	v_max_f32_e32 v208, 0, v177
	v_fma_f32 v201, v144, v204, 0
	v_max_f32_e32 v204, 0, v178
	v_fmac_f32_e32 v201, v145, v208
	v_max_f32_e32 v208, 0, v179
	v_fmac_f32_e32 v201, v146, v204
	v_max_f32_e32 v204, 0, v180
	v_fmac_f32_e32 v201, v147, v208
	v_max_f32_e32 v208, 0, v181
	v_fmac_f32_e32 v201, v148, v204
	v_max_f32_e32 v204, 0, v182
	v_fmac_f32_e32 v201, v149, v208
	v_max_f32_e32 v208, 0, v183
	v_fmac_f32_e32 v201, v150, v204
	v_max_f32_e32 v204, 0, v184
	v_fmac_f32_e32 v201, v151, v208
	v_max_f32_e32 v208, 0, v185
	v_fmac_f32_e32 v201, v152, v204
	v_max_f32_e32 v204, 0, v186
	v_fmac_f32_e32 v201, v153, v208
	v_max_f32_e32 v208, 0, v187
	v_fmac_f32_e32 v201, v154, v204
	v_max_f32_e32 v204, 0, v188
	v_fmac_f32_e32 v201, v155, v208
	v_max_f32_e32 v208, 0, v189
	v_fmac_f32_e32 v201, v156, v204
	v_max_f32_e32 v204, 0, v190
	v_fmac_f32_e32 v201, v157, v208
	v_max_f32_e32 v208, 0, v191
	v_fmac_f32_e32 v201, v158, v204
	v_fmac_f32_e32 v201, v159, v208
	v_cndmask_b32_e32 v201, v61, v201, vcc
	v_ashrrev_i32_e32 v207, 31, v201
	v_or_b32_e32 v207, 0x80000000, v207
	v_xor_b32_e32 v117, v201, v207
	s_cmp_le_u32 s15, 55
	s_cbranch_scc1 .Lidx_x55
	s_waitcnt lgkmcnt(0)
	v_mfma_f32_32x32x16_bf16 v[176:191], v[128:131], v[18:21], 0
	v_mfma_f32_32x32x16_bf16 v[176:191], v[132:135], v[22:25], v[176:191]
	v_mfma_f32_32x32x16_bf16 v[176:191], v[136:139], v[26:29], v[176:191]
	v_mfma_f32_32x32x16_bf16 v[176:191], v[140:143], v[30:33], v[176:191]
	v_cmp_le_i32_e32 vcc, 0x6c0, v59
	v_max_f32_e32 v204, 0, v160
	v_max_f32_e32 v208, 0, v161
	v_fma_f32 v201, v144, v204, 0
	v_max_f32_e32 v204, 0, v162
	v_fmac_f32_e32 v201, v145, v208
	v_max_f32_e32 v208, 0, v163
	v_fmac_f32_e32 v201, v146, v204
	v_max_f32_e32 v204, 0, v164
	v_fmac_f32_e32 v201, v147, v208
	v_max_f32_e32 v208, 0, v165
	v_fmac_f32_e32 v201, v148, v204
	v_max_f32_e32 v204, 0, v166
	v_fmac_f32_e32 v201, v149, v208
	v_max_f32_e32 v208, 0, v167
	v_fmac_f32_e32 v201, v150, v204
	v_max_f32_e32 v204, 0, v168
	v_fmac_f32_e32 v201, v151, v208
	v_max_f32_e32 v208, 0, v169
	v_fmac_f32_e32 v201, v152, v204
	v_max_f32_e32 v204, 0, v170
	v_fmac_f32_e32 v201, v153, v208
	v_max_f32_e32 v208, 0, v171
	v_fmac_f32_e32 v201, v154, v204
	v_max_f32_e32 v204, 0, v172
	v_fmac_f32_e32 v201, v155, v208
	v_max_f32_e32 v208, 0, v173
	v_fmac_f32_e32 v201, v156, v204
	v_max_f32_e32 v204, 0, v174
	v_fmac_f32_e32 v201, v157, v208
	v_max_f32_e32 v208, 0, v175
	v_fmac_f32_e32 v201, v158, v204
	v_fmac_f32_e32 v201, v159, v208
	v_cndmask_b32_e32 v201, v61, v201, vcc
	v_ashrrev_i32_e32 v207, 31, v201
	v_or_b32_e32 v207, 0x80000000, v207
	v_xor_b32_e32 v118, v201, v207
.Lidx_ce6:
.Lidx_c7:
	s_cmp_le_u32 s29, 7
	s_cbranch_scc1 .Lidx_fin7
	s_waitcnt vmcnt(0) lgkmcnt(0)
	s_barrier
	s_cmp_lt_u32 s15, 56
	s_cbranch_scc1 .Lidx_ce7
	s_cmp_le_u32 s15, 56
	s_cbranch_scc1 .Lidx_x56
	ds_read_b128 v[2:5], v57 offset:32768
	ds_read_b128 v[6:9], v57 offset:33792
	ds_read_b128 v[10:13], v57 offset:34816
	ds_read_b128 v[14:17], v57 offset:35840
	ds_read_b128 v[18:21], v57 offset:36864
	ds_read_b128 v[22:25], v57 offset:37888
	ds_read_b128 v[26:29], v57 offset:38912
	ds_read_b128 v[30:33], v57 offset:39936
	s_waitcnt lgkmcnt(4)
	v_mfma_f32_32x32x16_bf16 v[160:175], v[128:131], v[2:5], 0
	v_mfma_f32_32x32x16_bf16 v[160:175], v[132:135], v[6:9], v[160:175]
	v_mfma_f32_32x32x16_bf16 v[160:175], v[136:139], v[10:13], v[160:175]
	v_mfma_f32_32x32x16_bf16 v[160:175], v[140:143], v[14:17], v[160:175]
	v_cmp_le_i32_e32 vcc, 0x6e0, v59
	v_max_f32_e32 v204, 0, v176
	v_max_f32_e32 v208, 0, v177
	v_fma_f32 v201, v144, v204, 0
	v_max_f32_e32 v204, 0, v178
	v_fmac_f32_e32 v201, v145, v208
	v_max_f32_e32 v208, 0, v179
	v_fmac_f32_e32 v201, v146, v204
	v_max_f32_e32 v204, 0, v180
	v_fmac_f32_e32 v201, v147, v208
	v_max_f32_e32 v208, 0, v181
	v_fmac_f32_e32 v201, v148, v204
	v_max_f32_e32 v204, 0, v182
	v_fmac_f32_e32 v201, v149, v208
	v_max_f32_e32 v208, 0, v183
	v_fmac_f32_e32 v201, v150, v204
	v_max_f32_e32 v204, 0, v184
	v_fmac_f32_e32 v201, v151, v208
	v_max_f32_e32 v208, 0, v185
	v_fmac_f32_e32 v201, v152, v204
	v_max_f32_e32 v204, 0, v186
	v_fmac_f32_e32 v201, v153, v208
	v_max_f32_e32 v208, 0, v187
	v_fmac_f32_e32 v201, v154, v204
	v_max_f32_e32 v204, 0, v188
	v_fmac_f32_e32 v201, v155, v208
	v_max_f32_e32 v208, 0, v189
	v_fmac_f32_e32 v201, v156, v204
	v_max_f32_e32 v204, 0, v190
	v_fmac_f32_e32 v201, v157, v208
	v_max_f32_e32 v208, 0, v191
	v_fmac_f32_e32 v201, v158, v204
	v_fmac_f32_e32 v201, v159, v208
	v_cndmask_b32_e32 v201, v61, v201, vcc
	v_ashrrev_i32_e32 v207, 31, v201
	v_or_b32_e32 v207, 0x80000000, v207
	v_xor_b32_e32 v119, v201, v207
	s_cmp_le_u32 s15, 57
	s_cbranch_scc1 .Lidx_x57
	ds_read_b128 v[2:5], v57 offset:40960
	ds_read_b128 v[6:9], v57 offset:41984
	ds_read_b128 v[10:13], v57 offset:43008
	ds_read_b128 v[14:17], v57 offset:44032
	s_waitcnt lgkmcnt(4)
	v_mfma_f32_32x32x16_bf16 v[176:191], v[128:131], v[18:21], 0
	v_mfma_f32_32x32x16_bf16 v[176:191], v[132:135], v[22:25], v[176:191]
	v_mfma_f32_32x32x16_bf16 v[176:191], v[136:139], v[26:29], v[176:191]
	v_mfma_f32_32x32x16_bf16 v[176:191], v[140:143], v[30:33], v[176:191]
	v_cmp_le_i32_e32 vcc, 0x700, v59
	v_max_f32_e32 v204, 0, v160
	v_max_f32_e32 v208, 0, v161
	v_fma_f32 v201, v144, v204, 0
	v_max_f32_e32 v204, 0, v162
	v_fmac_f32_e32 v201, v145, v208
	v_max_f32_e32 v208, 0, v163
	v_fmac_f32_e32 v201, v146, v204
	v_max_f32_e32 v204, 0, v164
	v_fmac_f32_e32 v201, v147, v208
	v_max_f32_e32 v208, 0, v165
	v_fmac_f32_e32 v201, v148, v204
	v_max_f32_e32 v204, 0, v166
	v_fmac_f32_e32 v201, v149, v208
	v_max_f32_e32 v208, 0, v167
	v_fmac_f32_e32 v201, v150, v204
	v_max_f32_e32 v204, 0, v168
	v_fmac_f32_e32 v201, v151, v208
	v_max_f32_e32 v208, 0, v169
	v_fmac_f32_e32 v201, v152, v204
	v_max_f32_e32 v204, 0, v170
	v_fmac_f32_e32 v201, v153, v208
	v_max_f32_e32 v208, 0, v171
	v_fmac_f32_e32 v201, v154, v204
	v_max_f32_e32 v204, 0, v172
	v_fmac_f32_e32 v201, v155, v208
	v_max_f32_e32 v208, 0, v173
	v_fmac_f32_e32 v201, v156, v204
	v_max_f32_e32 v204, 0, v174
	v_fmac_f32_e32 v201, v157, v208
	v_max_f32_e32 v208, 0, v175
	v_fmac_f32_e32 v201, v158, v204
	v_fmac_f32_e32 v201, v159, v208
	v_cndmask_b32_e32 v201, v61, v201, vcc
	v_ashrrev_i32_e32 v207, 31, v201
	v_or_b32_e32 v207, 0x80000000, v207
	v_xor_b32_e32 v120, v201, v207
	s_cmp_le_u32 s15, 58
	s_cbranch_scc1 .Lidx_x58
	ds_read_b128 v[18:21], v57 offset:45056
	ds_read_b128 v[22:25], v57 offset:46080
	ds_read_b128 v[26:29], v57 offset:47104
	ds_read_b128 v[30:33], v57 offset:48128
	s_waitcnt lgkmcnt(4)
	v_mfma_f32_32x32x16_bf16 v[160:175], v[128:131], v[2:5], 0
	v_mfma_f32_32x32x16_bf16 v[160:175], v[132:135], v[6:9], v[160:175]
	v_mfma_f32_32x32x16_bf16 v[160:175], v[136:139], v[10:13], v[160:175]
	v_mfma_f32_32x32x16_bf16 v[160:175], v[140:143], v[14:17], v[160:175]
	v_cmp_le_i32_e32 vcc, 0x720, v59
	v_max_f32_e32 v204, 0, v176
	v_max_f32_e32 v208, 0, v177
	v_fma_f32 v201, v144, v204, 0
	v_max_f32_e32 v204, 0, v178
	v_fmac_f32_e32 v201, v145, v208
	v_max_f32_e32 v208, 0, v179
	v_fmac_f32_e32 v201, v146, v204
	v_max_f32_e32 v204, 0, v180
	v_fmac_f32_e32 v201, v147, v208
	v_max_f32_e32 v208, 0, v181
	v_fmac_f32_e32 v201, v148, v204
	v_max_f32_e32 v204, 0, v182
	v_fmac_f32_e32 v201, v149, v208
	v_max_f32_e32 v208, 0, v183
	v_fmac_f32_e32 v201, v150, v204
	v_max_f32_e32 v204, 0, v184
	v_fmac_f32_e32 v201, v151, v208
	v_max_f32_e32 v208, 0, v185
	v_fmac_f32_e32 v201, v152, v204
	v_max_f32_e32 v204, 0, v186
	v_fmac_f32_e32 v201, v153, v208
	v_max_f32_e32 v208, 0, v187
	v_fmac_f32_e32 v201, v154, v204
	v_max_f32_e32 v204, 0, v188
	v_fmac_f32_e32 v201, v155, v208
	v_max_f32_e32 v208, 0, v189
	v_fmac_f32_e32 v201, v156, v204
	v_max_f32_e32 v204, 0, v190
	v_fmac_f32_e32 v201, v157, v208
	v_max_f32_e32 v208, 0, v191
	v_fmac_f32_e32 v201, v158, v204
	v_fmac_f32_e32 v201, v159, v208
	v_cndmask_b32_e32 v201, v61, v201, vcc
	v_ashrrev_i32_e32 v207, 31, v201
	v_or_b32_e32 v207, 0x80000000, v207
	v_xor_b32_e32 v121, v201, v207
	s_cmp_le_u32 s15, 59
	s_cbranch_scc1 .Lidx_x59
	ds_read_b128 v[2:5], v57 offset:49152
	ds_read_b128 v[6:9], v57 offset:50176
	ds_read_b128 v[10:13], v57 offset:51200
	ds_read_b128 v[14:17], v57 offset:52224
	s_waitcnt lgkmcnt(4)
	v_mfma_f32_32x32x16_bf16 v[176:191], v[128:131], v[18:21], 0
	v_mfma_f32_32x32x16_bf16 v[176:191], v[132:135], v[22:25], v[176:191]
	v_mfma_f32_32x32x16_bf16 v[176:191], v[136:139], v[26:29], v[176:191]
	v_mfma_f32_32x32x16_bf16 v[176:191], v[140:143], v[30:33], v[176:191]
	v_cmp_le_i32_e32 vcc, 0x740, v59
	v_max_f32_e32 v204, 0, v160
	v_max_f32_e32 v208, 0, v161
	v_fma_f32 v201, v144, v204, 0
	v_max_f32_e32 v204, 0, v162
	v_fmac_f32_e32 v201, v145, v208
	v_max_f32_e32 v208, 0, v163
	v_fmac_f32_e32 v201, v146, v204
	v_max_f32_e32 v204, 0, v164
	v_fmac_f32_e32 v201, v147, v208
	v_max_f32_e32 v208, 0, v165
	v_fmac_f32_e32 v201, v148, v204
	v_max_f32_e32 v204, 0, v166
	v_fmac_f32_e32 v201, v149, v208
	v_max_f32_e32 v208, 0, v167
	v_fmac_f32_e32 v201, v150, v204
	v_max_f32_e32 v204, 0, v168
	v_fmac_f32_e32 v201, v151, v208
	v_max_f32_e32 v208, 0, v169
	v_fmac_f32_e32 v201, v152, v204
	v_max_f32_e32 v204, 0, v170
	v_fmac_f32_e32 v201, v153, v208
	v_max_f32_e32 v208, 0, v171
	v_fmac_f32_e32 v201, v154, v204
	v_max_f32_e32 v204, 0, v172
	v_fmac_f32_e32 v201, v155, v208
	v_max_f32_e32 v208, 0, v173
	v_fmac_f32_e32 v201, v156, v204
	v_max_f32_e32 v204, 0, v174
	v_fmac_f32_e32 v201, v157, v208
	v_max_f32_e32 v208, 0, v175
	v_fmac_f32_e32 v201, v158, v204
	v_fmac_f32_e32 v201, v159, v208
	v_cndmask_b32_e32 v201, v61, v201, vcc
	v_ashrrev_i32_e32 v207, 31, v201
	v_or_b32_e32 v207, 0x80000000, v207
	v_xor_b32_e32 v122, v201, v207
	s_cmp_le_u32 s15, 60
	s_cbranch_scc1 .Lidx_x60
	ds_read_b128 v[18:21], v57 offset:53248
	ds_read_b128 v[22:25], v57 offset:54272
	ds_read_b128 v[26:29], v57 offset:55296
	ds_read_b128 v[30:33], v57 offset:56320
	s_waitcnt lgkmcnt(4)
	v_mfma_f32_32x32x16_bf16 v[160:175], v[128:131], v[2:5], 0
	v_mfma_f32_32x32x16_bf16 v[160:175], v[132:135], v[6:9], v[160:175]
	v_mfma_f32_32x32x16_bf16 v[160:175], v[136:139], v[10:13], v[160:175]
	v_mfma_f32_32x32x16_bf16 v[160:175], v[140:143], v[14:17], v[160:175]
	v_cmp_le_i32_e32 vcc, 0x760, v59
	v_max_f32_e32 v204, 0, v176
	v_max_f32_e32 v208, 0, v177
	v_fma_f32 v201, v144, v204, 0
	v_max_f32_e32 v204, 0, v178
	v_fmac_f32_e32 v201, v145, v208
	v_max_f32_e32 v208, 0, v179
	v_fmac_f32_e32 v201, v146, v204
	v_max_f32_e32 v204, 0, v180
	v_fmac_f32_e32 v201, v147, v208
	v_max_f32_e32 v208, 0, v181
	v_fmac_f32_e32 v201, v148, v204
	v_max_f32_e32 v204, 0, v182
	v_fmac_f32_e32 v201, v149, v208
	v_max_f32_e32 v208, 0, v183
	v_fmac_f32_e32 v201, v150, v204
	v_max_f32_e32 v204, 0, v184
	v_fmac_f32_e32 v201, v151, v208
	v_max_f32_e32 v208, 0, v185
	v_fmac_f32_e32 v201, v152, v204
	v_max_f32_e32 v204, 0, v186
	v_fmac_f32_e32 v201, v153, v208
	v_max_f32_e32 v208, 0, v187
	v_fmac_f32_e32 v201, v154, v204
	v_max_f32_e32 v204, 0, v188
	v_fmac_f32_e32 v201, v155, v208
	v_max_f32_e32 v208, 0, v189
	v_fmac_f32_e32 v201, v156, v204
	v_max_f32_e32 v204, 0, v190
	v_fmac_f32_e32 v201, v157, v208
	v_max_f32_e32 v208, 0, v191
	v_fmac_f32_e32 v201, v158, v204
	v_fmac_f32_e32 v201, v159, v208
	v_cndmask_b32_e32 v201, v61, v201, vcc
	v_ashrrev_i32_e32 v207, 31, v201
	v_or_b32_e32 v207, 0x80000000, v207
	v_xor_b32_e32 v123, v201, v207
	s_cmp_le_u32 s15, 61
	s_cbranch_scc1 .Lidx_x61
	ds_read_b128 v[2:5], v57 offset:57344
	ds_read_b128 v[6:9], v57 offset:58368
	ds_read_b128 v[10:13], v57 offset:59392
	ds_read_b128 v[14:17], v57 offset:60416
	s_waitcnt lgkmcnt(4)
	v_mfma_f32_32x32x16_bf16 v[176:191], v[128:131], v[18:21], 0
	v_mfma_f32_32x32x16_bf16 v[176:191], v[132:135], v[22:25], v[176:191]
	v_mfma_f32_32x32x16_bf16 v[176:191], v[136:139], v[26:29], v[176:191]
	v_mfma_f32_32x32x16_bf16 v[176:191], v[140:143], v[30:33], v[176:191]
	v_cmp_le_i32_e32 vcc, 0x780, v59
	v_max_f32_e32 v204, 0, v160
	v_max_f32_e32 v208, 0, v161
	v_fma_f32 v201, v144, v204, 0
	v_max_f32_e32 v204, 0, v162
	v_fmac_f32_e32 v201, v145, v208
	v_max_f32_e32 v208, 0, v163
	v_fmac_f32_e32 v201, v146, v204
	v_max_f32_e32 v204, 0, v164
	v_fmac_f32_e32 v201, v147, v208
	v_max_f32_e32 v208, 0, v165
	v_fmac_f32_e32 v201, v148, v204
	v_max_f32_e32 v204, 0, v166
	v_fmac_f32_e32 v201, v149, v208
	v_max_f32_e32 v208, 0, v167
	v_fmac_f32_e32 v201, v150, v204
	v_max_f32_e32 v204, 0, v168
	v_fmac_f32_e32 v201, v151, v208
	v_max_f32_e32 v208, 0, v169
	v_fmac_f32_e32 v201, v152, v204
	v_max_f32_e32 v204, 0, v170
	v_fmac_f32_e32 v201, v153, v208
	v_max_f32_e32 v208, 0, v171
	v_fmac_f32_e32 v201, v154, v204
	v_max_f32_e32 v204, 0, v172
	v_fmac_f32_e32 v201, v155, v208
	v_max_f32_e32 v208, 0, v173
	v_fmac_f32_e32 v201, v156, v204
	v_max_f32_e32 v204, 0, v174
	v_fmac_f32_e32 v201, v157, v208
	v_max_f32_e32 v208, 0, v175
	v_fmac_f32_e32 v201, v158, v204
	v_fmac_f32_e32 v201, v159, v208
	v_cndmask_b32_e32 v201, v61, v201, vcc
	v_ashrrev_i32_e32 v207, 31, v201
	v_or_b32_e32 v207, 0x80000000, v207
	v_xor_b32_e32 v124, v201, v207
	s_cmp_le_u32 s15, 62
	s_cbranch_scc1 .Lidx_x62
	ds_read_b128 v[18:21], v57 offset:61440
	ds_read_b128 v[22:25], v57 offset:62464
	ds_read_b128 v[26:29], v57 offset:63488
	ds_read_b128 v[30:33], v57 offset:64512
	s_waitcnt lgkmcnt(4)
	v_mfma_f32_32x32x16_bf16 v[160:175], v[128:131], v[2:5], 0
	v_mfma_f32_32x32x16_bf16 v[160:175], v[132:135], v[6:9], v[160:175]
	v_mfma_f32_32x32x16_bf16 v[160:175], v[136:139], v[10:13], v[160:175]
	v_mfma_f32_32x32x16_bf16 v[160:175], v[140:143], v[14:17], v[160:175]
	v_cmp_le_i32_e32 vcc, 0x7a0, v59
	v_max_f32_e32 v204, 0, v176
	v_max_f32_e32 v208, 0, v177
	v_fma_f32 v201, v144, v204, 0
	v_max_f32_e32 v204, 0, v178
	v_fmac_f32_e32 v201, v145, v208
	v_max_f32_e32 v208, 0, v179
	v_fmac_f32_e32 v201, v146, v204
	v_max_f32_e32 v204, 0, v180
	v_fmac_f32_e32 v201, v147, v208
	v_max_f32_e32 v208, 0, v181
	v_fmac_f32_e32 v201, v148, v204
	v_max_f32_e32 v204, 0, v182
	v_fmac_f32_e32 v201, v149, v208
	v_max_f32_e32 v208, 0, v183
	v_fmac_f32_e32 v201, v150, v204
	v_max_f32_e32 v204, 0, v184
	v_fmac_f32_e32 v201, v151, v208
	v_max_f32_e32 v208, 0, v185
	v_fmac_f32_e32 v201, v152, v204
	v_max_f32_e32 v204, 0, v186
	v_fmac_f32_e32 v201, v153, v208
	v_max_f32_e32 v208, 0, v187
	v_fmac_f32_e32 v201, v154, v204
	v_max_f32_e32 v204, 0, v188
	v_fmac_f32_e32 v201, v155, v208
	v_max_f32_e32 v208, 0, v189
	v_fmac_f32_e32 v201, v156, v204
	v_max_f32_e32 v204, 0, v190
	v_fmac_f32_e32 v201, v157, v208
	v_max_f32_e32 v208, 0, v191
	v_fmac_f32_e32 v201, v158, v204
	v_fmac_f32_e32 v201, v159, v208
	v_cndmask_b32_e32 v201, v61, v201, vcc
	v_ashrrev_i32_e32 v207, 31, v201
	v_or_b32_e32 v207, 0x80000000, v207
	v_xor_b32_e32 v125, v201, v207
	s_cmp_le_u32 s15, 63
	s_cbranch_scc1 .Lidx_x63
	s_waitcnt lgkmcnt(0)
	v_mfma_f32_32x32x16_bf16 v[176:191], v[128:131], v[18:21], 0
	v_mfma_f32_32x32x16_bf16 v[176:191], v[132:135], v[22:25], v[176:191]
	v_mfma_f32_32x32x16_bf16 v[176:191], v[136:139], v[26:29], v[176:191]
	v_mfma_f32_32x32x16_bf16 v[176:191], v[140:143], v[30:33], v[176:191]
	v_cmp_le_i32_e32 vcc, 0x7c0, v59
	v_max_f32_e32 v204, 0, v160
	v_max_f32_e32 v208, 0, v161
	v_fma_f32 v201, v144, v204, 0
	v_max_f32_e32 v204, 0, v162
	v_fmac_f32_e32 v201, v145, v208
	v_max_f32_e32 v208, 0, v163
	v_fmac_f32_e32 v201, v146, v204
	v_max_f32_e32 v204, 0, v164
	v_fmac_f32_e32 v201, v147, v208
	v_max_f32_e32 v208, 0, v165
	v_fmac_f32_e32 v201, v148, v204
	v_max_f32_e32 v204, 0, v166
	v_fmac_f32_e32 v201, v149, v208
	v_max_f32_e32 v208, 0, v167
	v_fmac_f32_e32 v201, v150, v204
	v_max_f32_e32 v204, 0, v168
	v_fmac_f32_e32 v201, v151, v208
	v_max_f32_e32 v208, 0, v169
	v_fmac_f32_e32 v201, v152, v204
	v_max_f32_e32 v204, 0, v170
	v_fmac_f32_e32 v201, v153, v208
	v_max_f32_e32 v208, 0, v171
	v_fmac_f32_e32 v201, v154, v204
	v_max_f32_e32 v204, 0, v172
	v_fmac_f32_e32 v201, v155, v208
	v_max_f32_e32 v208, 0, v173
	v_fmac_f32_e32 v201, v156, v204
	v_max_f32_e32 v204, 0, v174
	v_fmac_f32_e32 v201, v157, v208
	v_max_f32_e32 v208, 0, v175
	v_fmac_f32_e32 v201, v158, v204
	v_fmac_f32_e32 v201, v159, v208
	v_cndmask_b32_e32 v201, v61, v201, vcc
	v_ashrrev_i32_e32 v207, 31, v201
	v_or_b32_e32 v207, 0x80000000, v207
	v_xor_b32_e32 v126, v201, v207
.Lidx_ce7:
.Lidx_fin8:
	s_cmp_lg_u32 s15, 64
	s_cbranch_scc1 .Lidx_search
	s_nop 15
	v_cmp_le_i32_e32 vcc, 0x7e0, v59
	v_max_f32_e32 v204, 0, v176
	v_max_f32_e32 v208, 0, v177
	v_fma_f32 v201, v144, v204, 0
	v_max_f32_e32 v204, 0, v178
	v_fmac_f32_e32 v201, v145, v208
	v_max_f32_e32 v208, 0, v179
	v_fmac_f32_e32 v201, v146, v204
	v_max_f32_e32 v204, 0, v180
	v_fmac_f32_e32 v201, v147, v208
	v_max_f32_e32 v208, 0, v181
	v_fmac_f32_e32 v201, v148, v204
	v_max_f32_e32 v204, 0, v182
	v_fmac_f32_e32 v201, v149, v208
	v_max_f32_e32 v208, 0, v183
	v_fmac_f32_e32 v201, v150, v204
	v_max_f32_e32 v204, 0, v184
	v_fmac_f32_e32 v201, v151, v208
	v_max_f32_e32 v208, 0, v185
	v_fmac_f32_e32 v201, v152, v204
	v_max_f32_e32 v204, 0, v186
	v_fmac_f32_e32 v201, v153, v208
	v_max_f32_e32 v208, 0, v187
	v_fmac_f32_e32 v201, v154, v204
	v_max_f32_e32 v204, 0, v188
	v_fmac_f32_e32 v201, v155, v208
	v_max_f32_e32 v208, 0, v189
	v_fmac_f32_e32 v201, v156, v204
	v_max_f32_e32 v204, 0, v190
	v_fmac_f32_e32 v201, v157, v208
	v_max_f32_e32 v208, 0, v191
	v_fmac_f32_e32 v201, v158, v204
	v_fmac_f32_e32 v201, v159, v208
	v_cndmask_b32_e32 v201, v61, v201, vcc
	v_ashrrev_i32_e32 v207, 31, v201
	v_or_b32_e32 v207, 0x80000000, v207
	v_xor_b32_e32 v127, v201, v207
	s_branch .Lidx_search
.Lidx_fin7:
	s_cmp_lg_u32 s15, 56
	s_cbranch_scc1 .Lidx_search
	s_nop 15
	v_cmp_le_i32_e32 vcc, 0x6e0, v59
	v_max_f32_e32 v204, 0, v176
	v_max_f32_e32 v208, 0, v177
	v_fma_f32 v201, v144, v204, 0
	v_max_f32_e32 v204, 0, v178
	v_fmac_f32_e32 v201, v145, v208
	v_max_f32_e32 v208, 0, v179
	v_fmac_f32_e32 v201, v146, v204
	v_max_f32_e32 v204, 0, v180
	v_fmac_f32_e32 v201, v147, v208
	v_max_f32_e32 v208, 0, v181
	v_fmac_f32_e32 v201, v148, v204
	v_max_f32_e32 v204, 0, v182
	v_fmac_f32_e32 v201, v149, v208
	v_max_f32_e32 v208, 0, v183
	v_fmac_f32_e32 v201, v150, v204
	v_max_f32_e32 v204, 0, v184
	v_fmac_f32_e32 v201, v151, v208
	v_max_f32_e32 v208, 0, v185
	v_fmac_f32_e32 v201, v152, v204
	v_max_f32_e32 v204, 0, v186
	v_fmac_f32_e32 v201, v153, v208
	v_max_f32_e32 v208, 0, v187
	v_fmac_f32_e32 v201, v154, v204
	v_max_f32_e32 v204, 0, v188
	v_fmac_f32_e32 v201, v155, v208
	v_max_f32_e32 v208, 0, v189
	v_fmac_f32_e32 v201, v156, v204
	v_max_f32_e32 v204, 0, v190
	v_fmac_f32_e32 v201, v157, v208
	v_max_f32_e32 v208, 0, v191
	v_fmac_f32_e32 v201, v158, v204
	v_fmac_f32_e32 v201, v159, v208
	v_cndmask_b32_e32 v201, v61, v201, vcc
	v_ashrrev_i32_e32 v207, 31, v201
	v_or_b32_e32 v207, 0x80000000, v207
	v_xor_b32_e32 v119, v201, v207
	s_branch .Lidx_search
.Lidx_fin6:
	s_cmp_lg_u32 s15, 48
	s_cbranch_scc1 .Lidx_search
	s_nop 15
	v_cmp_le_i32_e32 vcc, 0x5e0, v59
	v_max_f32_e32 v204, 0, v176
	v_max_f32_e32 v208, 0, v177
	v_fma_f32 v201, v144, v204, 0
	v_max_f32_e32 v204, 0, v178
	v_fmac_f32_e32 v201, v145, v208
	v_max_f32_e32 v208, 0, v179
	v_fmac_f32_e32 v201, v146, v204
	v_max_f32_e32 v204, 0, v180
	v_fmac_f32_e32 v201, v147, v208
	v_max_f32_e32 v208, 0, v181
	v_fmac_f32_e32 v201, v148, v204
	v_max_f32_e32 v204, 0, v182
	v_fmac_f32_e32 v201, v149, v208
	v_max_f32_e32 v208, 0, v183
	v_fmac_f32_e32 v201, v150, v204
	v_max_f32_e32 v204, 0, v184
	v_fmac_f32_e32 v201, v151, v208
	v_max_f32_e32 v208, 0, v185
	v_fmac_f32_e32 v201, v152, v204
	v_max_f32_e32 v204, 0, v186
	v_fmac_f32_e32 v201, v153, v208
	v_max_f32_e32 v208, 0, v187
	v_fmac_f32_e32 v201, v154, v204
	v_max_f32_e32 v204, 0, v188
	v_fmac_f32_e32 v201, v155, v208
	v_max_f32_e32 v208, 0, v189
	v_fmac_f32_e32 v201, v156, v204
	v_max_f32_e32 v204, 0, v190
	v_fmac_f32_e32 v201, v157, v208
	v_max_f32_e32 v208, 0, v191
	v_fmac_f32_e32 v201, v158, v204
	v_fmac_f32_e32 v201, v159, v208
	v_cndmask_b32_e32 v201, v61, v201, vcc
	v_ashrrev_i32_e32 v207, 31, v201
	v_or_b32_e32 v207, 0x80000000, v207
	v_xor_b32_e32 v111, v201, v207
	s_branch .Lidx_search
.Lidx_fin5:
	s_cmp_lg_u32 s15, 40
	s_cbranch_scc1 .Lidx_search
	s_nop 15
	v_cmp_le_i32_e32 vcc, 0x4e0, v59
	v_max_f32_e32 v204, 0, v176
	v_max_f32_e32 v208, 0, v177
	v_fma_f32 v201, v144, v204, 0
	v_max_f32_e32 v204, 0, v178
	v_fmac_f32_e32 v201, v145, v208
	v_max_f32_e32 v208, 0, v179
	v_fmac_f32_e32 v201, v146, v204
	v_max_f32_e32 v204, 0, v180
	v_fmac_f32_e32 v201, v147, v208
	v_max_f32_e32 v208, 0, v181
	v_fmac_f32_e32 v201, v148, v204
	v_max_f32_e32 v204, 0, v182
	v_fmac_f32_e32 v201, v149, v208
	v_max_f32_e32 v208, 0, v183
	v_fmac_f32_e32 v201, v150, v204
	v_max_f32_e32 v204, 0, v184
	v_fmac_f32_e32 v201, v151, v208
	v_max_f32_e32 v208, 0, v185
	v_fmac_f32_e32 v201, v152, v204
	v_max_f32_e32 v204, 0, v186
	v_fmac_f32_e32 v201, v153, v208
	v_max_f32_e32 v208, 0, v187
	v_fmac_f32_e32 v201, v154, v204
	v_max_f32_e32 v204, 0, v188
	v_fmac_f32_e32 v201, v155, v208
	v_max_f32_e32 v208, 0, v189
	v_fmac_f32_e32 v201, v156, v204
	v_max_f32_e32 v204, 0, v190
	v_fmac_f32_e32 v201, v157, v208
	v_max_f32_e32 v208, 0, v191
	v_fmac_f32_e32 v201, v158, v204
	v_fmac_f32_e32 v201, v159, v208
	v_cndmask_b32_e32 v201, v61, v201, vcc
	v_ashrrev_i32_e32 v207, 31, v201
	v_or_b32_e32 v207, 0x80000000, v207
	v_xor_b32_e32 v103, v201, v207
	s_branch .Lidx_search
.Lidx_fin4:
	s_cmp_lg_u32 s15, 32
	s_cbranch_scc1 .Lidx_search
	s_nop 15
	v_cmp_le_i32_e32 vcc, 0x3e0, v59
	v_max_f32_e32 v204, 0, v176
	v_max_f32_e32 v208, 0, v177
	v_fma_f32 v201, v144, v204, 0
	v_max_f32_e32 v204, 0, v178
	v_fmac_f32_e32 v201, v145, v208
	v_max_f32_e32 v208, 0, v179
	v_fmac_f32_e32 v201, v146, v204
	v_max_f32_e32 v204, 0, v180
	v_fmac_f32_e32 v201, v147, v208
	v_max_f32_e32 v208, 0, v181
	v_fmac_f32_e32 v201, v148, v204
	v_max_f32_e32 v204, 0, v182
	v_fmac_f32_e32 v201, v149, v208
	v_max_f32_e32 v208, 0, v183
	v_fmac_f32_e32 v201, v150, v204
	v_max_f32_e32 v204, 0, v184
	v_fmac_f32_e32 v201, v151, v208
	v_max_f32_e32 v208, 0, v185
	v_fmac_f32_e32 v201, v152, v204
	v_max_f32_e32 v204, 0, v186
	v_fmac_f32_e32 v201, v153, v208
	v_max_f32_e32 v208, 0, v187
	v_fmac_f32_e32 v201, v154, v204
	v_max_f32_e32 v204, 0, v188
	v_fmac_f32_e32 v201, v155, v208
	v_max_f32_e32 v208, 0, v189
	v_fmac_f32_e32 v201, v156, v204
	v_max_f32_e32 v204, 0, v190
	v_fmac_f32_e32 v201, v157, v208
	v_max_f32_e32 v208, 0, v191
	v_fmac_f32_e32 v201, v158, v204
	v_fmac_f32_e32 v201, v159, v208
	v_cndmask_b32_e32 v201, v61, v201, vcc
	v_ashrrev_i32_e32 v207, 31, v201
	v_or_b32_e32 v207, 0x80000000, v207
	v_xor_b32_e32 v95, v201, v207
	s_branch .Lidx_search
.Lidx_fin3:
	s_cmp_lg_u32 s15, 24
	s_cbranch_scc1 .Lidx_search
	s_nop 15
	v_cmp_le_i32_e32 vcc, 0x2e0, v59
	v_max_f32_e32 v204, 0, v176
	v_max_f32_e32 v208, 0, v177
	v_fma_f32 v201, v144, v204, 0
	v_max_f32_e32 v204, 0, v178
	v_fmac_f32_e32 v201, v145, v208
	v_max_f32_e32 v208, 0, v179
	v_fmac_f32_e32 v201, v146, v204
	v_max_f32_e32 v204, 0, v180
	v_fmac_f32_e32 v201, v147, v208
	v_max_f32_e32 v208, 0, v181
	v_fmac_f32_e32 v201, v148, v204
	v_max_f32_e32 v204, 0, v182
	v_fmac_f32_e32 v201, v149, v208
	v_max_f32_e32 v208, 0, v183
	v_fmac_f32_e32 v201, v150, v204
	v_max_f32_e32 v204, 0, v184
	v_fmac_f32_e32 v201, v151, v208
	v_max_f32_e32 v208, 0, v185
	v_fmac_f32_e32 v201, v152, v204
	v_max_f32_e32 v204, 0, v186
	v_fmac_f32_e32 v201, v153, v208
	v_max_f32_e32 v208, 0, v187
	v_fmac_f32_e32 v201, v154, v204
	v_max_f32_e32 v204, 0, v188
	v_fmac_f32_e32 v201, v155, v208
	v_max_f32_e32 v208, 0, v189
	v_fmac_f32_e32 v201, v156, v204
	v_max_f32_e32 v204, 0, v190
	v_fmac_f32_e32 v201, v157, v208
	v_max_f32_e32 v208, 0, v191
	v_fmac_f32_e32 v201, v158, v204
	v_fmac_f32_e32 v201, v159, v208
	v_cndmask_b32_e32 v201, v61, v201, vcc
	v_ashrrev_i32_e32 v207, 31, v201
	v_or_b32_e32 v207, 0x80000000, v207
	v_xor_b32_e32 v87, v201, v207
	s_branch .Lidx_search
.Lidx_fin2:
	s_cmp_lg_u32 s15, 16
	s_cbranch_scc1 .Lidx_search
	s_nop 15
	v_cmp_le_i32_e32 vcc, 0x1e0, v59
	v_max_f32_e32 v204, 0, v176
	v_max_f32_e32 v208, 0, v177
	v_fma_f32 v201, v144, v204, 0
	v_max_f32_e32 v204, 0, v178
	v_fmac_f32_e32 v201, v145, v208
	v_max_f32_e32 v208, 0, v179
	v_fmac_f32_e32 v201, v146, v204
	v_max_f32_e32 v204, 0, v180
	v_fmac_f32_e32 v201, v147, v208
	v_max_f32_e32 v208, 0, v181
	v_fmac_f32_e32 v201, v148, v204
	v_max_f32_e32 v204, 0, v182
	v_fmac_f32_e32 v201, v149, v208
	v_max_f32_e32 v208, 0, v183
	v_fmac_f32_e32 v201, v150, v204
	v_max_f32_e32 v204, 0, v184
	v_fmac_f32_e32 v201, v151, v208
	v_max_f32_e32 v208, 0, v185
	v_fmac_f32_e32 v201, v152, v204
	v_max_f32_e32 v204, 0, v186
	v_fmac_f32_e32 v201, v153, v208
	v_max_f32_e32 v208, 0, v187
	v_fmac_f32_e32 v201, v154, v204
	v_max_f32_e32 v204, 0, v188
	v_fmac_f32_e32 v201, v155, v208
	v_max_f32_e32 v208, 0, v189
	v_fmac_f32_e32 v201, v156, v204
	v_max_f32_e32 v204, 0, v190
	v_fmac_f32_e32 v201, v157, v208
	v_max_f32_e32 v208, 0, v191
	v_fmac_f32_e32 v201, v158, v204
	v_fmac_f32_e32 v201, v159, v208
	v_cndmask_b32_e32 v201, v61, v201, vcc
	v_ashrrev_i32_e32 v207, 31, v201
	v_or_b32_e32 v207, 0x80000000, v207
	v_xor_b32_e32 v79, v201, v207
	s_branch .Lidx_search
.Lidx_fin1:
	s_cmp_lg_u32 s15, 8
	s_cbranch_scc1 .Lidx_search
	s_nop 15
	v_cmp_le_i32_e32 vcc, 0xe0, v59
	v_max_f32_e32 v204, 0, v176
	v_max_f32_e32 v208, 0, v177
	v_fma_f32 v201, v144, v204, 0
	v_max_f32_e32 v204, 0, v178
	v_fmac_f32_e32 v201, v145, v208
	v_max_f32_e32 v208, 0, v179
	v_fmac_f32_e32 v201, v146, v204
	v_max_f32_e32 v204, 0, v180
	v_fmac_f32_e32 v201, v147, v208
	v_max_f32_e32 v208, 0, v181
	v_fmac_f32_e32 v201, v148, v204
	v_max_f32_e32 v204, 0, v182
	v_fmac_f32_e32 v201, v149, v208
	v_max_f32_e32 v208, 0, v183
	v_fmac_f32_e32 v201, v150, v204
	v_max_f32_e32 v204, 0, v184
	v_fmac_f32_e32 v201, v151, v208
	v_max_f32_e32 v208, 0, v185
	v_fmac_f32_e32 v201, v152, v204
	v_max_f32_e32 v204, 0, v186
	v_fmac_f32_e32 v201, v153, v208
	v_max_f32_e32 v208, 0, v187
	v_fmac_f32_e32 v201, v154, v204
	v_max_f32_e32 v204, 0, v188
	v_fmac_f32_e32 v201, v155, v208
	v_max_f32_e32 v208, 0, v189
	v_fmac_f32_e32 v201, v156, v204
	v_max_f32_e32 v204, 0, v190
	v_fmac_f32_e32 v201, v157, v208
	v_max_f32_e32 v208, 0, v191
	v_fmac_f32_e32 v201, v158, v204
	v_fmac_f32_e32 v201, v159, v208
	v_cndmask_b32_e32 v201, v61, v201, vcc
	v_ashrrev_i32_e32 v207, 31, v201
	v_or_b32_e32 v207, 0x80000000, v207
	v_xor_b32_e32 v71, v201, v207
	s_branch .Lidx_search
.Lidx_x1:
	s_nop 15
	v_cmp_le_i32_e32 vcc, 0, v59
	v_max_f32_e32 v204, 0, v160
	v_max_f32_e32 v208, 0, v161
	v_fma_f32 v201, v144, v204, 0
	v_max_f32_e32 v204, 0, v162
	v_fmac_f32_e32 v201, v145, v208
	v_max_f32_e32 v208, 0, v163
	v_fmac_f32_e32 v201, v146, v204
	v_max_f32_e32 v204, 0, v164
	v_fmac_f32_e32 v201, v147, v208
	v_max_f32_e32 v208, 0, v165
	v_fmac_f32_e32 v201, v148, v204
	v_max_f32_e32 v204, 0, v166
	v_fmac_f32_e32 v201, v149, v208
	v_max_f32_e32 v208, 0, v167
	v_fmac_f32_e32 v201, v150, v204
	v_max_f32_e32 v204, 0, v168
	v_fmac_f32_e32 v201, v151, v208
	v_max_f32_e32 v208, 0, v169
	v_fmac_f32_e32 v201, v152, v204
	v_max_f32_e32 v204, 0, v170
	v_fmac_f32_e32 v201, v153, v208
	v_max_f32_e32 v208, 0, v171
	v_fmac_f32_e32 v201, v154, v204
	v_max_f32_e32 v204, 0, v172
	v_fmac_f32_e32 v201, v155, v208
	v_max_f32_e32 v208, 0, v173
	v_fmac_f32_e32 v201, v156, v204
	v_max_f32_e32 v204, 0, v174
	v_fmac_f32_e32 v201, v157, v208
	v_max_f32_e32 v208, 0, v175
	v_fmac_f32_e32 v201, v158, v204
	v_fmac_f32_e32 v201, v159, v208
	v_cndmask_b32_e32 v201, v61, v201, vcc
	v_ashrrev_i32_e32 v207, 31, v201
	v_or_b32_e32 v207, 0x80000000, v207
	v_xor_b32_e32 v64, v201, v207
	s_branch .Lidx_ce0
.Lidx_x2:
	s_nop 15
	v_cmp_le_i32_e32 vcc, 32, v59
	v_max_f32_e32 v204, 0, v176
	v_max_f32_e32 v208, 0, v177
	v_fma_f32 v201, v144, v204, 0
	v_max_f32_e32 v204, 0, v178
	v_fmac_f32_e32 v201, v145, v208
	v_max_f32_e32 v208, 0, v179
	v_fmac_f32_e32 v201, v146, v204
	v_max_f32_e32 v204, 0, v180
	v_fmac_f32_e32 v201, v147, v208
	v_max_f32_e32 v208, 0, v181
	v_fmac_f32_e32 v201, v148, v204
	v_max_f32_e32 v204, 0, v182
	v_fmac_f32_e32 v201, v149, v208
	v_max_f32_e32 v208, 0, v183
	v_fmac_f32_e32 v201, v150, v204
	v_max_f32_e32 v204, 0, v184
	v_fmac_f32_e32 v201, v151, v208
	v_max_f32_e32 v208, 0, v185
	v_fmac_f32_e32 v201, v152, v204
	v_max_f32_e32 v204, 0, v186
	v_fmac_f32_e32 v201, v153, v208
	v_max_f32_e32 v208, 0, v187
	v_fmac_f32_e32 v201, v154, v204
	v_max_f32_e32 v204, 0, v188
	v_fmac_f32_e32 v201, v155, v208
	v_max_f32_e32 v208, 0, v189
	v_fmac_f32_e32 v201, v156, v204
	v_max_f32_e32 v204, 0, v190
	v_fmac_f32_e32 v201, v157, v208
	v_max_f32_e32 v208, 0, v191
	v_fmac_f32_e32 v201, v158, v204
	v_fmac_f32_e32 v201, v159, v208
	v_cndmask_b32_e32 v201, v61, v201, vcc
	v_ashrrev_i32_e32 v207, 31, v201
	v_or_b32_e32 v207, 0x80000000, v207
	v_xor_b32_e32 v65, v201, v207
	s_branch .Lidx_ce0
.Lidx_x3:
	s_nop 15
	v_cmp_le_i32_e32 vcc, 64, v59
	v_max_f32_e32 v204, 0, v160
	v_max_f32_e32 v208, 0, v161
	v_fma_f32 v201, v144, v204, 0
	v_max_f32_e32 v204, 0, v162
	v_fmac_f32_e32 v201, v145, v208
	v_max_f32_e32 v208, 0, v163
	v_fmac_f32_e32 v201, v146, v204
	v_max_f32_e32 v204, 0, v164
	v_fmac_f32_e32 v201, v147, v208
	v_max_f32_e32 v208, 0, v165
	v_fmac_f32_e32 v201, v148, v204
	v_max_f32_e32 v204, 0, v166
	v_fmac_f32_e32 v201, v149, v208
	v_max_f32_e32 v208, 0, v167
	v_fmac_f32_e32 v201, v150, v204
	v_max_f32_e32 v204, 0, v168
	v_fmac_f32_e32 v201, v151, v208
	v_max_f32_e32 v208, 0, v169
	v_fmac_f32_e32 v201, v152, v204
	v_max_f32_e32 v204, 0, v170
	v_fmac_f32_e32 v201, v153, v208
	v_max_f32_e32 v208, 0, v171
	v_fmac_f32_e32 v201, v154, v204
	v_max_f32_e32 v204, 0, v172
	v_fmac_f32_e32 v201, v155, v208
	v_max_f32_e32 v208, 0, v173
	v_fmac_f32_e32 v201, v156, v204
	v_max_f32_e32 v204, 0, v174
	v_fmac_f32_e32 v201, v157, v208
	v_max_f32_e32 v208, 0, v175
	v_fmac_f32_e32 v201, v158, v204
	v_fmac_f32_e32 v201, v159, v208
	v_cndmask_b32_e32 v201, v61, v201, vcc
	v_ashrrev_i32_e32 v207, 31, v201
	v_or_b32_e32 v207, 0x80000000, v207
	v_xor_b32_e32 v66, v201, v207
	s_branch .Lidx_ce0
.Lidx_x4:
	s_nop 15
	v_cmp_le_i32_e32 vcc, 0x60, v59
	v_max_f32_e32 v204, 0, v176
	v_max_f32_e32 v208, 0, v177
	v_fma_f32 v201, v144, v204, 0
	v_max_f32_e32 v204, 0, v178
	v_fmac_f32_e32 v201, v145, v208
	v_max_f32_e32 v208, 0, v179
	v_fmac_f32_e32 v201, v146, v204
	v_max_f32_e32 v204, 0, v180
	v_fmac_f32_e32 v201, v147, v208
	v_max_f32_e32 v208, 0, v181
	v_fmac_f32_e32 v201, v148, v204
	v_max_f32_e32 v204, 0, v182
	v_fmac_f32_e32 v201, v149, v208
	v_max_f32_e32 v208, 0, v183
	v_fmac_f32_e32 v201, v150, v204
	v_max_f32_e32 v204, 0, v184
	v_fmac_f32_e32 v201, v151, v208
	v_max_f32_e32 v208, 0, v185
	v_fmac_f32_e32 v201, v152, v204
	v_max_f32_e32 v204, 0, v186
	v_fmac_f32_e32 v201, v153, v208
	v_max_f32_e32 v208, 0, v187
	v_fmac_f32_e32 v201, v154, v204
	v_max_f32_e32 v204, 0, v188
	v_fmac_f32_e32 v201, v155, v208
	v_max_f32_e32 v208, 0, v189
	v_fmac_f32_e32 v201, v156, v204
	v_max_f32_e32 v204, 0, v190
	v_fmac_f32_e32 v201, v157, v208
	v_max_f32_e32 v208, 0, v191
	v_fmac_f32_e32 v201, v158, v204
	v_fmac_f32_e32 v201, v159, v208
	v_cndmask_b32_e32 v201, v61, v201, vcc
	v_ashrrev_i32_e32 v207, 31, v201
	v_or_b32_e32 v207, 0x80000000, v207
	v_xor_b32_e32 v67, v201, v207
	s_branch .Lidx_ce0
.Lidx_x5:
	s_nop 15
	v_cmp_le_i32_e32 vcc, 0x80, v59
	v_max_f32_e32 v204, 0, v160
	v_max_f32_e32 v208, 0, v161
	v_fma_f32 v201, v144, v204, 0
	v_max_f32_e32 v204, 0, v162
	v_fmac_f32_e32 v201, v145, v208
	v_max_f32_e32 v208, 0, v163
	v_fmac_f32_e32 v201, v146, v204
	v_max_f32_e32 v204, 0, v164
	v_fmac_f32_e32 v201, v147, v208
	v_max_f32_e32 v208, 0, v165
	v_fmac_f32_e32 v201, v148, v204
	v_max_f32_e32 v204, 0, v166
	v_fmac_f32_e32 v201, v149, v208
	v_max_f32_e32 v208, 0, v167
	v_fmac_f32_e32 v201, v150, v204
	v_max_f32_e32 v204, 0, v168
	v_fmac_f32_e32 v201, v151, v208
	v_max_f32_e32 v208, 0, v169
	v_fmac_f32_e32 v201, v152, v204
	v_max_f32_e32 v204, 0, v170
	v_fmac_f32_e32 v201, v153, v208
	v_max_f32_e32 v208, 0, v171
	v_fmac_f32_e32 v201, v154, v204
	v_max_f32_e32 v204, 0, v172
	v_fmac_f32_e32 v201, v155, v208
	v_max_f32_e32 v208, 0, v173
	v_fmac_f32_e32 v201, v156, v204
	v_max_f32_e32 v204, 0, v174
	v_fmac_f32_e32 v201, v157, v208
	v_max_f32_e32 v208, 0, v175
	v_fmac_f32_e32 v201, v158, v204
	v_fmac_f32_e32 v201, v159, v208
	v_cndmask_b32_e32 v201, v61, v201, vcc
	v_ashrrev_i32_e32 v207, 31, v201
	v_or_b32_e32 v207, 0x80000000, v207
	v_xor_b32_e32 v68, v201, v207
	s_branch .Lidx_ce0
.Lidx_x6:
	s_nop 15
	v_cmp_le_i32_e32 vcc, 0xa0, v59
	v_max_f32_e32 v204, 0, v176
	v_max_f32_e32 v208, 0, v177
	v_fma_f32 v201, v144, v204, 0
	v_max_f32_e32 v204, 0, v178
	v_fmac_f32_e32 v201, v145, v208
	v_max_f32_e32 v208, 0, v179
	v_fmac_f32_e32 v201, v146, v204
	v_max_f32_e32 v204, 0, v180
	v_fmac_f32_e32 v201, v147, v208
	v_max_f32_e32 v208, 0, v181
	v_fmac_f32_e32 v201, v148, v204
	v_max_f32_e32 v204, 0, v182
	v_fmac_f32_e32 v201, v149, v208
	v_max_f32_e32 v208, 0, v183
	v_fmac_f32_e32 v201, v150, v204
	v_max_f32_e32 v204, 0, v184
	v_fmac_f32_e32 v201, v151, v208
	v_max_f32_e32 v208, 0, v185
	v_fmac_f32_e32 v201, v152, v204
	v_max_f32_e32 v204, 0, v186
	v_fmac_f32_e32 v201, v153, v208
	v_max_f32_e32 v208, 0, v187
	v_fmac_f32_e32 v201, v154, v204
	v_max_f32_e32 v204, 0, v188
	v_fmac_f32_e32 v201, v155, v208
	v_max_f32_e32 v208, 0, v189
	v_fmac_f32_e32 v201, v156, v204
	v_max_f32_e32 v204, 0, v190
	v_fmac_f32_e32 v201, v157, v208
	v_max_f32_e32 v208, 0, v191
	v_fmac_f32_e32 v201, v158, v204
	v_fmac_f32_e32 v201, v159, v208
	v_cndmask_b32_e32 v201, v61, v201, vcc
	v_ashrrev_i32_e32 v207, 31, v201
	v_or_b32_e32 v207, 0x80000000, v207
	v_xor_b32_e32 v69, v201, v207
	s_branch .Lidx_ce0
.Lidx_x7:
	s_nop 15
	v_cmp_le_i32_e32 vcc, 0xc0, v59
	v_max_f32_e32 v204, 0, v160
	v_max_f32_e32 v208, 0, v161
	v_fma_f32 v201, v144, v204, 0
	v_max_f32_e32 v204, 0, v162
	v_fmac_f32_e32 v201, v145, v208
	v_max_f32_e32 v208, 0, v163
	v_fmac_f32_e32 v201, v146, v204
	v_max_f32_e32 v204, 0, v164
	v_fmac_f32_e32 v201, v147, v208
	v_max_f32_e32 v208, 0, v165
	v_fmac_f32_e32 v201, v148, v204
	v_max_f32_e32 v204, 0, v166
	v_fmac_f32_e32 v201, v149, v208
	v_max_f32_e32 v208, 0, v167
	v_fmac_f32_e32 v201, v150, v204
	v_max_f32_e32 v204, 0, v168
	v_fmac_f32_e32 v201, v151, v208
	v_max_f32_e32 v208, 0, v169
	v_fmac_f32_e32 v201, v152, v204
	v_max_f32_e32 v204, 0, v170
	v_fmac_f32_e32 v201, v153, v208
	v_max_f32_e32 v208, 0, v171
	v_fmac_f32_e32 v201, v154, v204
	v_max_f32_e32 v204, 0, v172
	v_fmac_f32_e32 v201, v155, v208
	v_max_f32_e32 v208, 0, v173
	v_fmac_f32_e32 v201, v156, v204
	v_max_f32_e32 v204, 0, v174
	v_fmac_f32_e32 v201, v157, v208
	v_max_f32_e32 v208, 0, v175
	v_fmac_f32_e32 v201, v158, v204
	v_fmac_f32_e32 v201, v159, v208
	v_cndmask_b32_e32 v201, v61, v201, vcc
	v_ashrrev_i32_e32 v207, 31, v201
	v_or_b32_e32 v207, 0x80000000, v207
	v_xor_b32_e32 v70, v201, v207
	s_branch .Lidx_ce0
.Lidx_x8:
	s_nop 15
	v_cmp_le_i32_e32 vcc, 0xe0, v59
	v_max_f32_e32 v204, 0, v176
	v_max_f32_e32 v208, 0, v177
	v_fma_f32 v201, v144, v204, 0
	v_max_f32_e32 v204, 0, v178
	v_fmac_f32_e32 v201, v145, v208
	v_max_f32_e32 v208, 0, v179
	v_fmac_f32_e32 v201, v146, v204
	v_max_f32_e32 v204, 0, v180
	v_fmac_f32_e32 v201, v147, v208
	v_max_f32_e32 v208, 0, v181
	v_fmac_f32_e32 v201, v148, v204
	v_max_f32_e32 v204, 0, v182
	v_fmac_f32_e32 v201, v149, v208
	v_max_f32_e32 v208, 0, v183
	v_fmac_f32_e32 v201, v150, v204
	v_max_f32_e32 v204, 0, v184
	v_fmac_f32_e32 v201, v151, v208
	v_max_f32_e32 v208, 0, v185
	v_fmac_f32_e32 v201, v152, v204
	v_max_f32_e32 v204, 0, v186
	v_fmac_f32_e32 v201, v153, v208
	v_max_f32_e32 v208, 0, v187
	v_fmac_f32_e32 v201, v154, v204
	v_max_f32_e32 v204, 0, v188
	v_fmac_f32_e32 v201, v155, v208
	v_max_f32_e32 v208, 0, v189
	v_fmac_f32_e32 v201, v156, v204
	v_max_f32_e32 v204, 0, v190
	v_fmac_f32_e32 v201, v157, v208
	v_max_f32_e32 v208, 0, v191
	v_fmac_f32_e32 v201, v158, v204
	v_fmac_f32_e32 v201, v159, v208
	v_cndmask_b32_e32 v201, v61, v201, vcc
	v_ashrrev_i32_e32 v207, 31, v201
	v_or_b32_e32 v207, 0x80000000, v207
	v_xor_b32_e32 v71, v201, v207
	s_branch .Lidx_ce1
.Lidx_x9:
	s_nop 15
	v_cmp_le_i32_e32 vcc, 0x100, v59
	v_max_f32_e32 v204, 0, v160
	v_max_f32_e32 v208, 0, v161
	v_fma_f32 v201, v144, v204, 0
	v_max_f32_e32 v204, 0, v162
	v_fmac_f32_e32 v201, v145, v208
	v_max_f32_e32 v208, 0, v163
	v_fmac_f32_e32 v201, v146, v204
	v_max_f32_e32 v204, 0, v164
	v_fmac_f32_e32 v201, v147, v208
	v_max_f32_e32 v208, 0, v165
	v_fmac_f32_e32 v201, v148, v204
	v_max_f32_e32 v204, 0, v166
	v_fmac_f32_e32 v201, v149, v208
	v_max_f32_e32 v208, 0, v167
	v_fmac_f32_e32 v201, v150, v204
	v_max_f32_e32 v204, 0, v168
	v_fmac_f32_e32 v201, v151, v208
	v_max_f32_e32 v208, 0, v169
	v_fmac_f32_e32 v201, v152, v204
	v_max_f32_e32 v204, 0, v170
	v_fmac_f32_e32 v201, v153, v208
	v_max_f32_e32 v208, 0, v171
	v_fmac_f32_e32 v201, v154, v204
	v_max_f32_e32 v204, 0, v172
	v_fmac_f32_e32 v201, v155, v208
	v_max_f32_e32 v208, 0, v173
	v_fmac_f32_e32 v201, v156, v204
	v_max_f32_e32 v204, 0, v174
	v_fmac_f32_e32 v201, v157, v208
	v_max_f32_e32 v208, 0, v175
	v_fmac_f32_e32 v201, v158, v204
	v_fmac_f32_e32 v201, v159, v208
	v_cndmask_b32_e32 v201, v61, v201, vcc
	v_ashrrev_i32_e32 v207, 31, v201
	v_or_b32_e32 v207, 0x80000000, v207
	v_xor_b32_e32 v72, v201, v207
	s_branch .Lidx_ce1
.Lidx_x10:
	s_nop 15
	v_cmp_le_i32_e32 vcc, 0x120, v59
	v_max_f32_e32 v204, 0, v176
	v_max_f32_e32 v208, 0, v177
	v_fma_f32 v201, v144, v204, 0
	v_max_f32_e32 v204, 0, v178
	v_fmac_f32_e32 v201, v145, v208
	v_max_f32_e32 v208, 0, v179
	v_fmac_f32_e32 v201, v146, v204
	v_max_f32_e32 v204, 0, v180
	v_fmac_f32_e32 v201, v147, v208
	v_max_f32_e32 v208, 0, v181
	v_fmac_f32_e32 v201, v148, v204
	v_max_f32_e32 v204, 0, v182
	v_fmac_f32_e32 v201, v149, v208
	v_max_f32_e32 v208, 0, v183
	v_fmac_f32_e32 v201, v150, v204
	v_max_f32_e32 v204, 0, v184
	v_fmac_f32_e32 v201, v151, v208
	v_max_f32_e32 v208, 0, v185
	v_fmac_f32_e32 v201, v152, v204
	v_max_f32_e32 v204, 0, v186
	v_fmac_f32_e32 v201, v153, v208
	v_max_f32_e32 v208, 0, v187
	v_fmac_f32_e32 v201, v154, v204
	v_max_f32_e32 v204, 0, v188
	v_fmac_f32_e32 v201, v155, v208
	v_max_f32_e32 v208, 0, v189
	v_fmac_f32_e32 v201, v156, v204
	v_max_f32_e32 v204, 0, v190
	v_fmac_f32_e32 v201, v157, v208
	v_max_f32_e32 v208, 0, v191
	v_fmac_f32_e32 v201, v158, v204
	v_fmac_f32_e32 v201, v159, v208
	v_cndmask_b32_e32 v201, v61, v201, vcc
	v_ashrrev_i32_e32 v207, 31, v201
	v_or_b32_e32 v207, 0x80000000, v207
	v_xor_b32_e32 v73, v201, v207
	s_branch .Lidx_ce1
.Lidx_x11:
	s_nop 15
	v_cmp_le_i32_e32 vcc, 0x140, v59
	v_max_f32_e32 v204, 0, v160
	v_max_f32_e32 v208, 0, v161
	v_fma_f32 v201, v144, v204, 0
	v_max_f32_e32 v204, 0, v162
	v_fmac_f32_e32 v201, v145, v208
	v_max_f32_e32 v208, 0, v163
	v_fmac_f32_e32 v201, v146, v204
	v_max_f32_e32 v204, 0, v164
	v_fmac_f32_e32 v201, v147, v208
	v_max_f32_e32 v208, 0, v165
	v_fmac_f32_e32 v201, v148, v204
	v_max_f32_e32 v204, 0, v166
	v_fmac_f32_e32 v201, v149, v208
	v_max_f32_e32 v208, 0, v167
	v_fmac_f32_e32 v201, v150, v204
	v_max_f32_e32 v204, 0, v168
	v_fmac_f32_e32 v201, v151, v208
	v_max_f32_e32 v208, 0, v169
	v_fmac_f32_e32 v201, v152, v204
	v_max_f32_e32 v204, 0, v170
	v_fmac_f32_e32 v201, v153, v208
	v_max_f32_e32 v208, 0, v171
	v_fmac_f32_e32 v201, v154, v204
	v_max_f32_e32 v204, 0, v172
	v_fmac_f32_e32 v201, v155, v208
	v_max_f32_e32 v208, 0, v173
	v_fmac_f32_e32 v201, v156, v204
	v_max_f32_e32 v204, 0, v174
	v_fmac_f32_e32 v201, v157, v208
	v_max_f32_e32 v208, 0, v175
	v_fmac_f32_e32 v201, v158, v204
	v_fmac_f32_e32 v201, v159, v208
	v_cndmask_b32_e32 v201, v61, v201, vcc
	v_ashrrev_i32_e32 v207, 31, v201
	v_or_b32_e32 v207, 0x80000000, v207
	v_xor_b32_e32 v74, v201, v207
	s_branch .Lidx_ce1
.Lidx_x12:
	s_nop 15
	v_cmp_le_i32_e32 vcc, 0x160, v59
	v_max_f32_e32 v204, 0, v176
	v_max_f32_e32 v208, 0, v177
	v_fma_f32 v201, v144, v204, 0
	v_max_f32_e32 v204, 0, v178
	v_fmac_f32_e32 v201, v145, v208
	v_max_f32_e32 v208, 0, v179
	v_fmac_f32_e32 v201, v146, v204
	v_max_f32_e32 v204, 0, v180
	v_fmac_f32_e32 v201, v147, v208
	v_max_f32_e32 v208, 0, v181
	v_fmac_f32_e32 v201, v148, v204
	v_max_f32_e32 v204, 0, v182
	v_fmac_f32_e32 v201, v149, v208
	v_max_f32_e32 v208, 0, v183
	v_fmac_f32_e32 v201, v150, v204
	v_max_f32_e32 v204, 0, v184
	v_fmac_f32_e32 v201, v151, v208
	v_max_f32_e32 v208, 0, v185
	v_fmac_f32_e32 v201, v152, v204
	v_max_f32_e32 v204, 0, v186
	v_fmac_f32_e32 v201, v153, v208
	v_max_f32_e32 v208, 0, v187
	v_fmac_f32_e32 v201, v154, v204
	v_max_f32_e32 v204, 0, v188
	v_fmac_f32_e32 v201, v155, v208
	v_max_f32_e32 v208, 0, v189
	v_fmac_f32_e32 v201, v156, v204
	v_max_f32_e32 v204, 0, v190
	v_fmac_f32_e32 v201, v157, v208
	v_max_f32_e32 v208, 0, v191
	v_fmac_f32_e32 v201, v158, v204
	v_fmac_f32_e32 v201, v159, v208
	v_cndmask_b32_e32 v201, v61, v201, vcc
	v_ashrrev_i32_e32 v207, 31, v201
	v_or_b32_e32 v207, 0x80000000, v207
	v_xor_b32_e32 v75, v201, v207
	s_branch .Lidx_ce1
.Lidx_x13:
	s_nop 15
	v_cmp_le_i32_e32 vcc, 0x180, v59
	v_max_f32_e32 v204, 0, v160
	v_max_f32_e32 v208, 0, v161
	v_fma_f32 v201, v144, v204, 0
	v_max_f32_e32 v204, 0, v162
	v_fmac_f32_e32 v201, v145, v208
	v_max_f32_e32 v208, 0, v163
	v_fmac_f32_e32 v201, v146, v204
	v_max_f32_e32 v204, 0, v164
	v_fmac_f32_e32 v201, v147, v208
	v_max_f32_e32 v208, 0, v165
	v_fmac_f32_e32 v201, v148, v204
	v_max_f32_e32 v204, 0, v166
	v_fmac_f32_e32 v201, v149, v208
	v_max_f32_e32 v208, 0, v167
	v_fmac_f32_e32 v201, v150, v204
	v_max_f32_e32 v204, 0, v168
	v_fmac_f32_e32 v201, v151, v208
	v_max_f32_e32 v208, 0, v169
	v_fmac_f32_e32 v201, v152, v204
	v_max_f32_e32 v204, 0, v170
	v_fmac_f32_e32 v201, v153, v208
	v_max_f32_e32 v208, 0, v171
	v_fmac_f32_e32 v201, v154, v204
	v_max_f32_e32 v204, 0, v172
	v_fmac_f32_e32 v201, v155, v208
	v_max_f32_e32 v208, 0, v173
	v_fmac_f32_e32 v201, v156, v204
	v_max_f32_e32 v204, 0, v174
	v_fmac_f32_e32 v201, v157, v208
	v_max_f32_e32 v208, 0, v175
	v_fmac_f32_e32 v201, v158, v204
	v_fmac_f32_e32 v201, v159, v208
	v_cndmask_b32_e32 v201, v61, v201, vcc
	v_ashrrev_i32_e32 v207, 31, v201
	v_or_b32_e32 v207, 0x80000000, v207
	v_xor_b32_e32 v76, v201, v207
	s_branch .Lidx_ce1
.Lidx_x14:
	s_nop 15
	v_cmp_le_i32_e32 vcc, 0x1a0, v59
	v_max_f32_e32 v204, 0, v176
	v_max_f32_e32 v208, 0, v177
	v_fma_f32 v201, v144, v204, 0
	v_max_f32_e32 v204, 0, v178
	v_fmac_f32_e32 v201, v145, v208
	v_max_f32_e32 v208, 0, v179
	v_fmac_f32_e32 v201, v146, v204
	v_max_f32_e32 v204, 0, v180
	v_fmac_f32_e32 v201, v147, v208
	v_max_f32_e32 v208, 0, v181
	v_fmac_f32_e32 v201, v148, v204
	v_max_f32_e32 v204, 0, v182
	v_fmac_f32_e32 v201, v149, v208
	v_max_f32_e32 v208, 0, v183
	v_fmac_f32_e32 v201, v150, v204
	v_max_f32_e32 v204, 0, v184
	v_fmac_f32_e32 v201, v151, v208
	v_max_f32_e32 v208, 0, v185
	v_fmac_f32_e32 v201, v152, v204
	v_max_f32_e32 v204, 0, v186
	v_fmac_f32_e32 v201, v153, v208
	v_max_f32_e32 v208, 0, v187
	v_fmac_f32_e32 v201, v154, v204
	v_max_f32_e32 v204, 0, v188
	v_fmac_f32_e32 v201, v155, v208
	v_max_f32_e32 v208, 0, v189
	v_fmac_f32_e32 v201, v156, v204
	v_max_f32_e32 v204, 0, v190
	v_fmac_f32_e32 v201, v157, v208
	v_max_f32_e32 v208, 0, v191
	v_fmac_f32_e32 v201, v158, v204
	v_fmac_f32_e32 v201, v159, v208
	v_cndmask_b32_e32 v201, v61, v201, vcc
	v_ashrrev_i32_e32 v207, 31, v201
	v_or_b32_e32 v207, 0x80000000, v207
	v_xor_b32_e32 v77, v201, v207
	s_branch .Lidx_ce1
.Lidx_x15:
	s_nop 15
	v_cmp_le_i32_e32 vcc, 0x1c0, v59
	v_max_f32_e32 v204, 0, v160
	v_max_f32_e32 v208, 0, v161
	v_fma_f32 v201, v144, v204, 0
	v_max_f32_e32 v204, 0, v162
	v_fmac_f32_e32 v201, v145, v208
	v_max_f32_e32 v208, 0, v163
	v_fmac_f32_e32 v201, v146, v204
	v_max_f32_e32 v204, 0, v164
	v_fmac_f32_e32 v201, v147, v208
	v_max_f32_e32 v208, 0, v165
	v_fmac_f32_e32 v201, v148, v204
	v_max_f32_e32 v204, 0, v166
	v_fmac_f32_e32 v201, v149, v208
	v_max_f32_e32 v208, 0, v167
	v_fmac_f32_e32 v201, v150, v204
	v_max_f32_e32 v204, 0, v168
	v_fmac_f32_e32 v201, v151, v208
	v_max_f32_e32 v208, 0, v169
	v_fmac_f32_e32 v201, v152, v204
	v_max_f32_e32 v204, 0, v170
	v_fmac_f32_e32 v201, v153, v208
	v_max_f32_e32 v208, 0, v171
	v_fmac_f32_e32 v201, v154, v204
	v_max_f32_e32 v204, 0, v172
	v_fmac_f32_e32 v201, v155, v208
	v_max_f32_e32 v208, 0, v173
	v_fmac_f32_e32 v201, v156, v204
	v_max_f32_e32 v204, 0, v174
	v_fmac_f32_e32 v201, v157, v208
	v_max_f32_e32 v208, 0, v175
	v_fmac_f32_e32 v201, v158, v204
	v_fmac_f32_e32 v201, v159, v208
	v_cndmask_b32_e32 v201, v61, v201, vcc
	v_ashrrev_i32_e32 v207, 31, v201
	v_or_b32_e32 v207, 0x80000000, v207
	v_xor_b32_e32 v78, v201, v207
	s_branch .Lidx_ce1
.Lidx_x16:
	s_nop 15
	v_cmp_le_i32_e32 vcc, 0x1e0, v59
	v_max_f32_e32 v204, 0, v176
	v_max_f32_e32 v208, 0, v177
	v_fma_f32 v201, v144, v204, 0
	v_max_f32_e32 v204, 0, v178
	v_fmac_f32_e32 v201, v145, v208
	v_max_f32_e32 v208, 0, v179
	v_fmac_f32_e32 v201, v146, v204
	v_max_f32_e32 v204, 0, v180
	v_fmac_f32_e32 v201, v147, v208
	v_max_f32_e32 v208, 0, v181
	v_fmac_f32_e32 v201, v148, v204
	v_max_f32_e32 v204, 0, v182
	v_fmac_f32_e32 v201, v149, v208
	v_max_f32_e32 v208, 0, v183
	v_fmac_f32_e32 v201, v150, v204
	v_max_f32_e32 v204, 0, v184
	v_fmac_f32_e32 v201, v151, v208
	v_max_f32_e32 v208, 0, v185
	v_fmac_f32_e32 v201, v152, v204
	v_max_f32_e32 v204, 0, v186
	v_fmac_f32_e32 v201, v153, v208
	v_max_f32_e32 v208, 0, v187
	v_fmac_f32_e32 v201, v154, v204
	v_max_f32_e32 v204, 0, v188
	v_fmac_f32_e32 v201, v155, v208
	v_max_f32_e32 v208, 0, v189
	v_fmac_f32_e32 v201, v156, v204
	v_max_f32_e32 v204, 0, v190
	v_fmac_f32_e32 v201, v157, v208
	v_max_f32_e32 v208, 0, v191
	v_fmac_f32_e32 v201, v158, v204
	v_fmac_f32_e32 v201, v159, v208
	v_cndmask_b32_e32 v201, v61, v201, vcc
	v_ashrrev_i32_e32 v207, 31, v201
	v_or_b32_e32 v207, 0x80000000, v207
	v_xor_b32_e32 v79, v201, v207
	s_branch .Lidx_ce2
.Lidx_x17:
	s_nop 15
	v_cmp_le_i32_e32 vcc, 0x200, v59
	v_max_f32_e32 v204, 0, v160
	v_max_f32_e32 v208, 0, v161
	v_fma_f32 v201, v144, v204, 0
	v_max_f32_e32 v204, 0, v162
	v_fmac_f32_e32 v201, v145, v208
	v_max_f32_e32 v208, 0, v163
	v_fmac_f32_e32 v201, v146, v204
	v_max_f32_e32 v204, 0, v164
	v_fmac_f32_e32 v201, v147, v208
	v_max_f32_e32 v208, 0, v165
	v_fmac_f32_e32 v201, v148, v204
	v_max_f32_e32 v204, 0, v166
	v_fmac_f32_e32 v201, v149, v208
	v_max_f32_e32 v208, 0, v167
	v_fmac_f32_e32 v201, v150, v204
	v_max_f32_e32 v204, 0, v168
	v_fmac_f32_e32 v201, v151, v208
	v_max_f32_e32 v208, 0, v169
	v_fmac_f32_e32 v201, v152, v204
	v_max_f32_e32 v204, 0, v170
	v_fmac_f32_e32 v201, v153, v208
	v_max_f32_e32 v208, 0, v171
	v_fmac_f32_e32 v201, v154, v204
	v_max_f32_e32 v204, 0, v172
	v_fmac_f32_e32 v201, v155, v208
	v_max_f32_e32 v208, 0, v173
	v_fmac_f32_e32 v201, v156, v204
	v_max_f32_e32 v204, 0, v174
	v_fmac_f32_e32 v201, v157, v208
	v_max_f32_e32 v208, 0, v175
	v_fmac_f32_e32 v201, v158, v204
	v_fmac_f32_e32 v201, v159, v208
	v_cndmask_b32_e32 v201, v61, v201, vcc
	v_ashrrev_i32_e32 v207, 31, v201
	v_or_b32_e32 v207, 0x80000000, v207
	v_xor_b32_e32 v80, v201, v207
	s_branch .Lidx_ce2
.Lidx_x18:
	s_nop 15
	v_cmp_le_i32_e32 vcc, 0x220, v59
	v_max_f32_e32 v204, 0, v176
	v_max_f32_e32 v208, 0, v177
	v_fma_f32 v201, v144, v204, 0
	v_max_f32_e32 v204, 0, v178
	v_fmac_f32_e32 v201, v145, v208
	v_max_f32_e32 v208, 0, v179
	v_fmac_f32_e32 v201, v146, v204
	v_max_f32_e32 v204, 0, v180
	v_fmac_f32_e32 v201, v147, v208
	v_max_f32_e32 v208, 0, v181
	v_fmac_f32_e32 v201, v148, v204
	v_max_f32_e32 v204, 0, v182
	v_fmac_f32_e32 v201, v149, v208
	v_max_f32_e32 v208, 0, v183
	v_fmac_f32_e32 v201, v150, v204
	v_max_f32_e32 v204, 0, v184
	v_fmac_f32_e32 v201, v151, v208
	v_max_f32_e32 v208, 0, v185
	v_fmac_f32_e32 v201, v152, v204
	v_max_f32_e32 v204, 0, v186
	v_fmac_f32_e32 v201, v153, v208
	v_max_f32_e32 v208, 0, v187
	v_fmac_f32_e32 v201, v154, v204
	v_max_f32_e32 v204, 0, v188
	v_fmac_f32_e32 v201, v155, v208
	v_max_f32_e32 v208, 0, v189
	v_fmac_f32_e32 v201, v156, v204
	v_max_f32_e32 v204, 0, v190
	v_fmac_f32_e32 v201, v157, v208
	v_max_f32_e32 v208, 0, v191
	v_fmac_f32_e32 v201, v158, v204
	v_fmac_f32_e32 v201, v159, v208
	v_cndmask_b32_e32 v201, v61, v201, vcc
	v_ashrrev_i32_e32 v207, 31, v201
	v_or_b32_e32 v207, 0x80000000, v207
	v_xor_b32_e32 v81, v201, v207
	s_branch .Lidx_ce2
.Lidx_x19:
	s_nop 15
	v_cmp_le_i32_e32 vcc, 0x240, v59
	v_max_f32_e32 v204, 0, v160
	v_max_f32_e32 v208, 0, v161
	v_fma_f32 v201, v144, v204, 0
	v_max_f32_e32 v204, 0, v162
	v_fmac_f32_e32 v201, v145, v208
	v_max_f32_e32 v208, 0, v163
	v_fmac_f32_e32 v201, v146, v204
	v_max_f32_e32 v204, 0, v164
	v_fmac_f32_e32 v201, v147, v208
	v_max_f32_e32 v208, 0, v165
	v_fmac_f32_e32 v201, v148, v204
	v_max_f32_e32 v204, 0, v166
	v_fmac_f32_e32 v201, v149, v208
	v_max_f32_e32 v208, 0, v167
	v_fmac_f32_e32 v201, v150, v204
	v_max_f32_e32 v204, 0, v168
	v_fmac_f32_e32 v201, v151, v208
	v_max_f32_e32 v208, 0, v169
	v_fmac_f32_e32 v201, v152, v204
	v_max_f32_e32 v204, 0, v170
	v_fmac_f32_e32 v201, v153, v208
	v_max_f32_e32 v208, 0, v171
	v_fmac_f32_e32 v201, v154, v204
	v_max_f32_e32 v204, 0, v172
	v_fmac_f32_e32 v201, v155, v208
	v_max_f32_e32 v208, 0, v173
	v_fmac_f32_e32 v201, v156, v204
	v_max_f32_e32 v204, 0, v174
	v_fmac_f32_e32 v201, v157, v208
	v_max_f32_e32 v208, 0, v175
	v_fmac_f32_e32 v201, v158, v204
	v_fmac_f32_e32 v201, v159, v208
	v_cndmask_b32_e32 v201, v61, v201, vcc
	v_ashrrev_i32_e32 v207, 31, v201
	v_or_b32_e32 v207, 0x80000000, v207
	v_xor_b32_e32 v82, v201, v207
	s_branch .Lidx_ce2
.Lidx_x20:
	s_nop 15
	v_cmp_le_i32_e32 vcc, 0x260, v59
	v_max_f32_e32 v204, 0, v176
	v_max_f32_e32 v208, 0, v177
	v_fma_f32 v201, v144, v204, 0
	v_max_f32_e32 v204, 0, v178
	v_fmac_f32_e32 v201, v145, v208
	v_max_f32_e32 v208, 0, v179
	v_fmac_f32_e32 v201, v146, v204
	v_max_f32_e32 v204, 0, v180
	v_fmac_f32_e32 v201, v147, v208
	v_max_f32_e32 v208, 0, v181
	v_fmac_f32_e32 v201, v148, v204
	v_max_f32_e32 v204, 0, v182
	v_fmac_f32_e32 v201, v149, v208
	v_max_f32_e32 v208, 0, v183
	v_fmac_f32_e32 v201, v150, v204
	v_max_f32_e32 v204, 0, v184
	v_fmac_f32_e32 v201, v151, v208
	v_max_f32_e32 v208, 0, v185
	v_fmac_f32_e32 v201, v152, v204
	v_max_f32_e32 v204, 0, v186
	v_fmac_f32_e32 v201, v153, v208
	v_max_f32_e32 v208, 0, v187
	v_fmac_f32_e32 v201, v154, v204
	v_max_f32_e32 v204, 0, v188
	v_fmac_f32_e32 v201, v155, v208
	v_max_f32_e32 v208, 0, v189
	v_fmac_f32_e32 v201, v156, v204
	v_max_f32_e32 v204, 0, v190
	v_fmac_f32_e32 v201, v157, v208
	v_max_f32_e32 v208, 0, v191
	v_fmac_f32_e32 v201, v158, v204
	v_fmac_f32_e32 v201, v159, v208
	v_cndmask_b32_e32 v201, v61, v201, vcc
	v_ashrrev_i32_e32 v207, 31, v201
	v_or_b32_e32 v207, 0x80000000, v207
	v_xor_b32_e32 v83, v201, v207
	s_branch .Lidx_ce2
.Lidx_x21:
	s_nop 15
	v_cmp_le_i32_e32 vcc, 0x280, v59
	v_max_f32_e32 v204, 0, v160
	v_max_f32_e32 v208, 0, v161
	v_fma_f32 v201, v144, v204, 0
	v_max_f32_e32 v204, 0, v162
	v_fmac_f32_e32 v201, v145, v208
	v_max_f32_e32 v208, 0, v163
	v_fmac_f32_e32 v201, v146, v204
	v_max_f32_e32 v204, 0, v164
	v_fmac_f32_e32 v201, v147, v208
	v_max_f32_e32 v208, 0, v165
	v_fmac_f32_e32 v201, v148, v204
	v_max_f32_e32 v204, 0, v166
	v_fmac_f32_e32 v201, v149, v208
	v_max_f32_e32 v208, 0, v167
	v_fmac_f32_e32 v201, v150, v204
	v_max_f32_e32 v204, 0, v168
	v_fmac_f32_e32 v201, v151, v208
	v_max_f32_e32 v208, 0, v169
	v_fmac_f32_e32 v201, v152, v204
	v_max_f32_e32 v204, 0, v170
	v_fmac_f32_e32 v201, v153, v208
	v_max_f32_e32 v208, 0, v171
	v_fmac_f32_e32 v201, v154, v204
	v_max_f32_e32 v204, 0, v172
	v_fmac_f32_e32 v201, v155, v208
	v_max_f32_e32 v208, 0, v173
	v_fmac_f32_e32 v201, v156, v204
	v_max_f32_e32 v204, 0, v174
	v_fmac_f32_e32 v201, v157, v208
	v_max_f32_e32 v208, 0, v175
	v_fmac_f32_e32 v201, v158, v204
	v_fmac_f32_e32 v201, v159, v208
	v_cndmask_b32_e32 v201, v61, v201, vcc
	v_ashrrev_i32_e32 v207, 31, v201
	v_or_b32_e32 v207, 0x80000000, v207
	v_xor_b32_e32 v84, v201, v207
	s_branch .Lidx_ce2
.Lidx_x22:
	s_nop 15
	v_cmp_le_i32_e32 vcc, 0x2a0, v59
	v_max_f32_e32 v204, 0, v176
	v_max_f32_e32 v208, 0, v177
	v_fma_f32 v201, v144, v204, 0
	v_max_f32_e32 v204, 0, v178
	v_fmac_f32_e32 v201, v145, v208
	v_max_f32_e32 v208, 0, v179
	v_fmac_f32_e32 v201, v146, v204
	v_max_f32_e32 v204, 0, v180
	v_fmac_f32_e32 v201, v147, v208
	v_max_f32_e32 v208, 0, v181
	v_fmac_f32_e32 v201, v148, v204
	v_max_f32_e32 v204, 0, v182
	v_fmac_f32_e32 v201, v149, v208
	v_max_f32_e32 v208, 0, v183
	v_fmac_f32_e32 v201, v150, v204
	v_max_f32_e32 v204, 0, v184
	v_fmac_f32_e32 v201, v151, v208
	v_max_f32_e32 v208, 0, v185
	v_fmac_f32_e32 v201, v152, v204
	v_max_f32_e32 v204, 0, v186
	v_fmac_f32_e32 v201, v153, v208
	v_max_f32_e32 v208, 0, v187
	v_fmac_f32_e32 v201, v154, v204
	v_max_f32_e32 v204, 0, v188
	v_fmac_f32_e32 v201, v155, v208
	v_max_f32_e32 v208, 0, v189
	v_fmac_f32_e32 v201, v156, v204
	v_max_f32_e32 v204, 0, v190
	v_fmac_f32_e32 v201, v157, v208
	v_max_f32_e32 v208, 0, v191
	v_fmac_f32_e32 v201, v158, v204
	v_fmac_f32_e32 v201, v159, v208
	v_cndmask_b32_e32 v201, v61, v201, vcc
	v_ashrrev_i32_e32 v207, 31, v201
	v_or_b32_e32 v207, 0x80000000, v207
	v_xor_b32_e32 v85, v201, v207
	s_branch .Lidx_ce2
.Lidx_x23:
	s_nop 15
	v_cmp_le_i32_e32 vcc, 0x2c0, v59
	v_max_f32_e32 v204, 0, v160
	v_max_f32_e32 v208, 0, v161
	v_fma_f32 v201, v144, v204, 0
	v_max_f32_e32 v204, 0, v162
	v_fmac_f32_e32 v201, v145, v208
	v_max_f32_e32 v208, 0, v163
	v_fmac_f32_e32 v201, v146, v204
	v_max_f32_e32 v204, 0, v164
	v_fmac_f32_e32 v201, v147, v208
	v_max_f32_e32 v208, 0, v165
	v_fmac_f32_e32 v201, v148, v204
	v_max_f32_e32 v204, 0, v166
	v_fmac_f32_e32 v201, v149, v208
	v_max_f32_e32 v208, 0, v167
	v_fmac_f32_e32 v201, v150, v204
	v_max_f32_e32 v204, 0, v168
	v_fmac_f32_e32 v201, v151, v208
	v_max_f32_e32 v208, 0, v169
	v_fmac_f32_e32 v201, v152, v204
	v_max_f32_e32 v204, 0, v170
	v_fmac_f32_e32 v201, v153, v208
	v_max_f32_e32 v208, 0, v171
	v_fmac_f32_e32 v201, v154, v204
	v_max_f32_e32 v204, 0, v172
	v_fmac_f32_e32 v201, v155, v208
	v_max_f32_e32 v208, 0, v173
	v_fmac_f32_e32 v201, v156, v204
	v_max_f32_e32 v204, 0, v174
	v_fmac_f32_e32 v201, v157, v208
	v_max_f32_e32 v208, 0, v175
	v_fmac_f32_e32 v201, v158, v204
	v_fmac_f32_e32 v201, v159, v208
	v_cndmask_b32_e32 v201, v61, v201, vcc
	v_ashrrev_i32_e32 v207, 31, v201
	v_or_b32_e32 v207, 0x80000000, v207
	v_xor_b32_e32 v86, v201, v207
	s_branch .Lidx_ce2
.Lidx_x24:
	s_nop 15
	v_cmp_le_i32_e32 vcc, 0x2e0, v59
	v_max_f32_e32 v204, 0, v176
	v_max_f32_e32 v208, 0, v177
	v_fma_f32 v201, v144, v204, 0
	v_max_f32_e32 v204, 0, v178
	v_fmac_f32_e32 v201, v145, v208
	v_max_f32_e32 v208, 0, v179
	v_fmac_f32_e32 v201, v146, v204
	v_max_f32_e32 v204, 0, v180
	v_fmac_f32_e32 v201, v147, v208
	v_max_f32_e32 v208, 0, v181
	v_fmac_f32_e32 v201, v148, v204
	v_max_f32_e32 v204, 0, v182
	v_fmac_f32_e32 v201, v149, v208
	v_max_f32_e32 v208, 0, v183
	v_fmac_f32_e32 v201, v150, v204
	v_max_f32_e32 v204, 0, v184
	v_fmac_f32_e32 v201, v151, v208
	v_max_f32_e32 v208, 0, v185
	v_fmac_f32_e32 v201, v152, v204
	v_max_f32_e32 v204, 0, v186
	v_fmac_f32_e32 v201, v153, v208
	v_max_f32_e32 v208, 0, v187
	v_fmac_f32_e32 v201, v154, v204
	v_max_f32_e32 v204, 0, v188
	v_fmac_f32_e32 v201, v155, v208
	v_max_f32_e32 v208, 0, v189
	v_fmac_f32_e32 v201, v156, v204
	v_max_f32_e32 v204, 0, v190
	v_fmac_f32_e32 v201, v157, v208
	v_max_f32_e32 v208, 0, v191
	v_fmac_f32_e32 v201, v158, v204
	v_fmac_f32_e32 v201, v159, v208
	v_cndmask_b32_e32 v201, v61, v201, vcc
	v_ashrrev_i32_e32 v207, 31, v201
	v_or_b32_e32 v207, 0x80000000, v207
	v_xor_b32_e32 v87, v201, v207
	s_branch .Lidx_ce3
.Lidx_x25:
	s_nop 15
	v_cmp_le_i32_e32 vcc, 0x300, v59
	v_max_f32_e32 v204, 0, v160
	v_max_f32_e32 v208, 0, v161
	v_fma_f32 v201, v144, v204, 0
	v_max_f32_e32 v204, 0, v162
	v_fmac_f32_e32 v201, v145, v208
	v_max_f32_e32 v208, 0, v163
	v_fmac_f32_e32 v201, v146, v204
	v_max_f32_e32 v204, 0, v164
	v_fmac_f32_e32 v201, v147, v208
	v_max_f32_e32 v208, 0, v165
	v_fmac_f32_e32 v201, v148, v204
	v_max_f32_e32 v204, 0, v166
	v_fmac_f32_e32 v201, v149, v208
	v_max_f32_e32 v208, 0, v167
	v_fmac_f32_e32 v201, v150, v204
	v_max_f32_e32 v204, 0, v168
	v_fmac_f32_e32 v201, v151, v208
	v_max_f32_e32 v208, 0, v169
	v_fmac_f32_e32 v201, v152, v204
	v_max_f32_e32 v204, 0, v170
	v_fmac_f32_e32 v201, v153, v208
	v_max_f32_e32 v208, 0, v171
	v_fmac_f32_e32 v201, v154, v204
	v_max_f32_e32 v204, 0, v172
	v_fmac_f32_e32 v201, v155, v208
	v_max_f32_e32 v208, 0, v173
	v_fmac_f32_e32 v201, v156, v204
	v_max_f32_e32 v204, 0, v174
	v_fmac_f32_e32 v201, v157, v208
	v_max_f32_e32 v208, 0, v175
	v_fmac_f32_e32 v201, v158, v204
	v_fmac_f32_e32 v201, v159, v208
	v_cndmask_b32_e32 v201, v61, v201, vcc
	v_ashrrev_i32_e32 v207, 31, v201
	v_or_b32_e32 v207, 0x80000000, v207
	v_xor_b32_e32 v88, v201, v207
	s_branch .Lidx_ce3
.Lidx_x26:
	s_nop 15
	v_cmp_le_i32_e32 vcc, 0x320, v59
	v_max_f32_e32 v204, 0, v176
	v_max_f32_e32 v208, 0, v177
	v_fma_f32 v201, v144, v204, 0
	v_max_f32_e32 v204, 0, v178
	v_fmac_f32_e32 v201, v145, v208
	v_max_f32_e32 v208, 0, v179
	v_fmac_f32_e32 v201, v146, v204
	v_max_f32_e32 v204, 0, v180
	v_fmac_f32_e32 v201, v147, v208
	v_max_f32_e32 v208, 0, v181
	v_fmac_f32_e32 v201, v148, v204
	v_max_f32_e32 v204, 0, v182
	v_fmac_f32_e32 v201, v149, v208
	v_max_f32_e32 v208, 0, v183
	v_fmac_f32_e32 v201, v150, v204
	v_max_f32_e32 v204, 0, v184
	v_fmac_f32_e32 v201, v151, v208
	v_max_f32_e32 v208, 0, v185
	v_fmac_f32_e32 v201, v152, v204
	v_max_f32_e32 v204, 0, v186
	v_fmac_f32_e32 v201, v153, v208
	v_max_f32_e32 v208, 0, v187
	v_fmac_f32_e32 v201, v154, v204
	v_max_f32_e32 v204, 0, v188
	v_fmac_f32_e32 v201, v155, v208
	v_max_f32_e32 v208, 0, v189
	v_fmac_f32_e32 v201, v156, v204
	v_max_f32_e32 v204, 0, v190
	v_fmac_f32_e32 v201, v157, v208
	v_max_f32_e32 v208, 0, v191
	v_fmac_f32_e32 v201, v158, v204
	v_fmac_f32_e32 v201, v159, v208
	v_cndmask_b32_e32 v201, v61, v201, vcc
	v_ashrrev_i32_e32 v207, 31, v201
	v_or_b32_e32 v207, 0x80000000, v207
	v_xor_b32_e32 v89, v201, v207
	s_branch .Lidx_ce3
.Lidx_x27:
	s_nop 15
	v_cmp_le_i32_e32 vcc, 0x340, v59
	v_max_f32_e32 v204, 0, v160
	v_max_f32_e32 v208, 0, v161
	v_fma_f32 v201, v144, v204, 0
	v_max_f32_e32 v204, 0, v162
	v_fmac_f32_e32 v201, v145, v208
	v_max_f32_e32 v208, 0, v163
	v_fmac_f32_e32 v201, v146, v204
	v_max_f32_e32 v204, 0, v164
	v_fmac_f32_e32 v201, v147, v208
	v_max_f32_e32 v208, 0, v165
	v_fmac_f32_e32 v201, v148, v204
	v_max_f32_e32 v204, 0, v166
	v_fmac_f32_e32 v201, v149, v208
	v_max_f32_e32 v208, 0, v167
	v_fmac_f32_e32 v201, v150, v204
	v_max_f32_e32 v204, 0, v168
	v_fmac_f32_e32 v201, v151, v208
	v_max_f32_e32 v208, 0, v169
	v_fmac_f32_e32 v201, v152, v204
	v_max_f32_e32 v204, 0, v170
	v_fmac_f32_e32 v201, v153, v208
	v_max_f32_e32 v208, 0, v171
	v_fmac_f32_e32 v201, v154, v204
	v_max_f32_e32 v204, 0, v172
	v_fmac_f32_e32 v201, v155, v208
	v_max_f32_e32 v208, 0, v173
	v_fmac_f32_e32 v201, v156, v204
	v_max_f32_e32 v204, 0, v174
	v_fmac_f32_e32 v201, v157, v208
	v_max_f32_e32 v208, 0, v175
	v_fmac_f32_e32 v201, v158, v204
	v_fmac_f32_e32 v201, v159, v208
	v_cndmask_b32_e32 v201, v61, v201, vcc
	v_ashrrev_i32_e32 v207, 31, v201
	v_or_b32_e32 v207, 0x80000000, v207
	v_xor_b32_e32 v90, v201, v207
	s_branch .Lidx_ce3
.Lidx_x28:
	s_nop 15
	v_cmp_le_i32_e32 vcc, 0x360, v59
	v_max_f32_e32 v204, 0, v176
	v_max_f32_e32 v208, 0, v177
	v_fma_f32 v201, v144, v204, 0
	v_max_f32_e32 v204, 0, v178
	v_fmac_f32_e32 v201, v145, v208
	v_max_f32_e32 v208, 0, v179
	v_fmac_f32_e32 v201, v146, v204
	v_max_f32_e32 v204, 0, v180
	v_fmac_f32_e32 v201, v147, v208
	v_max_f32_e32 v208, 0, v181
	v_fmac_f32_e32 v201, v148, v204
	v_max_f32_e32 v204, 0, v182
	v_fmac_f32_e32 v201, v149, v208
	v_max_f32_e32 v208, 0, v183
	v_fmac_f32_e32 v201, v150, v204
	v_max_f32_e32 v204, 0, v184
	v_fmac_f32_e32 v201, v151, v208
	v_max_f32_e32 v208, 0, v185
	v_fmac_f32_e32 v201, v152, v204
	v_max_f32_e32 v204, 0, v186
	v_fmac_f32_e32 v201, v153, v208
	v_max_f32_e32 v208, 0, v187
	v_fmac_f32_e32 v201, v154, v204
	v_max_f32_e32 v204, 0, v188
	v_fmac_f32_e32 v201, v155, v208
	v_max_f32_e32 v208, 0, v189
	v_fmac_f32_e32 v201, v156, v204
	v_max_f32_e32 v204, 0, v190
	v_fmac_f32_e32 v201, v157, v208
	v_max_f32_e32 v208, 0, v191
	v_fmac_f32_e32 v201, v158, v204
	v_fmac_f32_e32 v201, v159, v208
	v_cndmask_b32_e32 v201, v61, v201, vcc
	v_ashrrev_i32_e32 v207, 31, v201
	v_or_b32_e32 v207, 0x80000000, v207
	v_xor_b32_e32 v91, v201, v207
	s_branch .Lidx_ce3
.Lidx_x29:
	s_nop 15
	v_cmp_le_i32_e32 vcc, 0x380, v59
	v_max_f32_e32 v204, 0, v160
	v_max_f32_e32 v208, 0, v161
	v_fma_f32 v201, v144, v204, 0
	v_max_f32_e32 v204, 0, v162
	v_fmac_f32_e32 v201, v145, v208
	v_max_f32_e32 v208, 0, v163
	v_fmac_f32_e32 v201, v146, v204
	v_max_f32_e32 v204, 0, v164
	v_fmac_f32_e32 v201, v147, v208
	v_max_f32_e32 v208, 0, v165
	v_fmac_f32_e32 v201, v148, v204
	v_max_f32_e32 v204, 0, v166
	v_fmac_f32_e32 v201, v149, v208
	v_max_f32_e32 v208, 0, v167
	v_fmac_f32_e32 v201, v150, v204
	v_max_f32_e32 v204, 0, v168
	v_fmac_f32_e32 v201, v151, v208
	v_max_f32_e32 v208, 0, v169
	v_fmac_f32_e32 v201, v152, v204
	v_max_f32_e32 v204, 0, v170
	v_fmac_f32_e32 v201, v153, v208
	v_max_f32_e32 v208, 0, v171
	v_fmac_f32_e32 v201, v154, v204
	v_max_f32_e32 v204, 0, v172
	v_fmac_f32_e32 v201, v155, v208
	v_max_f32_e32 v208, 0, v173
	v_fmac_f32_e32 v201, v156, v204
	v_max_f32_e32 v204, 0, v174
	v_fmac_f32_e32 v201, v157, v208
	v_max_f32_e32 v208, 0, v175
	v_fmac_f32_e32 v201, v158, v204
	v_fmac_f32_e32 v201, v159, v208
	v_cndmask_b32_e32 v201, v61, v201, vcc
	v_ashrrev_i32_e32 v207, 31, v201
	v_or_b32_e32 v207, 0x80000000, v207
	v_xor_b32_e32 v92, v201, v207
	s_branch .Lidx_ce3
.Lidx_x30:
	s_nop 15
	v_cmp_le_i32_e32 vcc, 0x3a0, v59
	v_max_f32_e32 v204, 0, v176
	v_max_f32_e32 v208, 0, v177
	v_fma_f32 v201, v144, v204, 0
	v_max_f32_e32 v204, 0, v178
	v_fmac_f32_e32 v201, v145, v208
	v_max_f32_e32 v208, 0, v179
	v_fmac_f32_e32 v201, v146, v204
	v_max_f32_e32 v204, 0, v180
	v_fmac_f32_e32 v201, v147, v208
	v_max_f32_e32 v208, 0, v181
	v_fmac_f32_e32 v201, v148, v204
	v_max_f32_e32 v204, 0, v182
	v_fmac_f32_e32 v201, v149, v208
	v_max_f32_e32 v208, 0, v183
	v_fmac_f32_e32 v201, v150, v204
	v_max_f32_e32 v204, 0, v184
	v_fmac_f32_e32 v201, v151, v208
	v_max_f32_e32 v208, 0, v185
	v_fmac_f32_e32 v201, v152, v204
	v_max_f32_e32 v204, 0, v186
	v_fmac_f32_e32 v201, v153, v208
	v_max_f32_e32 v208, 0, v187
	v_fmac_f32_e32 v201, v154, v204
	v_max_f32_e32 v204, 0, v188
	v_fmac_f32_e32 v201, v155, v208
	v_max_f32_e32 v208, 0, v189
	v_fmac_f32_e32 v201, v156, v204
	v_max_f32_e32 v204, 0, v190
	v_fmac_f32_e32 v201, v157, v208
	v_max_f32_e32 v208, 0, v191
	v_fmac_f32_e32 v201, v158, v204
	v_fmac_f32_e32 v201, v159, v208
	v_cndmask_b32_e32 v201, v61, v201, vcc
	v_ashrrev_i32_e32 v207, 31, v201
	v_or_b32_e32 v207, 0x80000000, v207
	v_xor_b32_e32 v93, v201, v207
	s_branch .Lidx_ce3
.Lidx_x31:
	s_nop 15
	v_cmp_le_i32_e32 vcc, 0x3c0, v59
	v_max_f32_e32 v204, 0, v160
	v_max_f32_e32 v208, 0, v161
	v_fma_f32 v201, v144, v204, 0
	v_max_f32_e32 v204, 0, v162
	v_fmac_f32_e32 v201, v145, v208
	v_max_f32_e32 v208, 0, v163
	v_fmac_f32_e32 v201, v146, v204
	v_max_f32_e32 v204, 0, v164
	v_fmac_f32_e32 v201, v147, v208
	v_max_f32_e32 v208, 0, v165
	v_fmac_f32_e32 v201, v148, v204
	v_max_f32_e32 v204, 0, v166
	v_fmac_f32_e32 v201, v149, v208
	v_max_f32_e32 v208, 0, v167
	v_fmac_f32_e32 v201, v150, v204
	v_max_f32_e32 v204, 0, v168
	v_fmac_f32_e32 v201, v151, v208
	v_max_f32_e32 v208, 0, v169
	v_fmac_f32_e32 v201, v152, v204
	v_max_f32_e32 v204, 0, v170
	v_fmac_f32_e32 v201, v153, v208
	v_max_f32_e32 v208, 0, v171
	v_fmac_f32_e32 v201, v154, v204
	v_max_f32_e32 v204, 0, v172
	v_fmac_f32_e32 v201, v155, v208
	v_max_f32_e32 v208, 0, v173
	v_fmac_f32_e32 v201, v156, v204
	v_max_f32_e32 v204, 0, v174
	v_fmac_f32_e32 v201, v157, v208
	v_max_f32_e32 v208, 0, v175
	v_fmac_f32_e32 v201, v158, v204
	v_fmac_f32_e32 v201, v159, v208
	v_cndmask_b32_e32 v201, v61, v201, vcc
	v_ashrrev_i32_e32 v207, 31, v201
	v_or_b32_e32 v207, 0x80000000, v207
	v_xor_b32_e32 v94, v201, v207
	s_branch .Lidx_ce3
.Lidx_x32:
	s_nop 15
	v_cmp_le_i32_e32 vcc, 0x3e0, v59
	v_max_f32_e32 v204, 0, v176
	v_max_f32_e32 v208, 0, v177
	v_fma_f32 v201, v144, v204, 0
	v_max_f32_e32 v204, 0, v178
	v_fmac_f32_e32 v201, v145, v208
	v_max_f32_e32 v208, 0, v179
	v_fmac_f32_e32 v201, v146, v204
	v_max_f32_e32 v204, 0, v180
	v_fmac_f32_e32 v201, v147, v208
	v_max_f32_e32 v208, 0, v181
	v_fmac_f32_e32 v201, v148, v204
	v_max_f32_e32 v204, 0, v182
	v_fmac_f32_e32 v201, v149, v208
	v_max_f32_e32 v208, 0, v183
	v_fmac_f32_e32 v201, v150, v204
	v_max_f32_e32 v204, 0, v184
	v_fmac_f32_e32 v201, v151, v208
	v_max_f32_e32 v208, 0, v185
	v_fmac_f32_e32 v201, v152, v204
	v_max_f32_e32 v204, 0, v186
	v_fmac_f32_e32 v201, v153, v208
	v_max_f32_e32 v208, 0, v187
	v_fmac_f32_e32 v201, v154, v204
	v_max_f32_e32 v204, 0, v188
	v_fmac_f32_e32 v201, v155, v208
	v_max_f32_e32 v208, 0, v189
	v_fmac_f32_e32 v201, v156, v204
	v_max_f32_e32 v204, 0, v190
	v_fmac_f32_e32 v201, v157, v208
	v_max_f32_e32 v208, 0, v191
	v_fmac_f32_e32 v201, v158, v204
	v_fmac_f32_e32 v201, v159, v208
	v_cndmask_b32_e32 v201, v61, v201, vcc
	v_ashrrev_i32_e32 v207, 31, v201
	v_or_b32_e32 v207, 0x80000000, v207
	v_xor_b32_e32 v95, v201, v207
	s_branch .Lidx_ce4
.Lidx_x33:
	s_nop 15
	v_cmp_le_i32_e32 vcc, 0x400, v59
	v_max_f32_e32 v204, 0, v160
	v_max_f32_e32 v208, 0, v161
	v_fma_f32 v201, v144, v204, 0
	v_max_f32_e32 v204, 0, v162
	v_fmac_f32_e32 v201, v145, v208
	v_max_f32_e32 v208, 0, v163
	v_fmac_f32_e32 v201, v146, v204
	v_max_f32_e32 v204, 0, v164
	v_fmac_f32_e32 v201, v147, v208
	v_max_f32_e32 v208, 0, v165
	v_fmac_f32_e32 v201, v148, v204
	v_max_f32_e32 v204, 0, v166
	v_fmac_f32_e32 v201, v149, v208
	v_max_f32_e32 v208, 0, v167
	v_fmac_f32_e32 v201, v150, v204
	v_max_f32_e32 v204, 0, v168
	v_fmac_f32_e32 v201, v151, v208
	v_max_f32_e32 v208, 0, v169
	v_fmac_f32_e32 v201, v152, v204
	v_max_f32_e32 v204, 0, v170
	v_fmac_f32_e32 v201, v153, v208
	v_max_f32_e32 v208, 0, v171
	v_fmac_f32_e32 v201, v154, v204
	v_max_f32_e32 v204, 0, v172
	v_fmac_f32_e32 v201, v155, v208
	v_max_f32_e32 v208, 0, v173
	v_fmac_f32_e32 v201, v156, v204
	v_max_f32_e32 v204, 0, v174
	v_fmac_f32_e32 v201, v157, v208
	v_max_f32_e32 v208, 0, v175
	v_fmac_f32_e32 v201, v158, v204
	v_fmac_f32_e32 v201, v159, v208
	v_cndmask_b32_e32 v201, v61, v201, vcc
	v_ashrrev_i32_e32 v207, 31, v201
	v_or_b32_e32 v207, 0x80000000, v207
	v_xor_b32_e32 v96, v201, v207
	s_branch .Lidx_ce4
.Lidx_x34:
	s_nop 15
	v_cmp_le_i32_e32 vcc, 0x420, v59
	v_max_f32_e32 v204, 0, v176
	v_max_f32_e32 v208, 0, v177
	v_fma_f32 v201, v144, v204, 0
	v_max_f32_e32 v204, 0, v178
	v_fmac_f32_e32 v201, v145, v208
	v_max_f32_e32 v208, 0, v179
	v_fmac_f32_e32 v201, v146, v204
	v_max_f32_e32 v204, 0, v180
	v_fmac_f32_e32 v201, v147, v208
	v_max_f32_e32 v208, 0, v181
	v_fmac_f32_e32 v201, v148, v204
	v_max_f32_e32 v204, 0, v182
	v_fmac_f32_e32 v201, v149, v208
	v_max_f32_e32 v208, 0, v183
	v_fmac_f32_e32 v201, v150, v204
	v_max_f32_e32 v204, 0, v184
	v_fmac_f32_e32 v201, v151, v208
	v_max_f32_e32 v208, 0, v185
	v_fmac_f32_e32 v201, v152, v204
	v_max_f32_e32 v204, 0, v186
	v_fmac_f32_e32 v201, v153, v208
	v_max_f32_e32 v208, 0, v187
	v_fmac_f32_e32 v201, v154, v204
	v_max_f32_e32 v204, 0, v188
	v_fmac_f32_e32 v201, v155, v208
	v_max_f32_e32 v208, 0, v189
	v_fmac_f32_e32 v201, v156, v204
	v_max_f32_e32 v204, 0, v190
	v_fmac_f32_e32 v201, v157, v208
	v_max_f32_e32 v208, 0, v191
	v_fmac_f32_e32 v201, v158, v204
	v_fmac_f32_e32 v201, v159, v208
	v_cndmask_b32_e32 v201, v61, v201, vcc
	v_ashrrev_i32_e32 v207, 31, v201
	v_or_b32_e32 v207, 0x80000000, v207
	v_xor_b32_e32 v97, v201, v207
	s_branch .Lidx_ce4
.Lidx_x35:
	s_nop 15
	v_cmp_le_i32_e32 vcc, 0x440, v59
	v_max_f32_e32 v204, 0, v160
	v_max_f32_e32 v208, 0, v161
	v_fma_f32 v201, v144, v204, 0
	v_max_f32_e32 v204, 0, v162
	v_fmac_f32_e32 v201, v145, v208
	v_max_f32_e32 v208, 0, v163
	v_fmac_f32_e32 v201, v146, v204
	v_max_f32_e32 v204, 0, v164
	v_fmac_f32_e32 v201, v147, v208
	v_max_f32_e32 v208, 0, v165
	v_fmac_f32_e32 v201, v148, v204
	v_max_f32_e32 v204, 0, v166
	v_fmac_f32_e32 v201, v149, v208
	v_max_f32_e32 v208, 0, v167
	v_fmac_f32_e32 v201, v150, v204
	v_max_f32_e32 v204, 0, v168
	v_fmac_f32_e32 v201, v151, v208
	v_max_f32_e32 v208, 0, v169
	v_fmac_f32_e32 v201, v152, v204
	v_max_f32_e32 v204, 0, v170
	v_fmac_f32_e32 v201, v153, v208
	v_max_f32_e32 v208, 0, v171
	v_fmac_f32_e32 v201, v154, v204
	v_max_f32_e32 v204, 0, v172
	v_fmac_f32_e32 v201, v155, v208
	v_max_f32_e32 v208, 0, v173
	v_fmac_f32_e32 v201, v156, v204
	v_max_f32_e32 v204, 0, v174
	v_fmac_f32_e32 v201, v157, v208
	v_max_f32_e32 v208, 0, v175
	v_fmac_f32_e32 v201, v158, v204
	v_fmac_f32_e32 v201, v159, v208
	v_cndmask_b32_e32 v201, v61, v201, vcc
	v_ashrrev_i32_e32 v207, 31, v201
	v_or_b32_e32 v207, 0x80000000, v207
	v_xor_b32_e32 v98, v201, v207
	s_branch .Lidx_ce4
.Lidx_x36:
	s_nop 15
	v_cmp_le_i32_e32 vcc, 0x460, v59
	v_max_f32_e32 v204, 0, v176
	v_max_f32_e32 v208, 0, v177
	v_fma_f32 v201, v144, v204, 0
	v_max_f32_e32 v204, 0, v178
	v_fmac_f32_e32 v201, v145, v208
	v_max_f32_e32 v208, 0, v179
	v_fmac_f32_e32 v201, v146, v204
	v_max_f32_e32 v204, 0, v180
	v_fmac_f32_e32 v201, v147, v208
	v_max_f32_e32 v208, 0, v181
	v_fmac_f32_e32 v201, v148, v204
	v_max_f32_e32 v204, 0, v182
	v_fmac_f32_e32 v201, v149, v208
	v_max_f32_e32 v208, 0, v183
	v_fmac_f32_e32 v201, v150, v204
	v_max_f32_e32 v204, 0, v184
	v_fmac_f32_e32 v201, v151, v208
	v_max_f32_e32 v208, 0, v185
	v_fmac_f32_e32 v201, v152, v204
	v_max_f32_e32 v204, 0, v186
	v_fmac_f32_e32 v201, v153, v208
	v_max_f32_e32 v208, 0, v187
	v_fmac_f32_e32 v201, v154, v204
	v_max_f32_e32 v204, 0, v188
	v_fmac_f32_e32 v201, v155, v208
	v_max_f32_e32 v208, 0, v189
	v_fmac_f32_e32 v201, v156, v204
	v_max_f32_e32 v204, 0, v190
	v_fmac_f32_e32 v201, v157, v208
	v_max_f32_e32 v208, 0, v191
	v_fmac_f32_e32 v201, v158, v204
	v_fmac_f32_e32 v201, v159, v208
	v_cndmask_b32_e32 v201, v61, v201, vcc
	v_ashrrev_i32_e32 v207, 31, v201
	v_or_b32_e32 v207, 0x80000000, v207
	v_xor_b32_e32 v99, v201, v207
	s_branch .Lidx_ce4
.Lidx_x37:
	s_nop 15
	v_cmp_le_i32_e32 vcc, 0x480, v59
	v_max_f32_e32 v204, 0, v160
	v_max_f32_e32 v208, 0, v161
	v_fma_f32 v201, v144, v204, 0
	v_max_f32_e32 v204, 0, v162
	v_fmac_f32_e32 v201, v145, v208
	v_max_f32_e32 v208, 0, v163
	v_fmac_f32_e32 v201, v146, v204
	v_max_f32_e32 v204, 0, v164
	v_fmac_f32_e32 v201, v147, v208
	v_max_f32_e32 v208, 0, v165
	v_fmac_f32_e32 v201, v148, v204
	v_max_f32_e32 v204, 0, v166
	v_fmac_f32_e32 v201, v149, v208
	v_max_f32_e32 v208, 0, v167
	v_fmac_f32_e32 v201, v150, v204
	v_max_f32_e32 v204, 0, v168
	v_fmac_f32_e32 v201, v151, v208
	v_max_f32_e32 v208, 0, v169
	v_fmac_f32_e32 v201, v152, v204
	v_max_f32_e32 v204, 0, v170
	v_fmac_f32_e32 v201, v153, v208
	v_max_f32_e32 v208, 0, v171
	v_fmac_f32_e32 v201, v154, v204
	v_max_f32_e32 v204, 0, v172
	v_fmac_f32_e32 v201, v155, v208
	v_max_f32_e32 v208, 0, v173
	v_fmac_f32_e32 v201, v156, v204
	v_max_f32_e32 v204, 0, v174
	v_fmac_f32_e32 v201, v157, v208
	v_max_f32_e32 v208, 0, v175
	v_fmac_f32_e32 v201, v158, v204
	v_fmac_f32_e32 v201, v159, v208
	v_cndmask_b32_e32 v201, v61, v201, vcc
	v_ashrrev_i32_e32 v207, 31, v201
	v_or_b32_e32 v207, 0x80000000, v207
	v_xor_b32_e32 v100, v201, v207
	s_branch .Lidx_ce4
.Lidx_x38:
	s_nop 15
	v_cmp_le_i32_e32 vcc, 0x4a0, v59
	v_max_f32_e32 v204, 0, v176
	v_max_f32_e32 v208, 0, v177
	v_fma_f32 v201, v144, v204, 0
	v_max_f32_e32 v204, 0, v178
	v_fmac_f32_e32 v201, v145, v208
	v_max_f32_e32 v208, 0, v179
	v_fmac_f32_e32 v201, v146, v204
	v_max_f32_e32 v204, 0, v180
	v_fmac_f32_e32 v201, v147, v208
	v_max_f32_e32 v208, 0, v181
	v_fmac_f32_e32 v201, v148, v204
	v_max_f32_e32 v204, 0, v182
	v_fmac_f32_e32 v201, v149, v208
	v_max_f32_e32 v208, 0, v183
	v_fmac_f32_e32 v201, v150, v204
	v_max_f32_e32 v204, 0, v184
	v_fmac_f32_e32 v201, v151, v208
	v_max_f32_e32 v208, 0, v185
	v_fmac_f32_e32 v201, v152, v204
	v_max_f32_e32 v204, 0, v186
	v_fmac_f32_e32 v201, v153, v208
	v_max_f32_e32 v208, 0, v187
	v_fmac_f32_e32 v201, v154, v204
	v_max_f32_e32 v204, 0, v188
	v_fmac_f32_e32 v201, v155, v208
	v_max_f32_e32 v208, 0, v189
	v_fmac_f32_e32 v201, v156, v204
	v_max_f32_e32 v204, 0, v190
	v_fmac_f32_e32 v201, v157, v208
	v_max_f32_e32 v208, 0, v191
	v_fmac_f32_e32 v201, v158, v204
	v_fmac_f32_e32 v201, v159, v208
	v_cndmask_b32_e32 v201, v61, v201, vcc
	v_ashrrev_i32_e32 v207, 31, v201
	v_or_b32_e32 v207, 0x80000000, v207
	v_xor_b32_e32 v101, v201, v207
	s_branch .Lidx_ce4
.Lidx_x39:
	s_nop 15
	v_cmp_le_i32_e32 vcc, 0x4c0, v59
	v_max_f32_e32 v204, 0, v160
	v_max_f32_e32 v208, 0, v161
	v_fma_f32 v201, v144, v204, 0
	v_max_f32_e32 v204, 0, v162
	v_fmac_f32_e32 v201, v145, v208
	v_max_f32_e32 v208, 0, v163
	v_fmac_f32_e32 v201, v146, v204
	v_max_f32_e32 v204, 0, v164
	v_fmac_f32_e32 v201, v147, v208
	v_max_f32_e32 v208, 0, v165
	v_fmac_f32_e32 v201, v148, v204
	v_max_f32_e32 v204, 0, v166
	v_fmac_f32_e32 v201, v149, v208
	v_max_f32_e32 v208, 0, v167
	v_fmac_f32_e32 v201, v150, v204
	v_max_f32_e32 v204, 0, v168
	v_fmac_f32_e32 v201, v151, v208
	v_max_f32_e32 v208, 0, v169
	v_fmac_f32_e32 v201, v152, v204
	v_max_f32_e32 v204, 0, v170
	v_fmac_f32_e32 v201, v153, v208
	v_max_f32_e32 v208, 0, v171
	v_fmac_f32_e32 v201, v154, v204
	v_max_f32_e32 v204, 0, v172
	v_fmac_f32_e32 v201, v155, v208
	v_max_f32_e32 v208, 0, v173
	v_fmac_f32_e32 v201, v156, v204
	v_max_f32_e32 v204, 0, v174
	v_fmac_f32_e32 v201, v157, v208
	v_max_f32_e32 v208, 0, v175
	v_fmac_f32_e32 v201, v158, v204
	v_fmac_f32_e32 v201, v159, v208
	v_cndmask_b32_e32 v201, v61, v201, vcc
	v_ashrrev_i32_e32 v207, 31, v201
	v_or_b32_e32 v207, 0x80000000, v207
	v_xor_b32_e32 v102, v201, v207
	s_branch .Lidx_ce4
.Lidx_x40:
	s_nop 15
	v_cmp_le_i32_e32 vcc, 0x4e0, v59
	v_max_f32_e32 v204, 0, v176
	v_max_f32_e32 v208, 0, v177
	v_fma_f32 v201, v144, v204, 0
	v_max_f32_e32 v204, 0, v178
	v_fmac_f32_e32 v201, v145, v208
	v_max_f32_e32 v208, 0, v179
	v_fmac_f32_e32 v201, v146, v204
	v_max_f32_e32 v204, 0, v180
	v_fmac_f32_e32 v201, v147, v208
	v_max_f32_e32 v208, 0, v181
	v_fmac_f32_e32 v201, v148, v204
	v_max_f32_e32 v204, 0, v182
	v_fmac_f32_e32 v201, v149, v208
	v_max_f32_e32 v208, 0, v183
	v_fmac_f32_e32 v201, v150, v204
	v_max_f32_e32 v204, 0, v184
	v_fmac_f32_e32 v201, v151, v208
	v_max_f32_e32 v208, 0, v185
	v_fmac_f32_e32 v201, v152, v204
	v_max_f32_e32 v204, 0, v186
	v_fmac_f32_e32 v201, v153, v208
	v_max_f32_e32 v208, 0, v187
	v_fmac_f32_e32 v201, v154, v204
	v_max_f32_e32 v204, 0, v188
	v_fmac_f32_e32 v201, v155, v208
	v_max_f32_e32 v208, 0, v189
	v_fmac_f32_e32 v201, v156, v204
	v_max_f32_e32 v204, 0, v190
	v_fmac_f32_e32 v201, v157, v208
	v_max_f32_e32 v208, 0, v191
	v_fmac_f32_e32 v201, v158, v204
	v_fmac_f32_e32 v201, v159, v208
	v_cndmask_b32_e32 v201, v61, v201, vcc
	v_ashrrev_i32_e32 v207, 31, v201
	v_or_b32_e32 v207, 0x80000000, v207
	v_xor_b32_e32 v103, v201, v207
	s_branch .Lidx_ce5
.Lidx_x41:
	s_nop 15
	v_cmp_le_i32_e32 vcc, 0x500, v59
	v_max_f32_e32 v204, 0, v160
	v_max_f32_e32 v208, 0, v161
	v_fma_f32 v201, v144, v204, 0
	v_max_f32_e32 v204, 0, v162
	v_fmac_f32_e32 v201, v145, v208
	v_max_f32_e32 v208, 0, v163
	v_fmac_f32_e32 v201, v146, v204
	v_max_f32_e32 v204, 0, v164
	v_fmac_f32_e32 v201, v147, v208
	v_max_f32_e32 v208, 0, v165
	v_fmac_f32_e32 v201, v148, v204
	v_max_f32_e32 v204, 0, v166
	v_fmac_f32_e32 v201, v149, v208
	v_max_f32_e32 v208, 0, v167
	v_fmac_f32_e32 v201, v150, v204
	v_max_f32_e32 v204, 0, v168
	v_fmac_f32_e32 v201, v151, v208
	v_max_f32_e32 v208, 0, v169
	v_fmac_f32_e32 v201, v152, v204
	v_max_f32_e32 v204, 0, v170
	v_fmac_f32_e32 v201, v153, v208
	v_max_f32_e32 v208, 0, v171
	v_fmac_f32_e32 v201, v154, v204
	v_max_f32_e32 v204, 0, v172
	v_fmac_f32_e32 v201, v155, v208
	v_max_f32_e32 v208, 0, v173
	v_fmac_f32_e32 v201, v156, v204
	v_max_f32_e32 v204, 0, v174
	v_fmac_f32_e32 v201, v157, v208
	v_max_f32_e32 v208, 0, v175
	v_fmac_f32_e32 v201, v158, v204
	v_fmac_f32_e32 v201, v159, v208
	v_cndmask_b32_e32 v201, v61, v201, vcc
	v_ashrrev_i32_e32 v207, 31, v201
	v_or_b32_e32 v207, 0x80000000, v207
	v_xor_b32_e32 v104, v201, v207
	s_branch .Lidx_ce5
.Lidx_x42:
	s_nop 15
	v_cmp_le_i32_e32 vcc, 0x520, v59
	v_max_f32_e32 v204, 0, v176
	v_max_f32_e32 v208, 0, v177
	v_fma_f32 v201, v144, v204, 0
	v_max_f32_e32 v204, 0, v178
	v_fmac_f32_e32 v201, v145, v208
	v_max_f32_e32 v208, 0, v179
	v_fmac_f32_e32 v201, v146, v204
	v_max_f32_e32 v204, 0, v180
	v_fmac_f32_e32 v201, v147, v208
	v_max_f32_e32 v208, 0, v181
	v_fmac_f32_e32 v201, v148, v204
	v_max_f32_e32 v204, 0, v182
	v_fmac_f32_e32 v201, v149, v208
	v_max_f32_e32 v208, 0, v183
	v_fmac_f32_e32 v201, v150, v204
	v_max_f32_e32 v204, 0, v184
	v_fmac_f32_e32 v201, v151, v208
	v_max_f32_e32 v208, 0, v185
	v_fmac_f32_e32 v201, v152, v204
	v_max_f32_e32 v204, 0, v186
	v_fmac_f32_e32 v201, v153, v208
	v_max_f32_e32 v208, 0, v187
	v_fmac_f32_e32 v201, v154, v204
	v_max_f32_e32 v204, 0, v188
	v_fmac_f32_e32 v201, v155, v208
	v_max_f32_e32 v208, 0, v189
	v_fmac_f32_e32 v201, v156, v204
	v_max_f32_e32 v204, 0, v190
	v_fmac_f32_e32 v201, v157, v208
	v_max_f32_e32 v208, 0, v191
	v_fmac_f32_e32 v201, v158, v204
	v_fmac_f32_e32 v201, v159, v208
	v_cndmask_b32_e32 v201, v61, v201, vcc
	v_ashrrev_i32_e32 v207, 31, v201
	v_or_b32_e32 v207, 0x80000000, v207
	v_xor_b32_e32 v105, v201, v207
	s_branch .Lidx_ce5
.Lidx_x43:
	s_nop 15
	v_cmp_le_i32_e32 vcc, 0x540, v59
	v_max_f32_e32 v204, 0, v160
	v_max_f32_e32 v208, 0, v161
	v_fma_f32 v201, v144, v204, 0
	v_max_f32_e32 v204, 0, v162
	v_fmac_f32_e32 v201, v145, v208
	v_max_f32_e32 v208, 0, v163
	v_fmac_f32_e32 v201, v146, v204
	v_max_f32_e32 v204, 0, v164
	v_fmac_f32_e32 v201, v147, v208
	v_max_f32_e32 v208, 0, v165
	v_fmac_f32_e32 v201, v148, v204
	v_max_f32_e32 v204, 0, v166
	v_fmac_f32_e32 v201, v149, v208
	v_max_f32_e32 v208, 0, v167
	v_fmac_f32_e32 v201, v150, v204
	v_max_f32_e32 v204, 0, v168
	v_fmac_f32_e32 v201, v151, v208
	v_max_f32_e32 v208, 0, v169
	v_fmac_f32_e32 v201, v152, v204
	v_max_f32_e32 v204, 0, v170
	v_fmac_f32_e32 v201, v153, v208
	v_max_f32_e32 v208, 0, v171
	v_fmac_f32_e32 v201, v154, v204
	v_max_f32_e32 v204, 0, v172
	v_fmac_f32_e32 v201, v155, v208
	v_max_f32_e32 v208, 0, v173
	v_fmac_f32_e32 v201, v156, v204
	v_max_f32_e32 v204, 0, v174
	v_fmac_f32_e32 v201, v157, v208
	v_max_f32_e32 v208, 0, v175
	v_fmac_f32_e32 v201, v158, v204
	v_fmac_f32_e32 v201, v159, v208
	v_cndmask_b32_e32 v201, v61, v201, vcc
	v_ashrrev_i32_e32 v207, 31, v201
	v_or_b32_e32 v207, 0x80000000, v207
	v_xor_b32_e32 v106, v201, v207
	s_branch .Lidx_ce5
.Lidx_x44:
	s_nop 15
	v_cmp_le_i32_e32 vcc, 0x560, v59
	v_max_f32_e32 v204, 0, v176
	v_max_f32_e32 v208, 0, v177
	v_fma_f32 v201, v144, v204, 0
	v_max_f32_e32 v204, 0, v178
	v_fmac_f32_e32 v201, v145, v208
	v_max_f32_e32 v208, 0, v179
	v_fmac_f32_e32 v201, v146, v204
	v_max_f32_e32 v204, 0, v180
	v_fmac_f32_e32 v201, v147, v208
	v_max_f32_e32 v208, 0, v181
	v_fmac_f32_e32 v201, v148, v204
	v_max_f32_e32 v204, 0, v182
	v_fmac_f32_e32 v201, v149, v208
	v_max_f32_e32 v208, 0, v183
	v_fmac_f32_e32 v201, v150, v204
	v_max_f32_e32 v204, 0, v184
	v_fmac_f32_e32 v201, v151, v208
	v_max_f32_e32 v208, 0, v185
	v_fmac_f32_e32 v201, v152, v204
	v_max_f32_e32 v204, 0, v186
	v_fmac_f32_e32 v201, v153, v208
	v_max_f32_e32 v208, 0, v187
	v_fmac_f32_e32 v201, v154, v204
	v_max_f32_e32 v204, 0, v188
	v_fmac_f32_e32 v201, v155, v208
	v_max_f32_e32 v208, 0, v189
	v_fmac_f32_e32 v201, v156, v204
	v_max_f32_e32 v204, 0, v190
	v_fmac_f32_e32 v201, v157, v208
	v_max_f32_e32 v208, 0, v191
	v_fmac_f32_e32 v201, v158, v204
	v_fmac_f32_e32 v201, v159, v208
	v_cndmask_b32_e32 v201, v61, v201, vcc
	v_ashrrev_i32_e32 v207, 31, v201
	v_or_b32_e32 v207, 0x80000000, v207
	v_xor_b32_e32 v107, v201, v207
	s_branch .Lidx_ce5
.Lidx_x45:
	s_nop 15
	v_cmp_le_i32_e32 vcc, 0x580, v59
	v_max_f32_e32 v204, 0, v160
	v_max_f32_e32 v208, 0, v161
	v_fma_f32 v201, v144, v204, 0
	v_max_f32_e32 v204, 0, v162
	v_fmac_f32_e32 v201, v145, v208
	v_max_f32_e32 v208, 0, v163
	v_fmac_f32_e32 v201, v146, v204
	v_max_f32_e32 v204, 0, v164
	v_fmac_f32_e32 v201, v147, v208
	v_max_f32_e32 v208, 0, v165
	v_fmac_f32_e32 v201, v148, v204
	v_max_f32_e32 v204, 0, v166
	v_fmac_f32_e32 v201, v149, v208
	v_max_f32_e32 v208, 0, v167
	v_fmac_f32_e32 v201, v150, v204
	v_max_f32_e32 v204, 0, v168
	v_fmac_f32_e32 v201, v151, v208
	v_max_f32_e32 v208, 0, v169
	v_fmac_f32_e32 v201, v152, v204
	v_max_f32_e32 v204, 0, v170
	v_fmac_f32_e32 v201, v153, v208
	v_max_f32_e32 v208, 0, v171
	v_fmac_f32_e32 v201, v154, v204
	v_max_f32_e32 v204, 0, v172
	v_fmac_f32_e32 v201, v155, v208
	v_max_f32_e32 v208, 0, v173
	v_fmac_f32_e32 v201, v156, v204
	v_max_f32_e32 v204, 0, v174
	v_fmac_f32_e32 v201, v157, v208
	v_max_f32_e32 v208, 0, v175
	v_fmac_f32_e32 v201, v158, v204
	v_fmac_f32_e32 v201, v159, v208
	v_cndmask_b32_e32 v201, v61, v201, vcc
	v_ashrrev_i32_e32 v207, 31, v201
	v_or_b32_e32 v207, 0x80000000, v207
	v_xor_b32_e32 v108, v201, v207
	s_branch .Lidx_ce5
.Lidx_x46:
	s_nop 15
	v_cmp_le_i32_e32 vcc, 0x5a0, v59
	v_max_f32_e32 v204, 0, v176
	v_max_f32_e32 v208, 0, v177
	v_fma_f32 v201, v144, v204, 0
	v_max_f32_e32 v204, 0, v178
	v_fmac_f32_e32 v201, v145, v208
	v_max_f32_e32 v208, 0, v179
	v_fmac_f32_e32 v201, v146, v204
	v_max_f32_e32 v204, 0, v180
	v_fmac_f32_e32 v201, v147, v208
	v_max_f32_e32 v208, 0, v181
	v_fmac_f32_e32 v201, v148, v204
	v_max_f32_e32 v204, 0, v182
	v_fmac_f32_e32 v201, v149, v208
	v_max_f32_e32 v208, 0, v183
	v_fmac_f32_e32 v201, v150, v204
	v_max_f32_e32 v204, 0, v184
	v_fmac_f32_e32 v201, v151, v208
	v_max_f32_e32 v208, 0, v185
	v_fmac_f32_e32 v201, v152, v204
	v_max_f32_e32 v204, 0, v186
	v_fmac_f32_e32 v201, v153, v208
	v_max_f32_e32 v208, 0, v187
	v_fmac_f32_e32 v201, v154, v204
	v_max_f32_e32 v204, 0, v188
	v_fmac_f32_e32 v201, v155, v208
	v_max_f32_e32 v208, 0, v189
	v_fmac_f32_e32 v201, v156, v204
	v_max_f32_e32 v204, 0, v190
	v_fmac_f32_e32 v201, v157, v208
	v_max_f32_e32 v208, 0, v191
	v_fmac_f32_e32 v201, v158, v204
	v_fmac_f32_e32 v201, v159, v208
	v_cndmask_b32_e32 v201, v61, v201, vcc
	v_ashrrev_i32_e32 v207, 31, v201
	v_or_b32_e32 v207, 0x80000000, v207
	v_xor_b32_e32 v109, v201, v207
	s_branch .Lidx_ce5
.Lidx_x47:
	s_nop 15
	v_cmp_le_i32_e32 vcc, 0x5c0, v59
	v_max_f32_e32 v204, 0, v160
	v_max_f32_e32 v208, 0, v161
	v_fma_f32 v201, v144, v204, 0
	v_max_f32_e32 v204, 0, v162
	v_fmac_f32_e32 v201, v145, v208
	v_max_f32_e32 v208, 0, v163
	v_fmac_f32_e32 v201, v146, v204
	v_max_f32_e32 v204, 0, v164
	v_fmac_f32_e32 v201, v147, v208
	v_max_f32_e32 v208, 0, v165
	v_fmac_f32_e32 v201, v148, v204
	v_max_f32_e32 v204, 0, v166
	v_fmac_f32_e32 v201, v149, v208
	v_max_f32_e32 v208, 0, v167
	v_fmac_f32_e32 v201, v150, v204
	v_max_f32_e32 v204, 0, v168
	v_fmac_f32_e32 v201, v151, v208
	v_max_f32_e32 v208, 0, v169
	v_fmac_f32_e32 v201, v152, v204
	v_max_f32_e32 v204, 0, v170
	v_fmac_f32_e32 v201, v153, v208
	v_max_f32_e32 v208, 0, v171
	v_fmac_f32_e32 v201, v154, v204
	v_max_f32_e32 v204, 0, v172
	v_fmac_f32_e32 v201, v155, v208
	v_max_f32_e32 v208, 0, v173
	v_fmac_f32_e32 v201, v156, v204
	v_max_f32_e32 v204, 0, v174
	v_fmac_f32_e32 v201, v157, v208
	v_max_f32_e32 v208, 0, v175
	v_fmac_f32_e32 v201, v158, v204
	v_fmac_f32_e32 v201, v159, v208
	v_cndmask_b32_e32 v201, v61, v201, vcc
	v_ashrrev_i32_e32 v207, 31, v201
	v_or_b32_e32 v207, 0x80000000, v207
	v_xor_b32_e32 v110, v201, v207
	s_branch .Lidx_ce5
.Lidx_x48:
	s_nop 15
	v_cmp_le_i32_e32 vcc, 0x5e0, v59
	v_max_f32_e32 v204, 0, v176
	v_max_f32_e32 v208, 0, v177
	v_fma_f32 v201, v144, v204, 0
	v_max_f32_e32 v204, 0, v178
	v_fmac_f32_e32 v201, v145, v208
	v_max_f32_e32 v208, 0, v179
	v_fmac_f32_e32 v201, v146, v204
	v_max_f32_e32 v204, 0, v180
	v_fmac_f32_e32 v201, v147, v208
	v_max_f32_e32 v208, 0, v181
	v_fmac_f32_e32 v201, v148, v204
	v_max_f32_e32 v204, 0, v182
	v_fmac_f32_e32 v201, v149, v208
	v_max_f32_e32 v208, 0, v183
	v_fmac_f32_e32 v201, v150, v204
	v_max_f32_e32 v204, 0, v184
	v_fmac_f32_e32 v201, v151, v208
	v_max_f32_e32 v208, 0, v185
	v_fmac_f32_e32 v201, v152, v204
	v_max_f32_e32 v204, 0, v186
	v_fmac_f32_e32 v201, v153, v208
	v_max_f32_e32 v208, 0, v187
	v_fmac_f32_e32 v201, v154, v204
	v_max_f32_e32 v204, 0, v188
	v_fmac_f32_e32 v201, v155, v208
	v_max_f32_e32 v208, 0, v189
	v_fmac_f32_e32 v201, v156, v204
	v_max_f32_e32 v204, 0, v190
	v_fmac_f32_e32 v201, v157, v208
	v_max_f32_e32 v208, 0, v191
	v_fmac_f32_e32 v201, v158, v204
	v_fmac_f32_e32 v201, v159, v208
	v_cndmask_b32_e32 v201, v61, v201, vcc
	v_ashrrev_i32_e32 v207, 31, v201
	v_or_b32_e32 v207, 0x80000000, v207
	v_xor_b32_e32 v111, v201, v207
	s_branch .Lidx_ce6
.Lidx_x49:
	s_nop 15
	v_cmp_le_i32_e32 vcc, 0x600, v59
	v_max_f32_e32 v204, 0, v160
	v_max_f32_e32 v208, 0, v161
	v_fma_f32 v201, v144, v204, 0
	v_max_f32_e32 v204, 0, v162
	v_fmac_f32_e32 v201, v145, v208
	v_max_f32_e32 v208, 0, v163
	v_fmac_f32_e32 v201, v146, v204
	v_max_f32_e32 v204, 0, v164
	v_fmac_f32_e32 v201, v147, v208
	v_max_f32_e32 v208, 0, v165
	v_fmac_f32_e32 v201, v148, v204
	v_max_f32_e32 v204, 0, v166
	v_fmac_f32_e32 v201, v149, v208
	v_max_f32_e32 v208, 0, v167
	v_fmac_f32_e32 v201, v150, v204
	v_max_f32_e32 v204, 0, v168
	v_fmac_f32_e32 v201, v151, v208
	v_max_f32_e32 v208, 0, v169
	v_fmac_f32_e32 v201, v152, v204
	v_max_f32_e32 v204, 0, v170
	v_fmac_f32_e32 v201, v153, v208
	v_max_f32_e32 v208, 0, v171
	v_fmac_f32_e32 v201, v154, v204
	v_max_f32_e32 v204, 0, v172
	v_fmac_f32_e32 v201, v155, v208
	v_max_f32_e32 v208, 0, v173
	v_fmac_f32_e32 v201, v156, v204
	v_max_f32_e32 v204, 0, v174
	v_fmac_f32_e32 v201, v157, v208
	v_max_f32_e32 v208, 0, v175
	v_fmac_f32_e32 v201, v158, v204
	v_fmac_f32_e32 v201, v159, v208
	v_cndmask_b32_e32 v201, v61, v201, vcc
	v_ashrrev_i32_e32 v207, 31, v201
	v_or_b32_e32 v207, 0x80000000, v207
	v_xor_b32_e32 v112, v201, v207
	s_branch .Lidx_ce6
.Lidx_x50:
	s_nop 15
	v_cmp_le_i32_e32 vcc, 0x620, v59
	v_max_f32_e32 v204, 0, v176
	v_max_f32_e32 v208, 0, v177
	v_fma_f32 v201, v144, v204, 0
	v_max_f32_e32 v204, 0, v178
	v_fmac_f32_e32 v201, v145, v208
	v_max_f32_e32 v208, 0, v179
	v_fmac_f32_e32 v201, v146, v204
	v_max_f32_e32 v204, 0, v180
	v_fmac_f32_e32 v201, v147, v208
	v_max_f32_e32 v208, 0, v181
	v_fmac_f32_e32 v201, v148, v204
	v_max_f32_e32 v204, 0, v182
	v_fmac_f32_e32 v201, v149, v208
	v_max_f32_e32 v208, 0, v183
	v_fmac_f32_e32 v201, v150, v204
	v_max_f32_e32 v204, 0, v184
	v_fmac_f32_e32 v201, v151, v208
	v_max_f32_e32 v208, 0, v185
	v_fmac_f32_e32 v201, v152, v204
	v_max_f32_e32 v204, 0, v186
	v_fmac_f32_e32 v201, v153, v208
	v_max_f32_e32 v208, 0, v187
	v_fmac_f32_e32 v201, v154, v204
	v_max_f32_e32 v204, 0, v188
	v_fmac_f32_e32 v201, v155, v208
	v_max_f32_e32 v208, 0, v189
	v_fmac_f32_e32 v201, v156, v204
	v_max_f32_e32 v204, 0, v190
	v_fmac_f32_e32 v201, v157, v208
	v_max_f32_e32 v208, 0, v191
	v_fmac_f32_e32 v201, v158, v204
	v_fmac_f32_e32 v201, v159, v208
	v_cndmask_b32_e32 v201, v61, v201, vcc
	v_ashrrev_i32_e32 v207, 31, v201
	v_or_b32_e32 v207, 0x80000000, v207
	v_xor_b32_e32 v113, v201, v207
	s_branch .Lidx_ce6
.Lidx_x51:
	s_nop 15
	v_cmp_le_i32_e32 vcc, 0x640, v59
	v_max_f32_e32 v204, 0, v160
	v_max_f32_e32 v208, 0, v161
	v_fma_f32 v201, v144, v204, 0
	v_max_f32_e32 v204, 0, v162
	v_fmac_f32_e32 v201, v145, v208
	v_max_f32_e32 v208, 0, v163
	v_fmac_f32_e32 v201, v146, v204
	v_max_f32_e32 v204, 0, v164
	v_fmac_f32_e32 v201, v147, v208
	v_max_f32_e32 v208, 0, v165
	v_fmac_f32_e32 v201, v148, v204
	v_max_f32_e32 v204, 0, v166
	v_fmac_f32_e32 v201, v149, v208
	v_max_f32_e32 v208, 0, v167
	v_fmac_f32_e32 v201, v150, v204
	v_max_f32_e32 v204, 0, v168
	v_fmac_f32_e32 v201, v151, v208
	v_max_f32_e32 v208, 0, v169
	v_fmac_f32_e32 v201, v152, v204
	v_max_f32_e32 v204, 0, v170
	v_fmac_f32_e32 v201, v153, v208
	v_max_f32_e32 v208, 0, v171
	v_fmac_f32_e32 v201, v154, v204
	v_max_f32_e32 v204, 0, v172
	v_fmac_f32_e32 v201, v155, v208
	v_max_f32_e32 v208, 0, v173
	v_fmac_f32_e32 v201, v156, v204
	v_max_f32_e32 v204, 0, v174
	v_fmac_f32_e32 v201, v157, v208
	v_max_f32_e32 v208, 0, v175
	v_fmac_f32_e32 v201, v158, v204
	v_fmac_f32_e32 v201, v159, v208
	v_cndmask_b32_e32 v201, v61, v201, vcc
	v_ashrrev_i32_e32 v207, 31, v201
	v_or_b32_e32 v207, 0x80000000, v207
	v_xor_b32_e32 v114, v201, v207
	s_branch .Lidx_ce6
.Lidx_x52:
	s_nop 15
	v_cmp_le_i32_e32 vcc, 0x660, v59
	v_max_f32_e32 v204, 0, v176
	v_max_f32_e32 v208, 0, v177
	v_fma_f32 v201, v144, v204, 0
	v_max_f32_e32 v204, 0, v178
	v_fmac_f32_e32 v201, v145, v208
	v_max_f32_e32 v208, 0, v179
	v_fmac_f32_e32 v201, v146, v204
	v_max_f32_e32 v204, 0, v180
	v_fmac_f32_e32 v201, v147, v208
	v_max_f32_e32 v208, 0, v181
	v_fmac_f32_e32 v201, v148, v204
	v_max_f32_e32 v204, 0, v182
	v_fmac_f32_e32 v201, v149, v208
	v_max_f32_e32 v208, 0, v183
	v_fmac_f32_e32 v201, v150, v204
	v_max_f32_e32 v204, 0, v184
	v_fmac_f32_e32 v201, v151, v208
	v_max_f32_e32 v208, 0, v185
	v_fmac_f32_e32 v201, v152, v204
	v_max_f32_e32 v204, 0, v186
	v_fmac_f32_e32 v201, v153, v208
	v_max_f32_e32 v208, 0, v187
	v_fmac_f32_e32 v201, v154, v204
	v_max_f32_e32 v204, 0, v188
	v_fmac_f32_e32 v201, v155, v208
	v_max_f32_e32 v208, 0, v189
	v_fmac_f32_e32 v201, v156, v204
	v_max_f32_e32 v204, 0, v190
	v_fmac_f32_e32 v201, v157, v208
	v_max_f32_e32 v208, 0, v191
	v_fmac_f32_e32 v201, v158, v204
	v_fmac_f32_e32 v201, v159, v208
	v_cndmask_b32_e32 v201, v61, v201, vcc
	v_ashrrev_i32_e32 v207, 31, v201
	v_or_b32_e32 v207, 0x80000000, v207
	v_xor_b32_e32 v115, v201, v207
	s_branch .Lidx_ce6
.Lidx_x53:
	s_nop 15
	v_cmp_le_i32_e32 vcc, 0x680, v59
	v_max_f32_e32 v204, 0, v160
	v_max_f32_e32 v208, 0, v161
	v_fma_f32 v201, v144, v204, 0
	v_max_f32_e32 v204, 0, v162
	v_fmac_f32_e32 v201, v145, v208
	v_max_f32_e32 v208, 0, v163
	v_fmac_f32_e32 v201, v146, v204
	v_max_f32_e32 v204, 0, v164
	v_fmac_f32_e32 v201, v147, v208
	v_max_f32_e32 v208, 0, v165
	v_fmac_f32_e32 v201, v148, v204
	v_max_f32_e32 v204, 0, v166
	v_fmac_f32_e32 v201, v149, v208
	v_max_f32_e32 v208, 0, v167
	v_fmac_f32_e32 v201, v150, v204
	v_max_f32_e32 v204, 0, v168
	v_fmac_f32_e32 v201, v151, v208
	v_max_f32_e32 v208, 0, v169
	v_fmac_f32_e32 v201, v152, v204
	v_max_f32_e32 v204, 0, v170
	v_fmac_f32_e32 v201, v153, v208
	v_max_f32_e32 v208, 0, v171
	v_fmac_f32_e32 v201, v154, v204
	v_max_f32_e32 v204, 0, v172
	v_fmac_f32_e32 v201, v155, v208
	v_max_f32_e32 v208, 0, v173
	v_fmac_f32_e32 v201, v156, v204
	v_max_f32_e32 v204, 0, v174
	v_fmac_f32_e32 v201, v157, v208
	v_max_f32_e32 v208, 0, v175
	v_fmac_f32_e32 v201, v158, v204
	v_fmac_f32_e32 v201, v159, v208
	v_cndmask_b32_e32 v201, v61, v201, vcc
	v_ashrrev_i32_e32 v207, 31, v201
	v_or_b32_e32 v207, 0x80000000, v207
	v_xor_b32_e32 v116, v201, v207
	s_branch .Lidx_ce6
.Lidx_x54:
	s_nop 15
	v_cmp_le_i32_e32 vcc, 0x6a0, v59
	v_max_f32_e32 v204, 0, v176
	v_max_f32_e32 v208, 0, v177
	v_fma_f32 v201, v144, v204, 0
	v_max_f32_e32 v204, 0, v178
	v_fmac_f32_e32 v201, v145, v208
	v_max_f32_e32 v208, 0, v179
	v_fmac_f32_e32 v201, v146, v204
	v_max_f32_e32 v204, 0, v180
	v_fmac_f32_e32 v201, v147, v208
	v_max_f32_e32 v208, 0, v181
	v_fmac_f32_e32 v201, v148, v204
	v_max_f32_e32 v204, 0, v182
	v_fmac_f32_e32 v201, v149, v208
	v_max_f32_e32 v208, 0, v183
	v_fmac_f32_e32 v201, v150, v204
	v_max_f32_e32 v204, 0, v184
	v_fmac_f32_e32 v201, v151, v208
	v_max_f32_e32 v208, 0, v185
	v_fmac_f32_e32 v201, v152, v204
	v_max_f32_e32 v204, 0, v186
	v_fmac_f32_e32 v201, v153, v208
	v_max_f32_e32 v208, 0, v187
	v_fmac_f32_e32 v201, v154, v204
	v_max_f32_e32 v204, 0, v188
	v_fmac_f32_e32 v201, v155, v208
	v_max_f32_e32 v208, 0, v189
	v_fmac_f32_e32 v201, v156, v204
	v_max_f32_e32 v204, 0, v190
	v_fmac_f32_e32 v201, v157, v208
	v_max_f32_e32 v208, 0, v191
	v_fmac_f32_e32 v201, v158, v204
	v_fmac_f32_e32 v201, v159, v208
	v_cndmask_b32_e32 v201, v61, v201, vcc
	v_ashrrev_i32_e32 v207, 31, v201
	v_or_b32_e32 v207, 0x80000000, v207
	v_xor_b32_e32 v117, v201, v207
	s_branch .Lidx_ce6
.Lidx_x55:
	s_nop 15
	v_cmp_le_i32_e32 vcc, 0x6c0, v59
	v_max_f32_e32 v204, 0, v160
	v_max_f32_e32 v208, 0, v161
	v_fma_f32 v201, v144, v204, 0
	v_max_f32_e32 v204, 0, v162
	v_fmac_f32_e32 v201, v145, v208
	v_max_f32_e32 v208, 0, v163
	v_fmac_f32_e32 v201, v146, v204
	v_max_f32_e32 v204, 0, v164
	v_fmac_f32_e32 v201, v147, v208
	v_max_f32_e32 v208, 0, v165
	v_fmac_f32_e32 v201, v148, v204
	v_max_f32_e32 v204, 0, v166
	v_fmac_f32_e32 v201, v149, v208
	v_max_f32_e32 v208, 0, v167
	v_fmac_f32_e32 v201, v150, v204
	v_max_f32_e32 v204, 0, v168
	v_fmac_f32_e32 v201, v151, v208
	v_max_f32_e32 v208, 0, v169
	v_fmac_f32_e32 v201, v152, v204
	v_max_f32_e32 v204, 0, v170
	v_fmac_f32_e32 v201, v153, v208
	v_max_f32_e32 v208, 0, v171
	v_fmac_f32_e32 v201, v154, v204
	v_max_f32_e32 v204, 0, v172
	v_fmac_f32_e32 v201, v155, v208
	v_max_f32_e32 v208, 0, v173
	v_fmac_f32_e32 v201, v156, v204
	v_max_f32_e32 v204, 0, v174
	v_fmac_f32_e32 v201, v157, v208
	v_max_f32_e32 v208, 0, v175
	v_fmac_f32_e32 v201, v158, v204
	v_fmac_f32_e32 v201, v159, v208
	v_cndmask_b32_e32 v201, v61, v201, vcc
	v_ashrrev_i32_e32 v207, 31, v201
	v_or_b32_e32 v207, 0x80000000, v207
	v_xor_b32_e32 v118, v201, v207
	s_branch .Lidx_ce6
.Lidx_x56:
	s_nop 15
	v_cmp_le_i32_e32 vcc, 0x6e0, v59
	v_max_f32_e32 v204, 0, v176
	v_max_f32_e32 v208, 0, v177
	v_fma_f32 v201, v144, v204, 0
	v_max_f32_e32 v204, 0, v178
	v_fmac_f32_e32 v201, v145, v208
	v_max_f32_e32 v208, 0, v179
	v_fmac_f32_e32 v201, v146, v204
	v_max_f32_e32 v204, 0, v180
	v_fmac_f32_e32 v201, v147, v208
	v_max_f32_e32 v208, 0, v181
	v_fmac_f32_e32 v201, v148, v204
	v_max_f32_e32 v204, 0, v182
	v_fmac_f32_e32 v201, v149, v208
	v_max_f32_e32 v208, 0, v183
	v_fmac_f32_e32 v201, v150, v204
	v_max_f32_e32 v204, 0, v184
	v_fmac_f32_e32 v201, v151, v208
	v_max_f32_e32 v208, 0, v185
	v_fmac_f32_e32 v201, v152, v204
	v_max_f32_e32 v204, 0, v186
	v_fmac_f32_e32 v201, v153, v208
	v_max_f32_e32 v208, 0, v187
	v_fmac_f32_e32 v201, v154, v204
	v_max_f32_e32 v204, 0, v188
	v_fmac_f32_e32 v201, v155, v208
	v_max_f32_e32 v208, 0, v189
	v_fmac_f32_e32 v201, v156, v204
	v_max_f32_e32 v204, 0, v190
	v_fmac_f32_e32 v201, v157, v208
	v_max_f32_e32 v208, 0, v191
	v_fmac_f32_e32 v201, v158, v204
	v_fmac_f32_e32 v201, v159, v208
	v_cndmask_b32_e32 v201, v61, v201, vcc
	v_ashrrev_i32_e32 v207, 31, v201
	v_or_b32_e32 v207, 0x80000000, v207
	v_xor_b32_e32 v119, v201, v207
	s_branch .Lidx_ce7
.Lidx_x57:
	s_nop 15
	v_cmp_le_i32_e32 vcc, 0x700, v59
	v_max_f32_e32 v204, 0, v160
	v_max_f32_e32 v208, 0, v161
	v_fma_f32 v201, v144, v204, 0
	v_max_f32_e32 v204, 0, v162
	v_fmac_f32_e32 v201, v145, v208
	v_max_f32_e32 v208, 0, v163
	v_fmac_f32_e32 v201, v146, v204
	v_max_f32_e32 v204, 0, v164
	v_fmac_f32_e32 v201, v147, v208
	v_max_f32_e32 v208, 0, v165
	v_fmac_f32_e32 v201, v148, v204
	v_max_f32_e32 v204, 0, v166
	v_fmac_f32_e32 v201, v149, v208
	v_max_f32_e32 v208, 0, v167
	v_fmac_f32_e32 v201, v150, v204
	v_max_f32_e32 v204, 0, v168
	v_fmac_f32_e32 v201, v151, v208
	v_max_f32_e32 v208, 0, v169
	v_fmac_f32_e32 v201, v152, v204
	v_max_f32_e32 v204, 0, v170
	v_fmac_f32_e32 v201, v153, v208
	v_max_f32_e32 v208, 0, v171
	v_fmac_f32_e32 v201, v154, v204
	v_max_f32_e32 v204, 0, v172
	v_fmac_f32_e32 v201, v155, v208
	v_max_f32_e32 v208, 0, v173
	v_fmac_f32_e32 v201, v156, v204
	v_max_f32_e32 v204, 0, v174
	v_fmac_f32_e32 v201, v157, v208
	v_max_f32_e32 v208, 0, v175
	v_fmac_f32_e32 v201, v158, v204
	v_fmac_f32_e32 v201, v159, v208
	v_cndmask_b32_e32 v201, v61, v201, vcc
	v_ashrrev_i32_e32 v207, 31, v201
	v_or_b32_e32 v207, 0x80000000, v207
	v_xor_b32_e32 v120, v201, v207
	s_branch .Lidx_ce7
.Lidx_x58:
	s_nop 15
	v_cmp_le_i32_e32 vcc, 0x720, v59
	v_max_f32_e32 v204, 0, v176
	v_max_f32_e32 v208, 0, v177
	v_fma_f32 v201, v144, v204, 0
	v_max_f32_e32 v204, 0, v178
	v_fmac_f32_e32 v201, v145, v208
	v_max_f32_e32 v208, 0, v179
	v_fmac_f32_e32 v201, v146, v204
	v_max_f32_e32 v204, 0, v180
	v_fmac_f32_e32 v201, v147, v208
	v_max_f32_e32 v208, 0, v181
	v_fmac_f32_e32 v201, v148, v204
	v_max_f32_e32 v204, 0, v182
	v_fmac_f32_e32 v201, v149, v208
	v_max_f32_e32 v208, 0, v183
	v_fmac_f32_e32 v201, v150, v204
	v_max_f32_e32 v204, 0, v184
	v_fmac_f32_e32 v201, v151, v208
	v_max_f32_e32 v208, 0, v185
	v_fmac_f32_e32 v201, v152, v204
	v_max_f32_e32 v204, 0, v186
	v_fmac_f32_e32 v201, v153, v208
	v_max_f32_e32 v208, 0, v187
	v_fmac_f32_e32 v201, v154, v204
	v_max_f32_e32 v204, 0, v188
	v_fmac_f32_e32 v201, v155, v208
	v_max_f32_e32 v208, 0, v189
	v_fmac_f32_e32 v201, v156, v204
	v_max_f32_e32 v204, 0, v190
	v_fmac_f32_e32 v201, v157, v208
	v_max_f32_e32 v208, 0, v191
	v_fmac_f32_e32 v201, v158, v204
	v_fmac_f32_e32 v201, v159, v208
	v_cndmask_b32_e32 v201, v61, v201, vcc
	v_ashrrev_i32_e32 v207, 31, v201
	v_or_b32_e32 v207, 0x80000000, v207
	v_xor_b32_e32 v121, v201, v207
	s_branch .Lidx_ce7
.Lidx_x59:
	s_nop 15
	v_cmp_le_i32_e32 vcc, 0x740, v59
	v_max_f32_e32 v204, 0, v160
	v_max_f32_e32 v208, 0, v161
	v_fma_f32 v201, v144, v204, 0
	v_max_f32_e32 v204, 0, v162
	v_fmac_f32_e32 v201, v145, v208
	v_max_f32_e32 v208, 0, v163
	v_fmac_f32_e32 v201, v146, v204
	v_max_f32_e32 v204, 0, v164
	v_fmac_f32_e32 v201, v147, v208
	v_max_f32_e32 v208, 0, v165
	v_fmac_f32_e32 v201, v148, v204
	v_max_f32_e32 v204, 0, v166
	v_fmac_f32_e32 v201, v149, v208
	v_max_f32_e32 v208, 0, v167
	v_fmac_f32_e32 v201, v150, v204
	v_max_f32_e32 v204, 0, v168
	v_fmac_f32_e32 v201, v151, v208
	v_max_f32_e32 v208, 0, v169
	v_fmac_f32_e32 v201, v152, v204
	v_max_f32_e32 v204, 0, v170
	v_fmac_f32_e32 v201, v153, v208
	v_max_f32_e32 v208, 0, v171
	v_fmac_f32_e32 v201, v154, v204
	v_max_f32_e32 v204, 0, v172
	v_fmac_f32_e32 v201, v155, v208
	v_max_f32_e32 v208, 0, v173
	v_fmac_f32_e32 v201, v156, v204
	v_max_f32_e32 v204, 0, v174
	v_fmac_f32_e32 v201, v157, v208
	v_max_f32_e32 v208, 0, v175
	v_fmac_f32_e32 v201, v158, v204
	v_fmac_f32_e32 v201, v159, v208
	v_cndmask_b32_e32 v201, v61, v201, vcc
	v_ashrrev_i32_e32 v207, 31, v201
	v_or_b32_e32 v207, 0x80000000, v207
	v_xor_b32_e32 v122, v201, v207
	s_branch .Lidx_ce7
.Lidx_x60:
	s_nop 15
	v_cmp_le_i32_e32 vcc, 0x760, v59
	v_max_f32_e32 v204, 0, v176
	v_max_f32_e32 v208, 0, v177
	v_fma_f32 v201, v144, v204, 0
	v_max_f32_e32 v204, 0, v178
	v_fmac_f32_e32 v201, v145, v208
	v_max_f32_e32 v208, 0, v179
	v_fmac_f32_e32 v201, v146, v204
	v_max_f32_e32 v204, 0, v180
	v_fmac_f32_e32 v201, v147, v208
	v_max_f32_e32 v208, 0, v181
	v_fmac_f32_e32 v201, v148, v204
	v_max_f32_e32 v204, 0, v182
	v_fmac_f32_e32 v201, v149, v208
	v_max_f32_e32 v208, 0, v183
	v_fmac_f32_e32 v201, v150, v204
	v_max_f32_e32 v204, 0, v184
	v_fmac_f32_e32 v201, v151, v208
	v_max_f32_e32 v208, 0, v185
	v_fmac_f32_e32 v201, v152, v204
	v_max_f32_e32 v204, 0, v186
	v_fmac_f32_e32 v201, v153, v208
	v_max_f32_e32 v208, 0, v187
	v_fmac_f32_e32 v201, v154, v204
	v_max_f32_e32 v204, 0, v188
	v_fmac_f32_e32 v201, v155, v208
	v_max_f32_e32 v208, 0, v189
	v_fmac_f32_e32 v201, v156, v204
	v_max_f32_e32 v204, 0, v190
	v_fmac_f32_e32 v201, v157, v208
	v_max_f32_e32 v208, 0, v191
	v_fmac_f32_e32 v201, v158, v204
	v_fmac_f32_e32 v201, v159, v208
	v_cndmask_b32_e32 v201, v61, v201, vcc
	v_ashrrev_i32_e32 v207, 31, v201
	v_or_b32_e32 v207, 0x80000000, v207
	v_xor_b32_e32 v123, v201, v207
	s_branch .Lidx_ce7
.Lidx_x61:
	s_nop 15
	v_cmp_le_i32_e32 vcc, 0x780, v59
	v_max_f32_e32 v204, 0, v160
	v_max_f32_e32 v208, 0, v161
	v_fma_f32 v201, v144, v204, 0
	v_max_f32_e32 v204, 0, v162
	v_fmac_f32_e32 v201, v145, v208
	v_max_f32_e32 v208, 0, v163
	v_fmac_f32_e32 v201, v146, v204
	v_max_f32_e32 v204, 0, v164
	v_fmac_f32_e32 v201, v147, v208
	v_max_f32_e32 v208, 0, v165
	v_fmac_f32_e32 v201, v148, v204
	v_max_f32_e32 v204, 0, v166
	v_fmac_f32_e32 v201, v149, v208
	v_max_f32_e32 v208, 0, v167
	v_fmac_f32_e32 v201, v150, v204
	v_max_f32_e32 v204, 0, v168
	v_fmac_f32_e32 v201, v151, v208
	v_max_f32_e32 v208, 0, v169
	v_fmac_f32_e32 v201, v152, v204
	v_max_f32_e32 v204, 0, v170
	v_fmac_f32_e32 v201, v153, v208
	v_max_f32_e32 v208, 0, v171
	v_fmac_f32_e32 v201, v154, v204
	v_max_f32_e32 v204, 0, v172
	v_fmac_f32_e32 v201, v155, v208
	v_max_f32_e32 v208, 0, v173
	v_fmac_f32_e32 v201, v156, v204
	v_max_f32_e32 v204, 0, v174
	v_fmac_f32_e32 v201, v157, v208
	v_max_f32_e32 v208, 0, v175
	v_fmac_f32_e32 v201, v158, v204
	v_fmac_f32_e32 v201, v159, v208
	v_cndmask_b32_e32 v201, v61, v201, vcc
	v_ashrrev_i32_e32 v207, 31, v201
	v_or_b32_e32 v207, 0x80000000, v207
	v_xor_b32_e32 v124, v201, v207
	s_branch .Lidx_ce7
.Lidx_x62:
	s_nop 15
	v_cmp_le_i32_e32 vcc, 0x7a0, v59
	v_max_f32_e32 v204, 0, v176
	v_max_f32_e32 v208, 0, v177
	v_fma_f32 v201, v144, v204, 0
	v_max_f32_e32 v204, 0, v178
	v_fmac_f32_e32 v201, v145, v208
	v_max_f32_e32 v208, 0, v179
	v_fmac_f32_e32 v201, v146, v204
	v_max_f32_e32 v204, 0, v180
	v_fmac_f32_e32 v201, v147, v208
	v_max_f32_e32 v208, 0, v181
	v_fmac_f32_e32 v201, v148, v204
	v_max_f32_e32 v204, 0, v182
	v_fmac_f32_e32 v201, v149, v208
	v_max_f32_e32 v208, 0, v183
	v_fmac_f32_e32 v201, v150, v204
	v_max_f32_e32 v204, 0, v184
	v_fmac_f32_e32 v201, v151, v208
	v_max_f32_e32 v208, 0, v185
	v_fmac_f32_e32 v201, v152, v204
	v_max_f32_e32 v204, 0, v186
	v_fmac_f32_e32 v201, v153, v208
	v_max_f32_e32 v208, 0, v187
	v_fmac_f32_e32 v201, v154, v204
	v_max_f32_e32 v204, 0, v188
	v_fmac_f32_e32 v201, v155, v208
	v_max_f32_e32 v208, 0, v189
	v_fmac_f32_e32 v201, v156, v204
	v_max_f32_e32 v204, 0, v190
	v_fmac_f32_e32 v201, v157, v208
	v_max_f32_e32 v208, 0, v191
	v_fmac_f32_e32 v201, v158, v204
	v_fmac_f32_e32 v201, v159, v208
	v_cndmask_b32_e32 v201, v61, v201, vcc
	v_ashrrev_i32_e32 v207, 31, v201
	v_or_b32_e32 v207, 0x80000000, v207
	v_xor_b32_e32 v125, v201, v207
	s_branch .Lidx_ce7
.Lidx_x63:
	s_nop 15
	v_cmp_le_i32_e32 vcc, 0x7c0, v59
	v_max_f32_e32 v204, 0, v160
	v_max_f32_e32 v208, 0, v161
	v_fma_f32 v201, v144, v204, 0
	v_max_f32_e32 v204, 0, v162
	v_fmac_f32_e32 v201, v145, v208
	v_max_f32_e32 v208, 0, v163
	v_fmac_f32_e32 v201, v146, v204
	v_max_f32_e32 v204, 0, v164
	v_fmac_f32_e32 v201, v147, v208
	v_max_f32_e32 v208, 0, v165
	v_fmac_f32_e32 v201, v148, v204
	v_max_f32_e32 v204, 0, v166
	v_fmac_f32_e32 v201, v149, v208
	v_max_f32_e32 v208, 0, v167
	v_fmac_f32_e32 v201, v150, v204
	v_max_f32_e32 v204, 0, v168
	v_fmac_f32_e32 v201, v151, v208
	v_max_f32_e32 v208, 0, v169
	v_fmac_f32_e32 v201, v152, v204
	v_max_f32_e32 v204, 0, v170
	v_fmac_f32_e32 v201, v153, v208
	v_max_f32_e32 v208, 0, v171
	v_fmac_f32_e32 v201, v154, v204
	v_max_f32_e32 v204, 0, v172
	v_fmac_f32_e32 v201, v155, v208
	v_max_f32_e32 v208, 0, v173
	v_fmac_f32_e32 v201, v156, v204
	v_max_f32_e32 v204, 0, v174
	v_fmac_f32_e32 v201, v157, v208
	v_max_f32_e32 v208, 0, v175
	v_fmac_f32_e32 v201, v158, v204
	v_fmac_f32_e32 v201, v159, v208
	v_cndmask_b32_e32 v201, v61, v201, vcc
	v_ashrrev_i32_e32 v207, 31, v201
	v_or_b32_e32 v207, 0x80000000, v207
	v_xor_b32_e32 v126, v201, v207
	s_branch .Lidx_ce7
.Lidx_search:
	s_waitcnt vmcnt(0) lgkmcnt(0)
	v_mov_b32_e32 v62, 0
	s_mov_b32 s24, 0x80000000
